# GEMM main loops: static s_setprio 1 for the older wave half (waves 0-3) before the unit loop, per-phase priority flips removed; on top of scan/prep changes
# speedup vs baseline: 1.0122x; 1.0096x over previous
.LBB0_3:
	s_or_b64 exec, exec, s[8:9]
	s_waitcnt lgkmcnt(0)
	s_barrier
	s_load_dwordx2 s[0:1], s[6:7], 0x110
	v_cmp_eq_u32_e32 vcc, 0, v0
	s_waitcnt lgkmcnt(0)
	s_sub_i32 s0, s1, s0
	s_cmp_gt_i32 s0, 1
	s_cbranch_scc0 .LBB0_8
	s_setprio 0
	s_getreg_b32 s0, hwreg(HW_REG_XCC_ID, 0, 4)
	s_and_saveexec_b64 s[6:7], vcc
	s_cbranch_execz .LBB0_7
	s_mov_b64 s[8:9], exec
	v_mbcnt_lo_u32_b32 v1, s8, 0
	v_mbcnt_hi_u32_b32 v1, s9, v1
	v_cmp_eq_u32_e32 vcc, 0, v1
	s_and_b64 s[2:3], exec, vcc
	s_mov_b64 exec, s[2:3]
	s_cbranch_execz .LBB0_7
	s_lshl_b32 s0, s0, 8
	s_and_b32 s0, s0, 0xf00
	s_add_u32 s0, s4, s0
	s_addc_u32 s1, s5, 0
	s_bcnt1_i32_b64 s2, s[8:9]
	v_mov_b32_e32 v1, 0x4000
	v_mov_b32_e32 v2, s2
	global_atomic_add v1, v2, s[0:1] offset:1024

.LBB0_318:
	s_mov_b64 s[0:1], s[4:5]
	s_load_dword s0, s[0:1], 0x110
	s_waitcnt lgkmcnt(0)
	s_cmp_gt_i32 s0, s41
	s_cbranch_scc1 .LBB0_376
	s_mov_b64 s[0:1], s[4:5]
	s_load_dword s0, s[0:1], 0x114
	s_waitcnt lgkmcnt(0)
	s_cmp_ge_i32 s41, s0
	s_cbranch_scc1 .LBB0_375
	v_readlane_b32 s0, v254, 2
	v_readlane_b32 s1, v254, 3
	s_load_dword s1, s[0:1], 0x110
	s_add_i32 s0, s41, 1
	s_waitcnt lgkmcnt(0)
	s_cmp_gt_i32 s1, s0
	s_cbranch_scc1 .LBB0_375
	v_readlane_b32 s2, v254, 2
	v_readlane_b32 s3, v254, 3
	s_load_dword s1, s[2:3], 0x114
	s_waitcnt lgkmcnt(0)
	s_cmp_ge_i32 s0, s1
	s_cbranch_scc1 .LBB0_375
	v_readlane_b32 s6, v254, 2
	v_mov_b32_e32 v1, v0
	v_readlane_b32 s7, v254, 3
	v_readlane_b32 s0, v254, 0
	s_load_dword s1, s[6:7], 0x118
	s_waitcnt lgkmcnt(0)
	s_setprio 0
	s_getreg_b32 s0, hwreg(HW_REG_XCC_ID, 0, 4)
	s_waitcnt vmcnt(0)
	s_barrier
	s_mov_b64 s[4:5], exec
	v_readlane_b32 s2, v254, 6
	v_readlane_b32 s3, v254, 7
	s_and_b64 s[2:3], s[4:5], s[2:3]
	s_mov_b64 exec, s[2:3]
	s_cbranch_execz .LBB0_374
	s_add_i32 s3, 0, 0x26000
	v_mov_b32_e32 v1, s3
	s_load_dwordx2 s[6:7], s[6:7], 0x108
	s_waitcnt vmcnt(0) expcnt(0) lgkmcnt(0)
	ds_read_b32 v3, v1
	v_readlane_b32 s1, v254, 8
	s_and_b32 s2, s0, 15
	s_waitcnt lgkmcnt(0)
	v_cmp_ne_u32_e32 vcc, 0, v3
	v_mov_b32_e32 v1, s1
	ds_read_b32 v2, v1
	s_cbranch_vccnz .LBB0_338
	v_readlane_b32 s8, v254, 4
	v_readlane_b32 s12, v254, 2
	v_readlane_b32 s9, v254, 5
	v_readlane_b32 s13, v254, 3
	s_load_dwordx2 s[0:1], s[8:9], 0x4
	s_nop 0
	s_load_dword s12, s[12:13], 0x118
	s_add_u32 s8, s6, 0x4200
	s_addc_u32 s9, s7, 0
	s_add_u32 s10, s6, 0x4400
	s_addc_u32 s11, s7, 0
	s_waitcnt lgkmcnt(0)
	s_mul_i32 s34, s0, s12
	s_add_u32 s12, s6, 0x4500
	s_addc_u32 s13, s7, 0
	s_add_u32 s14, s6, 0x4600
	s_addc_u32 s15, s7, 0
	s_add_u32 s16, s6, 0x4700
	s_addc_u32 s17, s7, 0
	s_add_u32 s18, s6, 0x4800
	s_addc_u32 s19, s7, 0
	s_add_u32 s20, s6, 0x4900
	s_addc_u32 s21, s7, 0
	s_add_u32 s22, s6, 0x4a00
	s_addc_u32 s23, s7, 0
	s_add_u32 s24, s6, 0x4b00
	s_addc_u32 s25, s7, 0
	s_add_u32 s26, s6, 0x4c00
	s_addc_u32 s27, s7, 0
	s_add_u32 s28, s6, 0x4d00
	s_addc_u32 s29, s7, 0
	s_add_u32 s30, s6, 0x4e00
	s_addc_u32 s31, s7, 0
	s_add_u32 s64, s6, 0x4f00
	s_addc_u32 s65, s7, 0
	s_add_u32 s66, s6, 0x5000
	s_addc_u32 s67, s7, 0
	s_add_u32 s68, s6, 0x5100
	s_addc_u32 s69, s7, 0
	s_add_u32 s70, s6, 0x5200
	s_addc_u32 s71, s7, 0
	s_add_u32 s72, s6, 0x5300
	s_mul_i32 s34, s34, s1
	s_addc_u32 s73, s7, 0
	s_mov_b32 s0, 1
	s_branch .LBB0_326

.LBB0_381:
	s_andn2_b64 vcc, exec, s[4:5]
	s_cbranch_vccnz .LBB0_457
	v_ashrrev_i32_e32 v3, 31, v16
	v_lshrrev_b32_e32 v3, 26, v3
	v_add_u32_e32 v3, v16, v3
	s_waitcnt vmcnt(1)
	v_ashrrev_i32_e32 v10, 6, v3
	v_bfe_i32 v3, v16, 27, 1
	v_lshlrev_b32_e32 v2, 4, v16
	v_lshrrev_b32_e32 v3, 22, v3
	v_add_u32_e32 v3, v2, v3
	v_and_b32_e32 v3, 0xfffffc00, v3
	v_sub_u32_e32 v3, v2, v3
	v_lshrrev_b32_e32 v4, 4, v3
	v_bitop3_b32 v3, v4, v3, 32 bitop3:0x6c
	v_ashrrev_i32_e32 v5, 31, v3
	v_lshrrev_b32_e32 v5, 26, v5
	v_add_u32_e32 v5, v3, v5
	v_lshlrev_b32_e32 v4, 3, v10
	v_ashrrev_i32_e32 v11, 6, v5
	v_and_b32_e32 v5, 0xc0, v5
	v_and_b32_e32 v4, -16, v4
	v_sub_u32_e32 v3, v3, v5
	v_add_u32_e32 v4, v11, v4
	v_ashrrev_i16_sdwa v3, v226, sext(v3) dst_sel:DWORD dst_unused:UNUSED_PAD src0_sel:DWORD src1_sel:BYTE_0
	v_lshlrev_b32_e32 v6, 5, v10
	v_bfe_i32 v12, v3, 0, 16
	v_lshlrev_b32_e32 v3, 1, v4
	v_lshrrev_b32_e32 v5, 2, v4
	v_and_b32_e32 v7, 3, v11
	s_mov_b32 s0, 0x1fffe0
	v_and_b32_e32 v6, 32, v6
	v_and_b32_e32 v3, 24, v3
	v_and_b32_e32 v5, 4, v5
	v_and_or_b32 v7, v4, s0, v7
	v_or3_b32 v3, v7, v5, v3
	v_add_lshl_u32 v5, v6, v12, 1
	v_add_u32_e32 v2, 0x2000, v2
	v_lshl_add_u32 v132, v3, 11, v5
	v_ashrrev_i32_e32 v3, 31, v2
	v_lshrrev_b32_e32 v3, 22, v3
	v_add_u32_e32 v3, v2, v3
	v_ashrrev_i32_e32 v13, 10, v3
	v_mul_i32_i24_e32 v3, 0x400, v13
	v_sub_u32_e32 v2, v2, v3
	v_lshrrev_b32_e32 v3, 4, v2
	v_bitop3_b32 v2, v3, v2, 32 bitop3:0x6c
	v_lshl_add_u32 v130, v4, 11, v5
	v_ashrrev_i32_e32 v4, 31, v2
	v_lshrrev_b32_e32 v4, 26, v4
	v_lshlrev_b32_e32 v3, 3, v13
	v_add_u32_e32 v4, v2, v4
	v_and_b32_e32 v3, -16, v3
	v_ashrrev_i32_e32 v14, 6, v4
	v_add_u32_e32 v3, v14, v3
	v_and_b32_e32 v4, 0xc0, v4
	v_and_b32_e32 v6, 3, v14
	s_ashr_i32 s5, s35, 6
	s_ashr_i32 s7, s6, 31
	s_ashr_i32 s9, s8, 31
	s_ashr_i32 s4, s35, 8
	v_sub_u32_e32 v2, v2, v4
	v_and_or_b32 v6, v3, s0, v6
	s_lshl_b32 s38, s5, 10
	s_lshl_b64 s[0:1], s[6:7], 19
	s_lshl_b64 s[22:23], s[8:9], 19
	v_ashrrev_i16_sdwa v2, v226, sext(v2) dst_sel:DWORD dst_unused:UNUSED_PAD src0_sel:DWORD src1_sel:BYTE_0
	s_add_u32 s64, s16, s22
	v_lshlrev_b32_e32 v5, 5, v13
	v_bfe_i32 v15, v2, 0, 16
	v_lshlrev_b32_e32 v2, 1, v3
	v_lshrrev_b32_e32 v4, 2, v3
	s_addc_u32 s65, s17, s23
	s_add_i32 s40, s38, 0
	v_and_b32_e32 v5, 32, v5
	v_and_b32_e32 v2, 24, v2
	v_and_b32_e32 v4, 4, v4
	s_add_i32 m0, s40, 0x10000
	v_or3_b32 v2, v6, v4, v2
	v_add_lshl_u32 v4, v5, v15, 1
	global_load_lds_dwordx4 v132, s[64:65]
	s_add_i32 m0, s40, 0x12000
	v_lshl_add_u32 v136, v2, 11, v4
	s_add_u32 s30, s12, s0
	global_load_lds_dwordx4 v136, s[64:65]
	s_addc_u32 s31, s13, s1
	s_mov_b32 m0, s40
	s_add_i32 s43, s40, 0x2000
	v_lshl_add_u32 v134, v3, 11, v4
	global_load_lds_dwordx4 v130, s[30:31]
	s_mov_b32 m0, s43
	s_add_u32 s0, s64, 0x40000
	global_load_lds_dwordx4 v134, s[30:31]
	s_addc_u32 s1, s65, 0
	s_add_i32 m0, s40, 0x14000
	v_mov_b32_e32 v133, v195
	global_load_lds_dwordx4 v132, s[0:1]
	s_add_i32 m0, s40, 0x16000
	v_mov_b32_e32 v137, v195
	global_load_lds_dwordx4 v136, s[0:1]
	s_add_u32 s0, s30, 0x40000
	s_addc_u32 s1, s31, 0
	s_add_i32 s69, s40, 0x4000
	s_mov_b32 m0, s69
	s_add_i32 s70, s40, 0x6000
	global_load_lds_dwordx4 v130, s[0:1]
	s_mov_b32 m0, s70
	v_mov_b32_e32 v131, v195
	global_load_lds_dwordx4 v134, s[0:1]
	v_mov_b32_e32 v135, v195
	s_waitcnt vmcnt(0)
	v_lshl_add_u64 v[8:9], s[64:65], 0, v[132:133]
	v_lshl_add_u64 v[6:7], s[64:65], 0, v[136:137]
	v_lshl_add_u64 v[4:5], s[30:31], 0, v[130:131]
	s_cmp_lg_u32 s4, 1
	v_lshl_add_u64 v[2:3], s[30:31], 0, v[134:135]
	s_setprio 1
	s_cbranch_scc1 .LBB0_384
	s_barrier
	s_setprio 0

.LBB0_389:
	s_add_u32 s0, s30, 0xfffc0080
	s_addc_u32 s1, s31, -1
	s_add_i32 s33, 0, 0x10000
	v_add_u32_e32 v156, s33, v158
	ds_read_b128 v[152:155], v156
	ds_read_b128 v[162:165], v156 offset:1024
	ds_read_b128 v[166:169], v156 offset:2048
	ds_read_b128 v[170:173], v156 offset:3072
	s_cmp_eq_u32 s79, 12
	s_cselect_b32 s67, s7, s1
	s_cselect_b32 s66, s9, s0
	s_cselect_b32 s65, s23, s78
	s_cselect_b32 s64, s25, s77
	v_lshl_add_u64 v[156:157], s[30:31], 0, v[148:149]
	s_add_i32 m0, s40, 0xc000
	ds_read_b128 v[174:177], v161
	ds_read_b128 v[178:181], v161 offset:1024
	ds_read_b128 v[182:185], v161 offset:2048
	ds_read_b128 v[186:189], v161 offset:3072
	ds_read_b128 v[190:193], v161 offset:4096
	ds_read_b128 v[198:201], v161 offset:5120
	ds_read_b128 v[202:205], v161 offset:6144
	ds_read_b128 v[206:209], v161 offset:7168
	global_load_lds_dwordx4 v[156:157], off
	v_lshl_add_u64 v[156:157], s[30:31], 0, v[150:151]
	s_add_i32 m0, s40, 0xe000
	s_nop 0
	global_load_lds_dwordx4 v[156:157], off
	s_waitcnt lgkmcnt(8)
	s_barrier
	s_waitcnt lgkmcnt(0)
	s_waitcnt lgkmcnt(0)
	v_mfma_f32_16x16x32_bf16 v[126:129], v[152:155], v[174:177], v[126:129]
	v_mfma_f32_16x16x32_bf16 v[122:125], v[166:169], v[174:177], v[122:125]
	v_mfma_f32_16x16x32_bf16 v[110:113], v[152:155], v[182:185], v[110:113]
	v_mfma_f32_16x16x32_bf16 v[106:109], v[166:169], v[182:185], v[106:109]
	v_mfma_f32_16x16x32_bf16 v[94:97], v[152:155], v[190:193], v[94:97]
	v_mfma_f32_16x16x32_bf16 v[90:93], v[166:169], v[190:193], v[90:93]
	v_mfma_f32_16x16x32_bf16 v[78:81], v[152:155], v[202:205], v[78:81]
	v_mfma_f32_16x16x32_bf16 v[74:77], v[166:169], v[202:205], v[74:77]
	v_mfma_f32_16x16x32_bf16 v[126:129], v[162:165], v[178:181], v[126:129]
	v_mfma_f32_16x16x32_bf16 v[122:125], v[170:173], v[178:181], v[122:125]
	v_mfma_f32_16x16x32_bf16 v[110:113], v[162:165], v[186:189], v[110:113]
	v_mfma_f32_16x16x32_bf16 v[106:109], v[170:173], v[186:189], v[106:109]
	v_mfma_f32_16x16x32_bf16 v[94:97], v[162:165], v[198:201], v[94:97]
	v_mfma_f32_16x16x32_bf16 v[90:93], v[170:173], v[198:201], v[90:93]
	v_mfma_f32_16x16x32_bf16 v[78:81], v[162:165], v[206:209], v[78:81]
	v_mfma_f32_16x16x32_bf16 v[74:77], v[170:173], v[206:209], v[74:77]
	s_barrier
	s_add_i32 s36, 0, 0x14000
	v_add_u32_e32 v156, s36, v158
	s_add_i32 s0, s33, s38
	ds_read_b128 v[210:213], v156
	ds_read_b128 v[214:217], v156 offset:1024
	ds_read_b128 v[218:221], v156 offset:2048
	ds_read_b128 v[238:241], v156 offset:3072
	v_lshl_add_u64 v[156:157], s[64:65], 0, v[132:133]
	s_mov_b32 m0, s0
	v_lshl_add_u64 v[242:243], s[64:65], 0, v[136:137]
	global_load_lds_dwordx4 v[156:157], off
	s_add_i32 m0, s0, 0x2000
	s_nop 0
	global_load_lds_dwordx4 v[242:243], off
	s_barrier
	s_waitcnt lgkmcnt(0)
	s_waitcnt lgkmcnt(0)
	v_mfma_f32_16x16x32_bf16 v[118:121], v[210:213], v[174:177], v[118:121]
	v_mfma_f32_16x16x32_bf16 v[114:117], v[218:221], v[174:177], v[114:117]
	v_mfma_f32_16x16x32_bf16 v[102:105], v[210:213], v[182:185], v[102:105]
	v_mfma_f32_16x16x32_bf16 v[98:101], v[218:221], v[182:185], v[98:101]
	v_mfma_f32_16x16x32_bf16 v[86:89], v[210:213], v[190:193], v[86:89]
	v_mfma_f32_16x16x32_bf16 v[82:85], v[218:221], v[190:193], v[82:85]
	v_mfma_f32_16x16x32_bf16 v[70:73], v[210:213], v[202:205], v[70:73]
	v_mfma_f32_16x16x32_bf16 v[66:69], v[218:221], v[202:205], v[66:69]
	v_mfma_f32_16x16x32_bf16 v[118:121], v[214:217], v[178:181], v[118:121]
	v_mfma_f32_16x16x32_bf16 v[114:117], v[238:241], v[178:181], v[114:117]
	v_mfma_f32_16x16x32_bf16 v[102:105], v[214:217], v[186:189], v[102:105]
	v_mfma_f32_16x16x32_bf16 v[98:101], v[238:241], v[186:189], v[98:101]
	v_mfma_f32_16x16x32_bf16 v[86:89], v[214:217], v[198:201], v[86:89]
	v_mfma_f32_16x16x32_bf16 v[82:85], v[238:241], v[198:201], v[82:85]
	v_mfma_f32_16x16x32_bf16 v[70:73], v[214:217], v[206:209], v[70:73]
	v_mfma_f32_16x16x32_bf16 v[66:69], v[238:241], v[206:209], v[66:69]
	s_mov_b32 m0, s40
	v_lshl_add_u64 v[244:245], s[66:67], 0, v[130:131]
	s_barrier
	ds_read_b128 v[174:177], v161 offset:16384
	ds_read_b128 v[178:181], v161 offset:17408
	ds_read_b128 v[182:185], v161 offset:18432
	ds_read_b128 v[186:189], v161 offset:19456
	ds_read_b128 v[190:193], v161 offset:20480
	ds_read_b128 v[198:201], v161 offset:21504
	ds_read_b128 v[202:205], v161 offset:22528
	ds_read_b128 v[206:209], v161 offset:23552
	global_load_lds_dwordx4 v[244:245], off
	v_lshl_add_u64 v[246:247], s[66:67], 0, v[134:135]
	s_mov_b32 m0, s43
	s_nop 0
	global_load_lds_dwordx4 v[246:247], off
	s_barrier
	s_waitcnt lgkmcnt(0)
	s_waitcnt lgkmcnt(0)
	v_mfma_f32_16x16x32_bf16 v[62:65], v[152:155], v[174:177], v[62:65]
	v_mfma_f32_16x16x32_bf16 v[58:61], v[166:169], v[174:177], v[58:61]
	v_mfma_f32_16x16x32_bf16 v[46:49], v[152:155], v[182:185], v[46:49]
	v_mfma_f32_16x16x32_bf16 v[42:45], v[166:169], v[182:185], v[42:45]
	v_mfma_f32_16x16x32_bf16 v[30:33], v[152:155], v[190:193], v[30:33]
	v_mfma_f32_16x16x32_bf16 v[26:29], v[166:169], v[190:193], v[26:29]
	v_mfma_f32_16x16x32_bf16 v[14:17], v[152:155], v[202:205], v[14:17]
	v_mfma_f32_16x16x32_bf16 v[10:13], v[166:169], v[202:205], v[10:13]
	v_mfma_f32_16x16x32_bf16 v[62:65], v[162:165], v[178:181], v[62:65]
	v_mfma_f32_16x16x32_bf16 v[58:61], v[170:173], v[178:181], v[58:61]
	v_mfma_f32_16x16x32_bf16 v[46:49], v[162:165], v[186:189], v[46:49]
	v_mfma_f32_16x16x32_bf16 v[42:45], v[170:173], v[186:189], v[42:45]
	v_mfma_f32_16x16x32_bf16 v[30:33], v[162:165], v[198:201], v[30:33]
	v_mfma_f32_16x16x32_bf16 v[26:29], v[170:173], v[198:201], v[26:29]
	v_mfma_f32_16x16x32_bf16 v[14:17], v[162:165], v[206:209], v[14:17]
	v_mfma_f32_16x16x32_bf16 v[10:13], v[170:173], v[206:209], v[10:13]
	s_barrier
	s_add_u32 s0, s64, 0x40000
	s_addc_u32 s1, s65, 0
	s_add_i32 s33, s36, s38
	v_lshl_add_u64 v[152:153], s[0:1], 0, v[132:133]
	s_mov_b32 m0, s33
	s_nop 0
	global_load_lds_dwordx4 v[152:153], off
	v_lshl_add_u64 v[152:153], s[0:1], 0, v[136:137]
	s_add_i32 m0, s33, 0x2000
	s_nop 0
	global_load_lds_dwordx4 v[152:153], off
	s_waitcnt vmcnt(6)
	s_barrier
	v_mfma_f32_16x16x32_bf16 v[54:57], v[210:213], v[174:177], v[54:57]
	v_mfma_f32_16x16x32_bf16 v[50:53], v[218:221], v[174:177], v[50:53]
	v_mfma_f32_16x16x32_bf16 v[38:41], v[210:213], v[182:185], v[38:41]
	v_mfma_f32_16x16x32_bf16 v[34:37], v[218:221], v[182:185], v[34:37]
	v_mfma_f32_16x16x32_bf16 v[22:25], v[210:213], v[190:193], v[22:25]
	v_mfma_f32_16x16x32_bf16 v[18:21], v[218:221], v[190:193], v[18:21]
	v_mfma_f32_16x16x32_bf16 v[6:9], v[210:213], v[202:205], v[6:9]
	v_mfma_f32_16x16x32_bf16 v[2:5], v[218:221], v[202:205], v[2:5]
	v_mfma_f32_16x16x32_bf16 v[54:57], v[214:217], v[178:181], v[54:57]
	v_mfma_f32_16x16x32_bf16 v[50:53], v[238:241], v[178:181], v[50:53]
	v_mfma_f32_16x16x32_bf16 v[38:41], v[214:217], v[186:189], v[38:41]
	v_mfma_f32_16x16x32_bf16 v[34:37], v[238:241], v[186:189], v[34:37]
	v_mfma_f32_16x16x32_bf16 v[22:25], v[214:217], v[198:201], v[22:25]
	v_mfma_f32_16x16x32_bf16 v[18:21], v[238:241], v[198:201], v[18:21]
	v_mfma_f32_16x16x32_bf16 v[6:9], v[214:217], v[206:209], v[6:9]
	v_mfma_f32_16x16x32_bf16 v[2:5], v[238:241], v[206:209], v[2:5]
	s_add_i32 s33, 0, 0x18000
	v_add_u32_e32 v170, s33, v158
	s_barrier
	ds_read_b128 v[152:155], v170
	ds_read_b128 v[162:165], v170 offset:1024
	ds_read_b128 v[166:169], v170 offset:2048
	ds_read_b128 v[170:173], v170 offset:3072
	s_add_u32 s0, s66, 0x40000
	s_addc_u32 s1, s67, 0
	s_mov_b32 m0, s69
	v_lshl_add_u64 v[210:211], s[0:1], 0, v[130:131]
	ds_read_b128 v[174:177], v161 offset:32768
	ds_read_b128 v[178:181], v161 offset:33792
	ds_read_b128 v[182:185], v161 offset:34816
	ds_read_b128 v[186:189], v161 offset:35840
	ds_read_b128 v[190:193], v161 offset:36864
	ds_read_b128 v[198:201], v161 offset:37888
	ds_read_b128 v[202:205], v161 offset:38912
	ds_read_b128 v[206:209], v161 offset:39936
	global_load_lds_dwordx4 v[210:211], off
	v_lshl_add_u64 v[210:211], s[0:1], 0, v[134:135]
	s_mov_b32 m0, s70
	s_nop 0
	global_load_lds_dwordx4 v[210:211], off
	s_waitcnt lgkmcnt(8)
	s_barrier
	s_waitcnt lgkmcnt(0)
	s_waitcnt lgkmcnt(0)
	v_mfma_f32_16x16x32_bf16 v[126:129], v[152:155], v[174:177], v[126:129]
	v_mfma_f32_16x16x32_bf16 v[122:125], v[166:169], v[174:177], v[122:125]
	v_mfma_f32_16x16x32_bf16 v[110:113], v[152:155], v[182:185], v[110:113]
	v_mfma_f32_16x16x32_bf16 v[106:109], v[166:169], v[182:185], v[106:109]
	v_mfma_f32_16x16x32_bf16 v[94:97], v[152:155], v[190:193], v[94:97]
	v_mfma_f32_16x16x32_bf16 v[90:93], v[166:169], v[190:193], v[90:93]
	v_mfma_f32_16x16x32_bf16 v[78:81], v[152:155], v[202:205], v[78:81]
	v_mfma_f32_16x16x32_bf16 v[74:77], v[166:169], v[202:205], v[74:77]
	v_mfma_f32_16x16x32_bf16 v[126:129], v[162:165], v[178:181], v[126:129]
	v_mfma_f32_16x16x32_bf16 v[122:125], v[170:173], v[178:181], v[122:125]
	v_mfma_f32_16x16x32_bf16 v[110:113], v[162:165], v[186:189], v[110:113]
	v_mfma_f32_16x16x32_bf16 v[106:109], v[170:173], v[186:189], v[106:109]
	v_mfma_f32_16x16x32_bf16 v[94:97], v[162:165], v[198:201], v[94:97]
	v_mfma_f32_16x16x32_bf16 v[90:93], v[170:173], v[198:201], v[90:93]
	v_mfma_f32_16x16x32_bf16 v[78:81], v[162:165], v[206:209], v[78:81]
	v_mfma_f32_16x16x32_bf16 v[74:77], v[170:173], v[206:209], v[74:77]
	s_barrier
	s_add_i32 s36, 0, 0x1c000
	s_add_i32 s0, s33, s38
	v_add_u32_e32 v194, s36, v158
	v_lshl_add_u64 v[156:157], v[156:157], 0, s[54:55]
	s_mov_b32 m0, s0
	ds_read_b128 v[210:213], v194
	ds_read_b128 v[214:217], v194 offset:1024
	ds_read_b128 v[218:221], v194 offset:2048
	ds_read_b128 v[238:241], v194 offset:3072
	global_load_lds_dwordx4 v[156:157], off
	v_lshl_add_u64 v[156:157], v[242:243], 0, s[54:55]
	s_add_i32 m0, s0, 0x2000
	s_nop 0
	global_load_lds_dwordx4 v[156:157], off
	s_barrier
	s_waitcnt lgkmcnt(0)
	s_waitcnt lgkmcnt(0)
	v_mfma_f32_16x16x32_bf16 v[118:121], v[210:213], v[174:177], v[118:121]
	v_mfma_f32_16x16x32_bf16 v[114:117], v[218:221], v[174:177], v[114:117]
	v_mfma_f32_16x16x32_bf16 v[102:105], v[210:213], v[182:185], v[102:105]
	v_mfma_f32_16x16x32_bf16 v[98:101], v[218:221], v[182:185], v[98:101]
	v_mfma_f32_16x16x32_bf16 v[86:89], v[210:213], v[190:193], v[86:89]
	v_mfma_f32_16x16x32_bf16 v[82:85], v[218:221], v[190:193], v[82:85]
	v_mfma_f32_16x16x32_bf16 v[70:73], v[210:213], v[202:205], v[70:73]
	v_mfma_f32_16x16x32_bf16 v[66:69], v[218:221], v[202:205], v[66:69]
	v_mfma_f32_16x16x32_bf16 v[118:121], v[214:217], v[178:181], v[118:121]
	v_mfma_f32_16x16x32_bf16 v[114:117], v[238:241], v[178:181], v[114:117]
	v_mfma_f32_16x16x32_bf16 v[102:105], v[214:217], v[186:189], v[102:105]
	v_mfma_f32_16x16x32_bf16 v[98:101], v[238:241], v[186:189], v[98:101]
	v_mfma_f32_16x16x32_bf16 v[86:89], v[214:217], v[198:201], v[86:89]
	v_mfma_f32_16x16x32_bf16 v[82:85], v[238:241], v[198:201], v[82:85]
	v_mfma_f32_16x16x32_bf16 v[70:73], v[214:217], v[206:209], v[70:73]
	v_mfma_f32_16x16x32_bf16 v[66:69], v[238:241], v[206:209], v[66:69]
	s_mov_b32 m0, s71
	v_lshl_add_u64 v[156:157], v[244:245], 0, s[54:55]
	s_barrier
	ds_read_b128 v[174:177], v161 offset:49152
	ds_read_b128 v[178:181], v161 offset:50176
	ds_read_b128 v[182:185], v161 offset:51200
	ds_read_b128 v[186:189], v161 offset:52224
	ds_read_b128 v[190:193], v161 offset:53248
	ds_read_b128 v[198:201], v161 offset:54272
	ds_read_b128 v[202:205], v161 offset:55296
	ds_read_b128 v[206:209], v161 offset:56320
	global_load_lds_dwordx4 v[156:157], off
	v_lshl_add_u64 v[156:157], v[246:247], 0, s[54:55]
	s_mov_b32 m0, s72
	s_nop 0
	global_load_lds_dwordx4 v[156:157], off
	s_barrier
	s_waitcnt lgkmcnt(0)
	s_waitcnt lgkmcnt(0)
	v_mfma_f32_16x16x32_bf16 v[62:65], v[152:155], v[174:177], v[62:65]
	v_mfma_f32_16x16x32_bf16 v[58:61], v[166:169], v[174:177], v[58:61]
	v_mfma_f32_16x16x32_bf16 v[46:49], v[152:155], v[182:185], v[46:49]
	v_mfma_f32_16x16x32_bf16 v[42:45], v[166:169], v[182:185], v[42:45]
	v_mfma_f32_16x16x32_bf16 v[30:33], v[152:155], v[190:193], v[30:33]
	v_mfma_f32_16x16x32_bf16 v[26:29], v[166:169], v[190:193], v[26:29]
	v_mfma_f32_16x16x32_bf16 v[14:17], v[152:155], v[202:205], v[14:17]
	v_mfma_f32_16x16x32_bf16 v[10:13], v[166:169], v[202:205], v[10:13]
	v_mfma_f32_16x16x32_bf16 v[62:65], v[162:165], v[178:181], v[62:65]
	v_mfma_f32_16x16x32_bf16 v[58:61], v[170:173], v[178:181], v[58:61]
	v_mfma_f32_16x16x32_bf16 v[46:49], v[162:165], v[186:189], v[46:49]
	v_mfma_f32_16x16x32_bf16 v[42:45], v[170:173], v[186:189], v[42:45]
	v_mfma_f32_16x16x32_bf16 v[30:33], v[162:165], v[198:201], v[30:33]
	v_mfma_f32_16x16x32_bf16 v[26:29], v[170:173], v[198:201], v[26:29]
	v_mfma_f32_16x16x32_bf16 v[14:17], v[162:165], v[206:209], v[14:17]
	v_mfma_f32_16x16x32_bf16 v[10:13], v[170:173], v[206:209], v[10:13]
	s_barrier
	s_add_u32 s0, s64, 0x40080
	s_addc_u32 s1, s65, 0
	s_add_i32 s33, s36, s38
	v_lshl_add_u64 v[152:153], s[0:1], 0, v[132:133]
	s_mov_b32 m0, s33
	s_nop 0
	global_load_lds_dwordx4 v[152:153], off
	v_lshl_add_u64 v[152:153], s[0:1], 0, v[136:137]
	s_add_i32 m0, s33, 0x2000
	s_nop 0
	global_load_lds_dwordx4 v[152:153], off
	s_waitcnt vmcnt(6)
	s_barrier
	v_mfma_f32_16x16x32_bf16 v[54:57], v[210:213], v[174:177], v[54:57]
	v_mfma_f32_16x16x32_bf16 v[50:53], v[218:221], v[174:177], v[50:53]
	v_mfma_f32_16x16x32_bf16 v[38:41], v[210:213], v[182:185], v[38:41]
	v_mfma_f32_16x16x32_bf16 v[34:37], v[218:221], v[182:185], v[34:37]
	v_mfma_f32_16x16x32_bf16 v[22:25], v[210:213], v[190:193], v[22:25]
	v_mfma_f32_16x16x32_bf16 v[18:21], v[218:221], v[190:193], v[18:21]
	v_mfma_f32_16x16x32_bf16 v[6:9], v[210:213], v[202:205], v[6:9]
	v_mfma_f32_16x16x32_bf16 v[2:5], v[218:221], v[202:205], v[2:5]
	v_mfma_f32_16x16x32_bf16 v[54:57], v[214:217], v[178:181], v[54:57]
	v_mfma_f32_16x16x32_bf16 v[50:53], v[238:241], v[178:181], v[50:53]
	v_mfma_f32_16x16x32_bf16 v[38:41], v[214:217], v[186:189], v[38:41]
	v_mfma_f32_16x16x32_bf16 v[34:37], v[238:241], v[186:189], v[34:37]
	v_mfma_f32_16x16x32_bf16 v[22:25], v[214:217], v[198:201], v[22:25]
	v_mfma_f32_16x16x32_bf16 v[18:21], v[238:241], v[198:201], v[18:21]
	v_mfma_f32_16x16x32_bf16 v[6:9], v[214:217], v[206:209], v[6:9]
	v_mfma_f32_16x16x32_bf16 v[2:5], v[238:241], v[206:209], v[2:5]
	s_add_i32 s79, s79, 2
	s_add_u32 s30, s30, 0x100
	s_addc_u32 s31, s31, 0
	s_add_u32 s77, s77, 0x100
	s_addc_u32 s78, s78, 0
	s_cmp_gt_u32 s79, 13
	s_barrier
	s_cbranch_scc0 .LBB0_389
	s_lshl_b32 s0, s8, 8
	v_lshl_add_u32 v162, s6, 8, v139
	v_or_b32_e32 v152, s0, v138
	s_addk_i32 s0, 0xf200
	v_ashrrev_i32_e32 v155, 5, v162
	s_lshr_b32 s23, s0, 8
	v_and_b32_e32 v155, -8, v155
	v_add_u32_e32 v156, s23, v155
	v_add_u32_e32 v154, 0xfffffe00, v152
	s_movk_i32 s1, 0x3ff
	v_ashrrev_i32_e32 v157, 31, v156
	v_cmp_lt_u32_e64 s[8:9], s1, v154
	s_movk_i32 s1, 0xdff
	v_ashrrev_i32_e32 v153, 31, v152
	v_lshlrev_b64 v[156:157], 17, v[156:157]
	v_cmp_lt_i32_e64 s[6:7], s1, v152
	v_lshl_add_u64 v[152:153], v[152:153], 1, s[18:19]
	v_lshl_add_u64 v[156:157], s[20:21], 0, v[156:157]
	s_and_saveexec_b64 s[0:1], s[8:9]
	s_xor_b64 s[30:31], exec, s[0:1]
	s_cbranch_execz .LBB0_396
	s_and_saveexec_b64 s[0:1], s[6:7]
	s_xor_b64 s[64:65], exec, s[0:1]
	s_cbranch_execz .LBB0_393
	v_mul_f32_e32 v155, 0xbfb8aa3b, v126
	v_exp_f32_e32 v155, v155
	v_mul_f32_e32 v163, 0xbfb8aa3b, v122
	v_exp_f32_e32 v163, v163
	v_mul_f32_e32 v165, 0xbfb8aa3b, v114
	v_add_f32_e32 v155, 1.0, v155
	v_rcp_f32_e32 v168, v155
	v_add_f32_e32 v155, 1.0, v163
	v_rcp_f32_e32 v170, v155
	v_mul_f32_e32 v155, 0xbfb8aa3b, v127
	v_exp_f32_e32 v155, v155
	v_mul_f32_e32 v163, 0xbfb8aa3b, v123
	v_exp_f32_e32 v163, v163
	v_mul_f32_e32 v164, 0xbfb8aa3b, v118
	v_exp_f32_e32 v166, v165
	v_mul_f32_e32 v165, 0xbfb8aa3b, v119
	v_exp_f32_e32 v164, v164
	v_exp_f32_e32 v165, v165
	v_mul_f32_e32 v167, 0xbfb8aa3b, v115
	v_add_f32_e32 v155, 1.0, v155
	v_rcp_f32_e32 v169, v155
	v_exp_f32_e32 v167, v167
	v_add_f32_e32 v163, 1.0, v163
	v_rcp_f32_e32 v171, v163
	v_pk_add_f32 v[164:165], v[164:165], 1.0 op_sel_hi:[1,0]
	v_mul_f32_e32 v178, 0xbfb8aa3b, v117
	v_rcp_f32_e32 v155, v164
	v_pk_mul_f32 v[168:169], v[168:169], v[164:165]
	v_rcp_f32_e32 v163, v165
	v_pk_add_f32 v[164:165], v[166:167], 1.0 op_sel_hi:[1,0]
	s_nop 0
	v_rcp_f32_e32 v176, v164
	v_pk_mul_f32 v[166:167], v[170:171], v[164:165]
	v_mul_f32_e32 v164, 0xbfb8aa3b, v128
	v_rcp_f32_e32 v177, v165
	v_exp_f32_e32 v165, v164
	v_mul_f32_e32 v164, 0xbfb8aa3b, v124
	v_exp_f32_e32 v171, v164
	v_mul_f32_e32 v164, 0xbfb8aa3b, v120
	v_add_f32_e32 v165, 1.0, v165
	v_rcp_f32_e32 v172, v165
	v_add_f32_e32 v165, 1.0, v171
	v_rcp_f32_e32 v174, v165
	v_mul_f32_e32 v165, 0xbfb8aa3b, v129
	v_exp_f32_e32 v171, v165
	v_mul_f32_e32 v165, 0xbfb8aa3b, v125
	v_exp_f32_e32 v175, v165
	v_mul_f32_e32 v165, 0xbfb8aa3b, v121
	v_exp_f32_e32 v164, v164
	v_exp_f32_e32 v165, v165
	v_add_f32_e32 v171, 1.0, v171
	v_rcp_f32_e32 v173, v171
	v_mul_f32_e32 v170, 0xbfb8aa3b, v116
	v_exp_f32_e32 v170, v170
	v_exp_f32_e32 v171, v178
	v_pk_add_f32 v[164:165], v[164:165], 1.0 op_sel_hi:[1,0]
	v_cvt_pk_bf16_f32 v166, v166, v167
	v_rcp_f32_e32 v178, v164
	v_pk_mul_f32 v[172:173], v[172:173], v[164:165]
	v_add_f32_e32 v164, 1.0, v175
	v_rcp_f32_e32 v175, v164
	v_rcp_f32_e32 v179, v165
	v_pk_add_f32 v[164:165], v[170:171], 1.0 op_sel_hi:[1,0]
	s_nop 0
	v_rcp_f32_e32 v180, v164
	v_rcp_f32_e32 v181, v165
	v_pk_mul_f32 v[170:171], v[174:175], v[164:165]
	v_lshl_add_u64 v[174:175], v[140:141], 1, v[156:157]
	v_cvt_pk_bf16_f32 v164, v168, v169
	v_cvt_pk_bf16_f32 v165, v172, v173
	v_cvt_pk_bf16_f32 v167, v170, v171
	v_add_co_u32_e32 v168, vcc, 0x10000, v174
	global_store_dwordx4 v[174:175], v[164:167], off
	s_nop 0
	v_addc_co_u32_e32 v169, vcc, 0, v175, vcc
	v_cvt_pk_bf16_f32 v164, v155, v163
	v_cvt_pk_bf16_f32 v165, v178, v179
	v_cvt_pk_bf16_f32 v166, v176, v177
	v_cvt_pk_bf16_f32 v167, v180, v181
	global_store_dwordx4 v[168:169], v[164:167], off

.LBB0_464:
	s_andn2_b64 vcc, exec, s[8:9]
	s_cbranch_vccnz .LBB0_543
	v_ashrrev_i32_e32 v3, 31, v10
	v_lshrrev_b32_e32 v3, 26, v3
	v_add_u32_e32 v3, v10, v3
	v_ashrrev_i32_e32 v11, 6, v3
	v_bfe_i32 v3, v10, 27, 1
	v_lshlrev_b32_e32 v2, 4, v10
	v_lshrrev_b32_e32 v3, 22, v3
	v_add_u32_e32 v3, v2, v3
	v_and_b32_e32 v3, 0xfffffc00, v3
	v_sub_u32_e32 v3, v2, v3
	v_lshrrev_b32_e32 v4, 4, v3
	v_bitop3_b32 v3, v4, v3, 32 bitop3:0x6c
	v_ashrrev_i32_e32 v5, 31, v3
	v_lshrrev_b32_e32 v5, 26, v5
	v_add_u32_e32 v5, v3, v5
	v_lshlrev_b32_e32 v4, 3, v11
	v_ashrrev_i32_e32 v12, 6, v5
	v_and_b32_e32 v5, 0xc0, v5
	v_and_b32_e32 v4, -16, v4
	v_sub_u32_e32 v3, v3, v5
	v_add_u32_e32 v4, v12, v4
	v_ashrrev_i16_sdwa v3, v226, sext(v3) dst_sel:DWORD dst_unused:UNUSED_PAD src0_sel:DWORD src1_sel:BYTE_0
	v_lshlrev_b32_e32 v6, 5, v11
	v_bfe_i32 v13, v3, 0, 16
	v_lshlrev_b32_e32 v3, 1, v4
	v_lshrrev_b32_e32 v5, 2, v4
	v_and_b32_e32 v7, 3, v12
	s_mov_b32 s0, 0x1fffe0
	v_and_b32_e32 v6, 32, v6
	v_and_b32_e32 v3, 24, v3
	v_and_b32_e32 v5, 4, v5
	v_and_or_b32 v7, v4, s0, v7
	v_or3_b32 v3, v7, v5, v3
	v_add_lshl_u32 v5, v6, v13, 1
	v_add_u32_e32 v2, 0x2000, v2
	v_lshl_add_u32 v132, v3, 11, v5
	v_ashrrev_i32_e32 v3, 31, v2
	v_lshrrev_b32_e32 v3, 22, v3
	v_add_u32_e32 v3, v2, v3
	v_ashrrev_i32_e32 v14, 10, v3
	v_mul_i32_i24_e32 v3, 0x400, v14
	v_sub_u32_e32 v2, v2, v3
	v_lshrrev_b32_e32 v3, 4, v2
	v_bitop3_b32 v2, v3, v2, 32 bitop3:0x6c
	v_lshl_add_u32 v130, v4, 11, v5
	v_ashrrev_i32_e32 v4, 31, v2
	v_lshrrev_b32_e32 v4, 26, v4
	v_lshlrev_b32_e32 v3, 3, v14
	v_add_u32_e32 v4, v2, v4
	v_and_b32_e32 v3, -16, v3
	v_ashrrev_i32_e32 v15, 6, v4
	v_add_u32_e32 v3, v15, v3
	v_and_b32_e32 v6, 3, v15
	v_and_b32_e32 v4, 0xc0, v4
	v_and_or_b32 v6, v3, s0, v6
	s_ashr_i32 s0, s35, 6
	s_ashr_i32 s5, s4, 31
	s_ashr_i32 s7, s6, 31
	s_ashr_i32 s8, s35, 8
	v_sub_u32_e32 v2, v2, v4
	s_lshl_b32 s38, s0, 10
	s_lshl_b64 s[22:23], s[4:5], 19
	s_lshl_b64 s[24:25], s[6:7], 19
	v_ashrrev_i16_sdwa v2, v226, sext(v2) dst_sel:DWORD dst_unused:UNUSED_PAD src0_sel:DWORD src1_sel:BYTE_0
	s_add_u32 s64, s16, s24
	v_lshlrev_b32_e32 v5, 5, v14
	v_bfe_i32 v16, v2, 0, 16
	v_lshlrev_b32_e32 v2, 1, v3
	v_lshrrev_b32_e32 v4, 2, v3
	s_addc_u32 s65, s17, s25
	s_add_i32 s40, s38, 0
	v_and_b32_e32 v5, 32, v5
	v_and_b32_e32 v2, 24, v2
	v_and_b32_e32 v4, 4, v4
	s_add_i32 m0, s40, 0x10000
	v_or3_b32 v2, v6, v4, v2
	v_add_lshl_u32 v4, v5, v16, 1
	global_load_lds_dwordx4 v132, s[64:65]
	s_add_i32 m0, s40, 0x12000
	v_lshl_add_u32 v136, v2, 11, v4
	s_add_u32 s30, s12, s22
	global_load_lds_dwordx4 v136, s[64:65]
	s_addc_u32 s31, s13, s23
	s_mov_b32 m0, s40
	s_add_i32 s43, s40, 0x2000
	v_lshl_add_u32 v134, v3, 11, v4
	global_load_lds_dwordx4 v130, s[30:31]
	s_mov_b32 m0, s43
	s_add_u32 s22, s64, 0x40000
	global_load_lds_dwordx4 v134, s[30:31]
	s_addc_u32 s23, s65, 0
	s_add_i32 m0, s40, 0x14000
	v_mov_b32_e32 v133, v195
	global_load_lds_dwordx4 v132, s[22:23]
	s_add_i32 m0, s40, 0x16000
	v_mov_b32_e32 v137, v195
	global_load_lds_dwordx4 v136, s[22:23]
	s_add_u32 s22, s30, 0x40000
	s_addc_u32 s23, s31, 0
	s_add_i32 s69, s40, 0x4000
	s_mov_b32 m0, s69
	s_add_i32 s70, s40, 0x6000
	global_load_lds_dwordx4 v130, s[22:23]
	s_mov_b32 m0, s70
	v_mov_b32_e32 v131, v195
	global_load_lds_dwordx4 v134, s[22:23]
	v_mov_b32_e32 v135, v195
	s_waitcnt vmcnt(0)
	v_lshl_add_u64 v[8:9], s[64:65], 0, v[132:133]
	v_lshl_add_u64 v[6:7], s[64:65], 0, v[136:137]
	v_lshl_add_u64 v[4:5], s[30:31], 0, v[130:131]
	s_cmp_lg_u32 s8, 1
	v_lshl_add_u64 v[2:3], s[30:31], 0, v[134:135]
	s_setprio 1
	s_cbranch_scc1 .LBB0_467
	s_barrier
	s_setprio 0

.LBB0_475:
	s_add_u32 s0, s30, 0xfffc0080
	s_addc_u32 s1, s31, -1
	s_add_i32 s33, 0, 0x10000
	v_add_u32_e32 v156, s33, v158
	ds_read_b128 v[152:155], v156
	ds_read_b128 v[162:165], v156 offset:1024
	ds_read_b128 v[166:169], v156 offset:2048
	ds_read_b128 v[170:173], v156 offset:3072
	s_cmp_eq_u32 s79, 12
	s_cselect_b32 s67, s5, s1
	s_cselect_b32 s66, s7, s0
	s_cselect_b32 s65, s9, s78
	s_cselect_b32 s64, s23, s77
	v_lshl_add_u64 v[156:157], s[30:31], 0, v[148:149]
	s_add_i32 m0, s40, 0xc000
	ds_read_b128 v[174:177], v161
	ds_read_b128 v[178:181], v161 offset:1024
	ds_read_b128 v[182:185], v161 offset:2048
	ds_read_b128 v[186:189], v161 offset:3072
	ds_read_b128 v[190:193], v161 offset:4096
	ds_read_b128 v[198:201], v161 offset:5120
	ds_read_b128 v[202:205], v161 offset:6144
	ds_read_b128 v[206:209], v161 offset:7168
	global_load_lds_dwordx4 v[156:157], off
	v_lshl_add_u64 v[156:157], s[30:31], 0, v[150:151]
	s_add_i32 m0, s40, 0xe000
	s_nop 0
	global_load_lds_dwordx4 v[156:157], off
	s_waitcnt lgkmcnt(8)
	s_barrier
	s_waitcnt lgkmcnt(0)
	s_waitcnt lgkmcnt(0)
	v_mfma_f32_16x16x32_bf16 v[126:129], v[152:155], v[174:177], v[126:129]
	v_mfma_f32_16x16x32_bf16 v[122:125], v[166:169], v[174:177], v[122:125]
	v_mfma_f32_16x16x32_bf16 v[110:113], v[152:155], v[182:185], v[110:113]
	v_mfma_f32_16x16x32_bf16 v[106:109], v[166:169], v[182:185], v[106:109]
	v_mfma_f32_16x16x32_bf16 v[94:97], v[152:155], v[190:193], v[94:97]
	v_mfma_f32_16x16x32_bf16 v[90:93], v[166:169], v[190:193], v[90:93]
	v_mfma_f32_16x16x32_bf16 v[78:81], v[152:155], v[202:205], v[78:81]
	v_mfma_f32_16x16x32_bf16 v[74:77], v[166:169], v[202:205], v[74:77]
	v_mfma_f32_16x16x32_bf16 v[126:129], v[162:165], v[178:181], v[126:129]
	v_mfma_f32_16x16x32_bf16 v[122:125], v[170:173], v[178:181], v[122:125]
	v_mfma_f32_16x16x32_bf16 v[110:113], v[162:165], v[186:189], v[110:113]
	v_mfma_f32_16x16x32_bf16 v[106:109], v[170:173], v[186:189], v[106:109]
	v_mfma_f32_16x16x32_bf16 v[94:97], v[162:165], v[198:201], v[94:97]
	v_mfma_f32_16x16x32_bf16 v[90:93], v[170:173], v[198:201], v[90:93]
	v_mfma_f32_16x16x32_bf16 v[78:81], v[162:165], v[206:209], v[78:81]
	v_mfma_f32_16x16x32_bf16 v[74:77], v[170:173], v[206:209], v[74:77]
	s_barrier
	s_add_i32 s36, 0, 0x14000
	v_add_u32_e32 v156, s36, v158
	s_add_i32 s0, s33, s38
	ds_read_b128 v[210:213], v156
	ds_read_b128 v[214:217], v156 offset:1024
	ds_read_b128 v[218:221], v156 offset:2048
	ds_read_b128 v[238:241], v156 offset:3072
	v_lshl_add_u64 v[156:157], s[64:65], 0, v[132:133]
	s_mov_b32 m0, s0
	v_lshl_add_u64 v[242:243], s[64:65], 0, v[136:137]
	global_load_lds_dwordx4 v[156:157], off
	s_add_i32 m0, s0, 0x2000
	s_nop 0
	global_load_lds_dwordx4 v[242:243], off
	s_barrier
	s_waitcnt lgkmcnt(0)
	s_waitcnt lgkmcnt(0)
	v_mfma_f32_16x16x32_bf16 v[118:121], v[210:213], v[174:177], v[118:121]
	v_mfma_f32_16x16x32_bf16 v[114:117], v[218:221], v[174:177], v[114:117]
	v_mfma_f32_16x16x32_bf16 v[102:105], v[210:213], v[182:185], v[102:105]
	v_mfma_f32_16x16x32_bf16 v[98:101], v[218:221], v[182:185], v[98:101]
	v_mfma_f32_16x16x32_bf16 v[86:89], v[210:213], v[190:193], v[86:89]
	v_mfma_f32_16x16x32_bf16 v[82:85], v[218:221], v[190:193], v[82:85]
	v_mfma_f32_16x16x32_bf16 v[70:73], v[210:213], v[202:205], v[70:73]
	v_mfma_f32_16x16x32_bf16 v[66:69], v[218:221], v[202:205], v[66:69]
	v_mfma_f32_16x16x32_bf16 v[118:121], v[214:217], v[178:181], v[118:121]
	v_mfma_f32_16x16x32_bf16 v[114:117], v[238:241], v[178:181], v[114:117]
	v_mfma_f32_16x16x32_bf16 v[102:105], v[214:217], v[186:189], v[102:105]
	v_mfma_f32_16x16x32_bf16 v[98:101], v[238:241], v[186:189], v[98:101]
	v_mfma_f32_16x16x32_bf16 v[86:89], v[214:217], v[198:201], v[86:89]
	v_mfma_f32_16x16x32_bf16 v[82:85], v[238:241], v[198:201], v[82:85]
	v_mfma_f32_16x16x32_bf16 v[70:73], v[214:217], v[206:209], v[70:73]
	v_mfma_f32_16x16x32_bf16 v[66:69], v[238:241], v[206:209], v[66:69]
	s_mov_b32 m0, s40
	v_lshl_add_u64 v[244:245], s[66:67], 0, v[130:131]
	s_barrier
	ds_read_b128 v[174:177], v161 offset:16384
	ds_read_b128 v[178:181], v161 offset:17408
	ds_read_b128 v[182:185], v161 offset:18432
	ds_read_b128 v[186:189], v161 offset:19456
	ds_read_b128 v[190:193], v161 offset:20480
	ds_read_b128 v[198:201], v161 offset:21504
	ds_read_b128 v[202:205], v161 offset:22528
	ds_read_b128 v[206:209], v161 offset:23552
	global_load_lds_dwordx4 v[244:245], off
	v_lshl_add_u64 v[246:247], s[66:67], 0, v[134:135]
	s_mov_b32 m0, s43
	s_nop 0
	global_load_lds_dwordx4 v[246:247], off
	s_barrier
	s_waitcnt lgkmcnt(0)
	s_waitcnt lgkmcnt(0)
	v_mfma_f32_16x16x32_bf16 v[62:65], v[152:155], v[174:177], v[62:65]
	v_mfma_f32_16x16x32_bf16 v[58:61], v[166:169], v[174:177], v[58:61]
	v_mfma_f32_16x16x32_bf16 v[46:49], v[152:155], v[182:185], v[46:49]
	v_mfma_f32_16x16x32_bf16 v[42:45], v[166:169], v[182:185], v[42:45]
	v_mfma_f32_16x16x32_bf16 v[30:33], v[152:155], v[190:193], v[30:33]
	v_mfma_f32_16x16x32_bf16 v[26:29], v[166:169], v[190:193], v[26:29]
	v_mfma_f32_16x16x32_bf16 v[14:17], v[152:155], v[202:205], v[14:17]
	v_mfma_f32_16x16x32_bf16 v[10:13], v[166:169], v[202:205], v[10:13]
	v_mfma_f32_16x16x32_bf16 v[62:65], v[162:165], v[178:181], v[62:65]
	v_mfma_f32_16x16x32_bf16 v[58:61], v[170:173], v[178:181], v[58:61]
	v_mfma_f32_16x16x32_bf16 v[46:49], v[162:165], v[186:189], v[46:49]
	v_mfma_f32_16x16x32_bf16 v[42:45], v[170:173], v[186:189], v[42:45]
	v_mfma_f32_16x16x32_bf16 v[30:33], v[162:165], v[198:201], v[30:33]
	v_mfma_f32_16x16x32_bf16 v[26:29], v[170:173], v[198:201], v[26:29]
	v_mfma_f32_16x16x32_bf16 v[14:17], v[162:165], v[206:209], v[14:17]
	v_mfma_f32_16x16x32_bf16 v[10:13], v[170:173], v[206:209], v[10:13]
	s_barrier
	s_add_u32 s0, s64, 0x40000
	s_addc_u32 s1, s65, 0
	s_add_i32 s33, s36, s38
	v_lshl_add_u64 v[152:153], s[0:1], 0, v[132:133]
	s_mov_b32 m0, s33
	s_nop 0
	global_load_lds_dwordx4 v[152:153], off
	v_lshl_add_u64 v[152:153], s[0:1], 0, v[136:137]
	s_add_i32 m0, s33, 0x2000
	s_nop 0
	global_load_lds_dwordx4 v[152:153], off
	s_waitcnt vmcnt(6)
	s_barrier
	v_mfma_f32_16x16x32_bf16 v[54:57], v[210:213], v[174:177], v[54:57]
	v_mfma_f32_16x16x32_bf16 v[50:53], v[218:221], v[174:177], v[50:53]
	v_mfma_f32_16x16x32_bf16 v[38:41], v[210:213], v[182:185], v[38:41]
	v_mfma_f32_16x16x32_bf16 v[34:37], v[218:221], v[182:185], v[34:37]
	v_mfma_f32_16x16x32_bf16 v[22:25], v[210:213], v[190:193], v[22:25]
	v_mfma_f32_16x16x32_bf16 v[18:21], v[218:221], v[190:193], v[18:21]
	v_mfma_f32_16x16x32_bf16 v[6:9], v[210:213], v[202:205], v[6:9]
	v_mfma_f32_16x16x32_bf16 v[2:5], v[218:221], v[202:205], v[2:5]
	v_mfma_f32_16x16x32_bf16 v[54:57], v[214:217], v[178:181], v[54:57]
	v_mfma_f32_16x16x32_bf16 v[50:53], v[238:241], v[178:181], v[50:53]
	v_mfma_f32_16x16x32_bf16 v[38:41], v[214:217], v[186:189], v[38:41]
	v_mfma_f32_16x16x32_bf16 v[34:37], v[238:241], v[186:189], v[34:37]
	v_mfma_f32_16x16x32_bf16 v[22:25], v[214:217], v[198:201], v[22:25]
	v_mfma_f32_16x16x32_bf16 v[18:21], v[238:241], v[198:201], v[18:21]
	v_mfma_f32_16x16x32_bf16 v[6:9], v[214:217], v[206:209], v[6:9]
	v_mfma_f32_16x16x32_bf16 v[2:5], v[238:241], v[206:209], v[2:5]
	s_add_i32 s33, 0, 0x18000
	v_add_u32_e32 v170, s33, v158
	s_barrier
	ds_read_b128 v[152:155], v170
	ds_read_b128 v[162:165], v170 offset:1024
	ds_read_b128 v[166:169], v170 offset:2048
	ds_read_b128 v[170:173], v170 offset:3072
	s_add_u32 s0, s66, 0x40000
	s_addc_u32 s1, s67, 0
	s_mov_b32 m0, s69
	v_lshl_add_u64 v[210:211], s[0:1], 0, v[130:131]
	ds_read_b128 v[174:177], v161 offset:32768
	ds_read_b128 v[178:181], v161 offset:33792
	ds_read_b128 v[182:185], v161 offset:34816
	ds_read_b128 v[186:189], v161 offset:35840
	ds_read_b128 v[190:193], v161 offset:36864
	ds_read_b128 v[198:201], v161 offset:37888
	ds_read_b128 v[202:205], v161 offset:38912
	ds_read_b128 v[206:209], v161 offset:39936
	global_load_lds_dwordx4 v[210:211], off
	v_lshl_add_u64 v[210:211], s[0:1], 0, v[134:135]
	s_mov_b32 m0, s70
	s_nop 0
	global_load_lds_dwordx4 v[210:211], off
	s_waitcnt lgkmcnt(8)
	s_barrier
	s_waitcnt lgkmcnt(0)
	s_waitcnt lgkmcnt(0)
	v_mfma_f32_16x16x32_bf16 v[126:129], v[152:155], v[174:177], v[126:129]
	v_mfma_f32_16x16x32_bf16 v[122:125], v[166:169], v[174:177], v[122:125]
	v_mfma_f32_16x16x32_bf16 v[110:113], v[152:155], v[182:185], v[110:113]
	v_mfma_f32_16x16x32_bf16 v[106:109], v[166:169], v[182:185], v[106:109]
	v_mfma_f32_16x16x32_bf16 v[94:97], v[152:155], v[190:193], v[94:97]
	v_mfma_f32_16x16x32_bf16 v[90:93], v[166:169], v[190:193], v[90:93]
	v_mfma_f32_16x16x32_bf16 v[78:81], v[152:155], v[202:205], v[78:81]
	v_mfma_f32_16x16x32_bf16 v[74:77], v[166:169], v[202:205], v[74:77]
	v_mfma_f32_16x16x32_bf16 v[126:129], v[162:165], v[178:181], v[126:129]
	v_mfma_f32_16x16x32_bf16 v[122:125], v[170:173], v[178:181], v[122:125]
	v_mfma_f32_16x16x32_bf16 v[110:113], v[162:165], v[186:189], v[110:113]
	v_mfma_f32_16x16x32_bf16 v[106:109], v[170:173], v[186:189], v[106:109]
	v_mfma_f32_16x16x32_bf16 v[94:97], v[162:165], v[198:201], v[94:97]
	v_mfma_f32_16x16x32_bf16 v[90:93], v[170:173], v[198:201], v[90:93]
	v_mfma_f32_16x16x32_bf16 v[78:81], v[162:165], v[206:209], v[78:81]
	v_mfma_f32_16x16x32_bf16 v[74:77], v[170:173], v[206:209], v[74:77]
	s_barrier
	s_add_i32 s36, 0, 0x1c000
	s_add_i32 s0, s33, s38
	v_add_u32_e32 v194, s36, v158
	v_lshl_add_u64 v[156:157], v[156:157], 0, s[54:55]
	s_mov_b32 m0, s0
	ds_read_b128 v[210:213], v194
	ds_read_b128 v[214:217], v194 offset:1024
	ds_read_b128 v[218:221], v194 offset:2048
	ds_read_b128 v[238:241], v194 offset:3072
	global_load_lds_dwordx4 v[156:157], off
	v_lshl_add_u64 v[156:157], v[242:243], 0, s[54:55]
	s_add_i32 m0, s0, 0x2000
	s_nop 0
	global_load_lds_dwordx4 v[156:157], off
	s_barrier
	s_waitcnt lgkmcnt(0)
	s_waitcnt lgkmcnt(0)
	v_mfma_f32_16x16x32_bf16 v[118:121], v[210:213], v[174:177], v[118:121]
	v_mfma_f32_16x16x32_bf16 v[114:117], v[218:221], v[174:177], v[114:117]
	v_mfma_f32_16x16x32_bf16 v[102:105], v[210:213], v[182:185], v[102:105]
	v_mfma_f32_16x16x32_bf16 v[98:101], v[218:221], v[182:185], v[98:101]
	v_mfma_f32_16x16x32_bf16 v[86:89], v[210:213], v[190:193], v[86:89]
	v_mfma_f32_16x16x32_bf16 v[82:85], v[218:221], v[190:193], v[82:85]
	v_mfma_f32_16x16x32_bf16 v[70:73], v[210:213], v[202:205], v[70:73]
	v_mfma_f32_16x16x32_bf16 v[66:69], v[218:221], v[202:205], v[66:69]
	v_mfma_f32_16x16x32_bf16 v[118:121], v[214:217], v[178:181], v[118:121]
	v_mfma_f32_16x16x32_bf16 v[114:117], v[238:241], v[178:181], v[114:117]
	v_mfma_f32_16x16x32_bf16 v[102:105], v[214:217], v[186:189], v[102:105]
	v_mfma_f32_16x16x32_bf16 v[98:101], v[238:241], v[186:189], v[98:101]
	v_mfma_f32_16x16x32_bf16 v[86:89], v[214:217], v[198:201], v[86:89]
	v_mfma_f32_16x16x32_bf16 v[82:85], v[238:241], v[198:201], v[82:85]
	v_mfma_f32_16x16x32_bf16 v[70:73], v[214:217], v[206:209], v[70:73]
	v_mfma_f32_16x16x32_bf16 v[66:69], v[238:241], v[206:209], v[66:69]
	s_mov_b32 m0, s71
	v_lshl_add_u64 v[156:157], v[244:245], 0, s[54:55]
	s_barrier
	ds_read_b128 v[174:177], v161 offset:49152
	ds_read_b128 v[178:181], v161 offset:50176
	ds_read_b128 v[182:185], v161 offset:51200
	ds_read_b128 v[186:189], v161 offset:52224
	ds_read_b128 v[190:193], v161 offset:53248
	ds_read_b128 v[198:201], v161 offset:54272
	ds_read_b128 v[202:205], v161 offset:55296
	ds_read_b128 v[206:209], v161 offset:56320
	global_load_lds_dwordx4 v[156:157], off
	v_lshl_add_u64 v[156:157], v[246:247], 0, s[54:55]
	s_mov_b32 m0, s72
	s_nop 0
	global_load_lds_dwordx4 v[156:157], off
	s_barrier
	s_waitcnt lgkmcnt(0)
	s_waitcnt lgkmcnt(0)
	v_mfma_f32_16x16x32_bf16 v[62:65], v[152:155], v[174:177], v[62:65]
	v_mfma_f32_16x16x32_bf16 v[58:61], v[166:169], v[174:177], v[58:61]
	v_mfma_f32_16x16x32_bf16 v[46:49], v[152:155], v[182:185], v[46:49]
	v_mfma_f32_16x16x32_bf16 v[42:45], v[166:169], v[182:185], v[42:45]
	v_mfma_f32_16x16x32_bf16 v[30:33], v[152:155], v[190:193], v[30:33]
	v_mfma_f32_16x16x32_bf16 v[26:29], v[166:169], v[190:193], v[26:29]
	v_mfma_f32_16x16x32_bf16 v[14:17], v[152:155], v[202:205], v[14:17]
	v_mfma_f32_16x16x32_bf16 v[10:13], v[166:169], v[202:205], v[10:13]
	v_mfma_f32_16x16x32_bf16 v[62:65], v[162:165], v[178:181], v[62:65]
	v_mfma_f32_16x16x32_bf16 v[58:61], v[170:173], v[178:181], v[58:61]
	v_mfma_f32_16x16x32_bf16 v[46:49], v[162:165], v[186:189], v[46:49]
	v_mfma_f32_16x16x32_bf16 v[42:45], v[170:173], v[186:189], v[42:45]
	v_mfma_f32_16x16x32_bf16 v[30:33], v[162:165], v[198:201], v[30:33]
	v_mfma_f32_16x16x32_bf16 v[26:29], v[170:173], v[198:201], v[26:29]
	v_mfma_f32_16x16x32_bf16 v[14:17], v[162:165], v[206:209], v[14:17]
	v_mfma_f32_16x16x32_bf16 v[10:13], v[170:173], v[206:209], v[10:13]
	s_barrier
	s_add_u32 s0, s64, 0x40080
	s_addc_u32 s1, s65, 0
	s_add_i32 s33, s36, s38
	v_lshl_add_u64 v[152:153], s[0:1], 0, v[132:133]
	s_mov_b32 m0, s33
	s_nop 0
	global_load_lds_dwordx4 v[152:153], off
	v_lshl_add_u64 v[152:153], s[0:1], 0, v[136:137]
	s_add_i32 m0, s33, 0x2000
	s_nop 0
	global_load_lds_dwordx4 v[152:153], off
	s_waitcnt vmcnt(6)
	s_barrier
	v_mfma_f32_16x16x32_bf16 v[54:57], v[210:213], v[174:177], v[54:57]
	v_mfma_f32_16x16x32_bf16 v[50:53], v[218:221], v[174:177], v[50:53]
	v_mfma_f32_16x16x32_bf16 v[38:41], v[210:213], v[182:185], v[38:41]
	v_mfma_f32_16x16x32_bf16 v[34:37], v[218:221], v[182:185], v[34:37]
	v_mfma_f32_16x16x32_bf16 v[22:25], v[210:213], v[190:193], v[22:25]
	v_mfma_f32_16x16x32_bf16 v[18:21], v[218:221], v[190:193], v[18:21]
	v_mfma_f32_16x16x32_bf16 v[6:9], v[210:213], v[202:205], v[6:9]
	v_mfma_f32_16x16x32_bf16 v[2:5], v[218:221], v[202:205], v[2:5]
	v_mfma_f32_16x16x32_bf16 v[54:57], v[214:217], v[178:181], v[54:57]
	v_mfma_f32_16x16x32_bf16 v[50:53], v[238:241], v[178:181], v[50:53]
	v_mfma_f32_16x16x32_bf16 v[38:41], v[214:217], v[186:189], v[38:41]
	v_mfma_f32_16x16x32_bf16 v[34:37], v[238:241], v[186:189], v[34:37]
	v_mfma_f32_16x16x32_bf16 v[22:25], v[214:217], v[198:201], v[22:25]
	v_mfma_f32_16x16x32_bf16 v[18:21], v[238:241], v[198:201], v[18:21]
	v_mfma_f32_16x16x32_bf16 v[6:9], v[214:217], v[206:209], v[6:9]
	v_mfma_f32_16x16x32_bf16 v[2:5], v[238:241], v[206:209], v[2:5]
	s_add_i32 s79, s79, 2
	s_add_u32 s30, s30, 0x100
	s_addc_u32 s31, s31, 0
	s_add_u32 s77, s77, 0x100
	s_addc_u32 s78, s78, 0
	s_cmp_gt_u32 s79, 13
	s_barrier
	s_cbranch_scc0 .LBB0_475
	s_lshl_b32 s0, s6, 8
	v_lshl_add_u32 v162, s4, 8, v139
	v_or_b32_e32 v152, s0, v138
	s_addk_i32 s0, 0xf200
	v_ashrrev_i32_e32 v155, 5, v162
	s_lshr_b32 s9, s0, 8
	v_and_b32_e32 v155, -8, v155
	v_add_u32_e32 v154, 0xfffffe00, v152
	s_movk_i32 s1, 0x3ff
	v_add_u32_e32 v156, s9, v155
	v_cmp_lt_u32_e64 s[6:7], s1, v154
	s_movk_i32 s1, 0xdff
	v_ashrrev_i32_e32 v157, 31, v156
	v_cmp_lt_i32_e64 s[4:5], s1, v152
	v_ashrrev_i32_e32 v153, 31, v152
	v_lshlrev_b64 v[156:157], 17, v[156:157]
	s_and_saveexec_b64 s[0:1], s[6:7]
	s_xor_b64 s[30:31], exec, s[0:1]
	s_cbranch_execz .LBB0_482
	s_and_saveexec_b64 s[0:1], s[4:5]
	s_xor_b64 s[64:65], exec, s[0:1]
	s_cbranch_execz .LBB0_479
	v_mul_f32_e32 v155, 0xbfb8aa3b, v126
	v_exp_f32_e32 v155, v155
	v_mul_f32_e32 v163, 0xbfb8aa3b, v122
	v_exp_f32_e32 v163, v163
	v_mul_f32_e32 v165, 0xbfb8aa3b, v114
	v_add_f32_e32 v155, 1.0, v155
	v_rcp_f32_e32 v168, v155
	v_add_f32_e32 v155, 1.0, v163
	v_rcp_f32_e32 v170, v155
	v_mul_f32_e32 v155, 0xbfb8aa3b, v127
	v_exp_f32_e32 v155, v155
	v_mul_f32_e32 v163, 0xbfb8aa3b, v123
	v_exp_f32_e32 v163, v163
	v_mul_f32_e32 v164, 0xbfb8aa3b, v118
	v_exp_f32_e32 v166, v165
	v_mul_f32_e32 v165, 0xbfb8aa3b, v119
	v_exp_f32_e32 v164, v164
	v_exp_f32_e32 v165, v165
	v_mul_f32_e32 v167, 0xbfb8aa3b, v115
	v_add_f32_e32 v155, 1.0, v155
	v_rcp_f32_e32 v169, v155
	v_exp_f32_e32 v167, v167
	v_add_f32_e32 v163, 1.0, v163
	v_rcp_f32_e32 v171, v163
	v_pk_add_f32 v[164:165], v[164:165], 1.0 op_sel_hi:[1,0]
	v_mul_f32_e32 v178, 0xbfb8aa3b, v117
	v_rcp_f32_e32 v155, v164
	v_pk_mul_f32 v[168:169], v[168:169], v[164:165]
	v_rcp_f32_e32 v163, v165
	v_pk_add_f32 v[164:165], v[166:167], 1.0 op_sel_hi:[1,0]
	s_nop 0
	v_rcp_f32_e32 v176, v164
	v_pk_mul_f32 v[166:167], v[170:171], v[164:165]
	v_mul_f32_e32 v164, 0xbfb8aa3b, v128
	v_rcp_f32_e32 v177, v165
	v_exp_f32_e32 v165, v164
	v_mul_f32_e32 v164, 0xbfb8aa3b, v124
	v_exp_f32_e32 v171, v164
	v_mul_f32_e32 v164, 0xbfb8aa3b, v120
	v_add_f32_e32 v165, 1.0, v165
	v_rcp_f32_e32 v172, v165
	v_add_f32_e32 v165, 1.0, v171
	v_rcp_f32_e32 v174, v165
	v_mul_f32_e32 v165, 0xbfb8aa3b, v129
	v_exp_f32_e32 v171, v165
	v_mul_f32_e32 v165, 0xbfb8aa3b, v125
	v_exp_f32_e32 v175, v165
	v_mul_f32_e32 v165, 0xbfb8aa3b, v121
	v_exp_f32_e32 v164, v164
	v_exp_f32_e32 v165, v165
	v_add_f32_e32 v171, 1.0, v171
	v_rcp_f32_e32 v173, v171
	v_mul_f32_e32 v170, 0xbfb8aa3b, v116
	v_exp_f32_e32 v170, v170
	v_exp_f32_e32 v171, v178
	v_pk_add_f32 v[164:165], v[164:165], 1.0 op_sel_hi:[1,0]
	v_cvt_pk_bf16_f32 v166, v166, v167
	v_rcp_f32_e32 v178, v164
	v_pk_mul_f32 v[172:173], v[172:173], v[164:165]
	v_add_f32_e32 v164, 1.0, v175
	v_rcp_f32_e32 v175, v164
	v_rcp_f32_e32 v179, v165
	v_pk_add_f32 v[164:165], v[170:171], 1.0 op_sel_hi:[1,0]
	s_nop 0
	v_rcp_f32_e32 v180, v164
	v_rcp_f32_e32 v181, v165
	v_pk_mul_f32 v[170:171], v[174:175], v[164:165]
	v_lshl_add_u64 v[174:175], v[140:141], 0, v[156:157]
	v_cvt_pk_bf16_f32 v164, v168, v169
	v_cvt_pk_bf16_f32 v165, v172, v173
	v_cvt_pk_bf16_f32 v167, v170, v171
	v_add_co_u32_e32 v168, vcc, 0x10000, v174
	global_store_dwordx4 v[174:175], v[164:167], off
	s_nop 0
	v_addc_co_u32_e32 v169, vcc, 0, v175, vcc
	v_cvt_pk_bf16_f32 v164, v155, v163
	v_cvt_pk_bf16_f32 v165, v178, v179
	v_cvt_pk_bf16_f32 v166, v176, v177
	v_cvt_pk_bf16_f32 v167, v180, v181
	global_store_dwordx4 v[168:169], v[164:167], off

.LBB0_899:
	s_mov_b64 s[0:1], s[10:11]
	s_load_dword s0, s[0:1], 0x110
	s_waitcnt lgkmcnt(0)
	s_cmp_gt_i32 s0, s68
	s_cbranch_scc1 .LBB0_957
	s_mov_b64 s[0:1], s[10:11]
	s_load_dword s0, s[0:1], 0x114
	s_waitcnt lgkmcnt(0)
	s_cmp_ge_i32 s68, s0
	s_cbranch_scc1 .LBB0_956
	v_readlane_b32 s0, v254, 2
	v_readlane_b32 s1, v254, 3
	s_load_dword s1, s[0:1], 0x110
	s_add_i32 s0, s41, 2
	s_waitcnt lgkmcnt(0)
	s_cmp_gt_i32 s1, s0
	s_cbranch_scc1 .LBB0_956
	v_readlane_b32 s2, v254, 2
	v_readlane_b32 s3, v254, 3
	s_load_dword s1, s[2:3], 0x114
	s_waitcnt lgkmcnt(0)
	s_cmp_ge_i32 s0, s1
	s_cbranch_scc1 .LBB0_956
	v_readlane_b32 s6, v254, 2
	v_mov_b32_e32 v1, v0
	v_readlane_b32 s7, v254, 3
	s_load_dword s0, s[6:7], 0x118
	v_readlane_b32 s1, v254, 0
	s_waitcnt lgkmcnt(0)
	s_setprio 0
	s_getreg_b32 s0, hwreg(HW_REG_XCC_ID, 0, 4)
	s_waitcnt vmcnt(0)
	s_barrier
	s_mov_b64 s[4:5], exec
	v_readlane_b32 s2, v254, 6
	v_readlane_b32 s3, v254, 7
	s_and_b64 s[2:3], s[4:5], s[2:3]
	s_mov_b64 exec, s[2:3]
	s_cbranch_execz .LBB0_955
	s_add_i32 s3, 0, 0x26000
	v_mov_b32_e32 v1, s3
	s_load_dwordx2 s[6:7], s[6:7], 0x108
	s_waitcnt vmcnt(0) expcnt(0) lgkmcnt(0)
	ds_read_b32 v3, v1
	v_readlane_b32 s1, v254, 8
	s_and_b32 s2, s0, 15
	s_waitcnt lgkmcnt(0)
	v_cmp_ne_u32_e32 vcc, 0, v3
	v_mov_b32_e32 v1, s1
	ds_read_b32 v2, v1
	s_cbranch_vccnz .LBB0_919
	v_readlane_b32 s8, v254, 4
	v_readlane_b32 s12, v254, 2
	v_readlane_b32 s9, v254, 5
	v_readlane_b32 s13, v254, 3
	s_load_dwordx2 s[0:1], s[8:9], 0x4
	s_nop 0
	s_load_dword s12, s[12:13], 0x118
	s_add_u32 s8, s6, 0x4200
	s_addc_u32 s9, s7, 0
	s_add_u32 s10, s6, 0x4400
	s_addc_u32 s11, s7, 0
	s_waitcnt lgkmcnt(0)
	s_mul_i32 s34, s0, s12
	s_add_u32 s12, s6, 0x4500
	s_addc_u32 s13, s7, 0
	s_add_u32 s14, s6, 0x4600
	s_addc_u32 s15, s7, 0
	s_add_u32 s16, s6, 0x4700
	s_addc_u32 s17, s7, 0
	s_add_u32 s18, s6, 0x4800
	s_addc_u32 s19, s7, 0
	s_add_u32 s20, s6, 0x4900
	s_addc_u32 s21, s7, 0
	s_add_u32 s22, s6, 0x4a00
	s_addc_u32 s23, s7, 0
	s_add_u32 s24, s6, 0x4b00
	s_addc_u32 s25, s7, 0
	s_add_u32 s26, s6, 0x4c00
	s_addc_u32 s27, s7, 0
	s_add_u32 s28, s6, 0x4d00
	s_addc_u32 s29, s7, 0
	s_add_u32 s30, s6, 0x4e00
	s_addc_u32 s31, s7, 0
	s_add_u32 s64, s6, 0x4f00
	s_addc_u32 s65, s7, 0
	s_add_u32 s66, s6, 0x5000
	s_addc_u32 s67, s7, 0
	s_add_u32 s68, s6, 0x5100
	s_addc_u32 s69, s7, 0
	s_add_u32 s70, s6, 0x5200
	s_addc_u32 s71, s7, 0
	s_add_u32 s72, s6, 0x5300
	s_mul_i32 s34, s34, s1
	s_addc_u32 s73, s7, 0
	s_mov_b32 s0, 1
	s_branch .LBB0_907

.LBB0_1042:
	s_mov_b64 s[0:1], s[18:19]
	s_load_dword s0, s[0:1], 0x110
	s_waitcnt lgkmcnt(0)
	s_cmp_gt_i32 s0, s89
	s_cbranch_scc1 .LBB0_1100
	s_mov_b64 s[0:1], s[18:19]
	s_load_dword s0, s[0:1], 0x114
	s_waitcnt lgkmcnt(0)
	s_cmp_ge_i32 s89, s0
	s_cbranch_scc1 .LBB0_1099
	v_readlane_b32 s0, v254, 2
	v_readlane_b32 s1, v254, 3
	s_load_dword s1, s[0:1], 0x110
	s_add_i32 s0, s41, 3
	s_waitcnt lgkmcnt(0)
	s_cmp_gt_i32 s1, s0
	s_cbranch_scc1 .LBB0_1099
	v_readlane_b32 s2, v254, 2
	v_readlane_b32 s3, v254, 3
	s_load_dword s1, s[2:3], 0x114
	s_waitcnt lgkmcnt(0)
	s_cmp_ge_i32 s0, s1
	s_cbranch_scc1 .LBB0_1099
	v_readlane_b32 s6, v254, 2
	v_mov_b32_e32 v1, v0
	v_readlane_b32 s7, v254, 3
	s_load_dword s0, s[6:7], 0x118
	v_readlane_b32 s1, v254, 0
	s_waitcnt lgkmcnt(0)
	s_setprio 0
	s_getreg_b32 s0, hwreg(HW_REG_XCC_ID, 0, 4)
	s_waitcnt vmcnt(0)
	s_barrier
	s_mov_b64 s[4:5], exec
	v_readlane_b32 s2, v254, 6
	v_readlane_b32 s3, v254, 7
	s_and_b64 s[2:3], s[4:5], s[2:3]
	s_mov_b64 exec, s[2:3]
	s_cbranch_execz .LBB0_1098
	s_add_i32 s3, 0, 0x26000
	v_mov_b32_e32 v1, s3
	s_load_dwordx2 s[6:7], s[6:7], 0x108
	s_waitcnt vmcnt(0) expcnt(0) lgkmcnt(0)
	ds_read_b32 v3, v1
	v_readlane_b32 s1, v254, 8
	s_and_b32 s2, s0, 15
	s_waitcnt lgkmcnt(0)
	v_cmp_ne_u32_e32 vcc, 0, v3
	v_mov_b32_e32 v1, s1
	ds_read_b32 v2, v1
	s_cbranch_vccnz .LBB0_1062
	v_readlane_b32 s8, v254, 4
	v_readlane_b32 s12, v254, 2
	v_readlane_b32 s9, v254, 5
	v_readlane_b32 s13, v254, 3
	s_load_dwordx2 s[0:1], s[8:9], 0x4
	s_nop 0
	s_load_dword s12, s[12:13], 0x118
	s_add_u32 s8, s6, 0x4200
	s_addc_u32 s9, s7, 0
	s_add_u32 s10, s6, 0x4400
	s_addc_u32 s11, s7, 0
	s_waitcnt lgkmcnt(0)
	s_mul_i32 s34, s0, s12
	s_add_u32 s12, s6, 0x4500
	s_addc_u32 s13, s7, 0
	s_add_u32 s14, s6, 0x4600
	s_addc_u32 s15, s7, 0
	s_add_u32 s16, s6, 0x4700
	s_addc_u32 s17, s7, 0
	s_add_u32 s18, s6, 0x4800
	s_addc_u32 s19, s7, 0
	s_add_u32 s20, s6, 0x4900
	s_addc_u32 s21, s7, 0
	s_add_u32 s22, s6, 0x4a00
	s_addc_u32 s23, s7, 0
	s_add_u32 s24, s6, 0x4b00
	s_addc_u32 s25, s7, 0
	s_add_u32 s26, s6, 0x4c00
	s_addc_u32 s27, s7, 0
	s_add_u32 s28, s6, 0x4d00
	s_addc_u32 s29, s7, 0
	s_add_u32 s30, s6, 0x4e00
	s_addc_u32 s31, s7, 0
	s_add_u32 s64, s6, 0x4f00
	s_addc_u32 s65, s7, 0
	s_add_u32 s66, s6, 0x5000
	s_addc_u32 s67, s7, 0
	s_add_u32 s68, s6, 0x5100
	s_addc_u32 s69, s7, 0
	s_add_u32 s70, s6, 0x5200
	s_addc_u32 s71, s7, 0
	s_add_u32 s72, s6, 0x5300
	s_mul_i32 s34, s34, s1
	s_addc_u32 s73, s7, 0
	s_mov_b32 s0, 1
	s_branch .LBB0_1050

.LBB0_1191:
	s_mov_b64 s[0:1], s[4:5]
	s_load_dword s0, s[0:1], 0x110
	s_waitcnt lgkmcnt(0)
	s_cmp_gt_i32 s0, s2
	s_cbranch_scc1 .LBB0_1249
	s_mov_b64 s[0:1], s[4:5]
	s_load_dword s0, s[0:1], 0x114
	s_waitcnt lgkmcnt(0)
	s_cmp_ge_i32 s2, s0
	s_cbranch_scc1 .LBB0_1248
	v_readlane_b32 s0, v254, 2
	v_readlane_b32 s1, v254, 3
	s_load_dword s1, s[0:1], 0x110
	s_add_i32 s0, s41, 4
	s_waitcnt lgkmcnt(0)
	s_cmp_gt_i32 s1, s0
	s_cbranch_scc1 .LBB0_1248
	v_readlane_b32 s2, v254, 2
	v_readlane_b32 s3, v254, 3
	s_load_dword s1, s[2:3], 0x114
	s_waitcnt lgkmcnt(0)
	s_cmp_ge_i32 s0, s1
	s_cbranch_scc1 .LBB0_1248
	v_readlane_b32 s6, v254, 2
	v_mov_b32_e32 v1, v0
	v_readlane_b32 s7, v254, 3
	s_load_dword s0, s[6:7], 0x118
	v_readlane_b32 s1, v254, 0
	s_waitcnt lgkmcnt(0)
	s_setprio 0
	s_getreg_b32 s0, hwreg(HW_REG_XCC_ID, 0, 4)
	s_waitcnt vmcnt(0)
	s_barrier
	s_mov_b64 s[4:5], exec
	v_readlane_b32 s2, v254, 6
	v_readlane_b32 s3, v254, 7
	s_and_b64 s[2:3], s[4:5], s[2:3]
	s_mov_b64 exec, s[2:3]
	s_cbranch_execz .LBB0_1247
	s_add_i32 s3, 0, 0x26000
	v_mov_b32_e32 v1, s3
	s_load_dwordx2 s[6:7], s[6:7], 0x108
	s_waitcnt vmcnt(0) expcnt(0) lgkmcnt(0)
	ds_read_b32 v3, v1
	v_readlane_b32 s1, v254, 8
	s_and_b32 s2, s0, 15
	s_waitcnt lgkmcnt(0)
	v_cmp_ne_u32_e32 vcc, 0, v3
	v_mov_b32_e32 v1, s1
	ds_read_b32 v2, v1
	s_cbranch_vccnz .LBB0_1211
	v_readlane_b32 s8, v254, 4
	v_readlane_b32 s12, v254, 2
	v_readlane_b32 s9, v254, 5
	v_readlane_b32 s13, v254, 3
	s_load_dwordx2 s[0:1], s[8:9], 0x4
	s_nop 0
	s_load_dword s12, s[12:13], 0x118
	s_add_u32 s8, s6, 0x4200
	s_addc_u32 s9, s7, 0
	s_add_u32 s10, s6, 0x4400
	s_addc_u32 s11, s7, 0
	s_waitcnt lgkmcnt(0)
	s_mul_i32 s34, s0, s12
	s_add_u32 s12, s6, 0x4500
	s_addc_u32 s13, s7, 0
	s_add_u32 s14, s6, 0x4600
	s_addc_u32 s15, s7, 0
	s_add_u32 s16, s6, 0x4700
	s_addc_u32 s17, s7, 0
	s_add_u32 s18, s6, 0x4800
	s_addc_u32 s19, s7, 0
	s_add_u32 s20, s6, 0x4900
	s_addc_u32 s21, s7, 0
	s_add_u32 s22, s6, 0x4a00
	s_addc_u32 s23, s7, 0
	s_add_u32 s24, s6, 0x4b00
	s_addc_u32 s25, s7, 0
	s_add_u32 s26, s6, 0x4c00
	s_addc_u32 s27, s7, 0
	s_add_u32 s28, s6, 0x4d00
	s_addc_u32 s29, s7, 0
	s_add_u32 s30, s6, 0x4e00
	s_addc_u32 s31, s7, 0
	s_add_u32 s64, s6, 0x4f00
	s_addc_u32 s65, s7, 0
	s_add_u32 s66, s6, 0x5000
	s_addc_u32 s67, s7, 0
	s_add_u32 s68, s6, 0x5100
	s_addc_u32 s69, s7, 0
	s_add_u32 s70, s6, 0x5200
	s_addc_u32 s71, s7, 0
	s_add_u32 s72, s6, 0x5300
	s_mul_i32 s34, s34, s1
	s_addc_u32 s73, s7, 0
	s_mov_b32 s0, 1
	s_branch .LBB0_1199

.LBB0_1259:
	s_mov_b64 s[0:1], s[4:5]
	s_load_dword s0, s[0:1], 0x110
	s_waitcnt lgkmcnt(0)
	s_cmp_gt_i32 s0, s2
	s_cbranch_scc1 .LBB0_1317
	s_mov_b64 s[0:1], s[4:5]
	s_load_dword s0, s[0:1], 0x114
	s_waitcnt lgkmcnt(0)
	s_cmp_ge_i32 s2, s0
	s_cbranch_scc1 .LBB0_1316
	v_readlane_b32 s0, v254, 2
	v_readlane_b32 s1, v254, 3
	s_load_dword s1, s[0:1], 0x110
	s_add_i32 s0, s41, 5
	s_waitcnt lgkmcnt(0)
	s_cmp_gt_i32 s1, s0
	s_cbranch_scc1 .LBB0_1316
	v_readlane_b32 s2, v254, 2
	v_readlane_b32 s3, v254, 3
	s_load_dword s1, s[2:3], 0x114
	s_waitcnt lgkmcnt(0)
	s_cmp_ge_i32 s0, s1
	s_cbranch_scc1 .LBB0_1316
	v_readlane_b32 s6, v254, 2
	v_mov_b32_e32 v1, v0
	v_readlane_b32 s7, v254, 3
	s_load_dword s0, s[6:7], 0x118
	v_readlane_b32 s1, v254, 0
	s_waitcnt lgkmcnt(0)
	s_setprio 0
	s_getreg_b32 s0, hwreg(HW_REG_XCC_ID, 0, 4)
	s_waitcnt vmcnt(0)
	s_barrier
	s_mov_b64 s[4:5], exec
	v_readlane_b32 s2, v254, 6
	v_readlane_b32 s3, v254, 7
	s_and_b64 s[2:3], s[4:5], s[2:3]
	s_mov_b64 exec, s[2:3]
	s_cbranch_execz .LBB0_1315
	s_add_i32 s3, 0, 0x26000
	v_mov_b32_e32 v1, s3
	s_load_dwordx2 s[6:7], s[6:7], 0x108
	s_waitcnt vmcnt(0) expcnt(0) lgkmcnt(0)
	ds_read_b32 v3, v1
	v_readlane_b32 s1, v254, 8
	s_and_b32 s2, s0, 15
	s_waitcnt lgkmcnt(0)
	v_cmp_ne_u32_e32 vcc, 0, v3
	v_mov_b32_e32 v1, s1
	ds_read_b32 v2, v1
	s_cbranch_vccnz .LBB0_1279
	v_readlane_b32 s8, v254, 4
	v_readlane_b32 s12, v254, 2
	v_readlane_b32 s9, v254, 5
	v_readlane_b32 s13, v254, 3
	s_load_dwordx2 s[0:1], s[8:9], 0x4
	s_nop 0
	s_load_dword s12, s[12:13], 0x118
	s_add_u32 s8, s6, 0x4200
	s_addc_u32 s9, s7, 0
	s_add_u32 s10, s6, 0x4400
	s_addc_u32 s11, s7, 0
	s_waitcnt lgkmcnt(0)
	s_mul_i32 s34, s0, s12
	s_add_u32 s12, s6, 0x4500
	s_addc_u32 s13, s7, 0
	s_add_u32 s14, s6, 0x4600
	s_addc_u32 s15, s7, 0
	s_add_u32 s16, s6, 0x4700
	s_addc_u32 s17, s7, 0
	s_add_u32 s18, s6, 0x4800
	s_addc_u32 s19, s7, 0
	s_add_u32 s20, s6, 0x4900
	s_addc_u32 s21, s7, 0
	s_add_u32 s22, s6, 0x4a00
	s_addc_u32 s23, s7, 0
	s_add_u32 s24, s6, 0x4b00
	s_addc_u32 s25, s7, 0
	s_add_u32 s26, s6, 0x4c00
	s_addc_u32 s27, s7, 0
	s_add_u32 s28, s6, 0x4d00
	s_addc_u32 s29, s7, 0
	s_add_u32 s30, s6, 0x4e00
	s_addc_u32 s31, s7, 0
	s_add_u32 s64, s6, 0x4f00
	s_addc_u32 s65, s7, 0
	s_add_u32 s66, s6, 0x5000
	s_addc_u32 s67, s7, 0
	s_add_u32 s68, s6, 0x5100
	s_addc_u32 s69, s7, 0
	s_add_u32 s70, s6, 0x5200
	s_addc_u32 s71, s7, 0
	s_add_u32 s72, s6, 0x5300
	s_mul_i32 s34, s34, s1
	s_addc_u32 s73, s7, 0
	s_mov_b32 s0, 1
	s_branch .LBB0_1267

.LBB0_1321:
	s_andn2_b64 vcc, exec, s[4:5]
	s_cbranch_vccnz .LBB0_1341
	v_lshlrev_b32_e32 v1, 4, v13
	v_add_u32_e32 v2, 0x2000, v1
	v_ashrrev_i32_e32 v3, 31, v2
	v_lshrrev_b32_e32 v3, 22, v3
	v_add_u32_e32 v3, v2, v3
	s_waitcnt vmcnt(1)
	v_ashrrev_i32_e32 v10, 10, v3
	v_mul_i32_i24_e32 v3, 0x400, v10
	v_sub_u32_e32 v2, v2, v3
	v_lshrrev_b32_e32 v3, 4, v2
	v_bitop3_b32 v2, v3, v2, 32 bitop3:0x6c
	v_ashrrev_i32_e32 v3, 31, v2
	v_lshrrev_b32_e32 v3, 26, v3
	s_lshl_b32 s1, s7, 10
	v_add_u32_e32 v3, v2, v3
	v_lshlrev_b32_e32 v4, 3, v10
	s_add_u32 s1, s10, s1
	v_ashrrev_i32_e32 v11, 6, v3
	v_and_b32_e32 v4, -16, v4
	s_addc_u32 s4, s11, 0
	v_add_u32_e32 v4, v11, v4
	s_add_u32 s40, s1, 0x2b800000
	v_and_b32_e32 v5, 3, v11
	s_mov_b32 s1, 0x3fffe0
	v_lshrrev_b32_e32 v6, 2, v4
	v_lshlrev_b32_e32 v7, 1, v4
	v_and_b32_e32 v3, 0xc0, v3
	v_and_or_b32 v5, v4, s1, v5
	v_and_b32_e32 v6, 4, v6
	v_and_b32_e32 v7, 24, v7
	v_sub_u32_e32 v2, v2, v3
	v_or3_b32 v5, v5, v6, v7
	v_lshlrev_b32_e32 v6, 5, v10
	v_ashrrev_i16_sdwa v2, v226, sext(v2) dst_sel:DWORD dst_unused:UNUSED_PAD src0_sel:DWORD src1_sel:BYTE_0
	v_and_b32_e32 v6, 32, v6
	v_bfe_i32 v12, v2, 0, 16
	v_add_lshl_u32 v2, v6, v12, 1
	v_lshl_add_u32 v198, v5, 10, v2
	v_lshl_add_u32 v200, v4, 10, v2
	v_bfe_i32 v2, v13, 27, 1
	v_lshrrev_b32_e32 v2, 22, v2
	v_add_u32_e32 v2, v1, v2
	v_and_b32_e32 v2, 0xfffffc00, v2
	v_sub_u32_e32 v1, v1, v2
	v_lshrrev_b32_e32 v2, 4, v1
	v_ashrrev_i32_e32 v3, 31, v13
	v_bitop3_b32 v1, v2, v1, 32 bitop3:0x6c
	v_lshrrev_b32_e32 v3, 26, v3
	v_ashrrev_i32_e32 v2, 31, v1
	v_add_u32_e32 v3, v13, v3
	v_lshrrev_b32_e32 v2, 26, v2
	v_ashrrev_i32_e32 v15, 6, v3
	s_addc_u32 s43, s4, 0
	v_add_u32_e32 v2, v1, v2
	v_lshlrev_b32_e32 v3, 3, v15
	s_ashr_i32 s68, s34, 31
	s_lshr_b32 s65, s0, 8
	v_ashrrev_i32_e32 v14, 6, v2
	v_and_b32_e32 v3, -16, v3
	s_lshr_b32 s67, s0, 9
	s_lshr_b32 s0, s68, 29
	v_add_u32_e32 v3, v14, v3
	v_and_b32_e32 v4, 3, v14
	s_add_i32 s0, s34, s0
	s_ashr_i32 s5, s35, 6
	v_and_or_b32 v4, v3, s1, v4
	s_ashr_i32 s1, s0, 3
	s_and_b32 s0, s0, -8
	s_ashr_i32 s6, s35, 8
	s_lshl_b32 s66, s5, 10
	s_sub_i32 s0, s34, s0
	s_or_b32 s69, s67, 1
	s_cmp_lt_i32 s0, 0
	s_cselect_b32 s4, s69, s67
	s_mul_i32 s0, s4, s0
	s_add_i32 s0, s0, s1
	s_ashr_i32 s1, s0, 31
	s_lshr_b32 s1, s1, 27
	s_add_i32 s1, s0, s1
	v_lshrrev_b32_e32 v5, 2, v3
	v_lshlrev_b32_e32 v6, 1, v3
	v_and_b32_e32 v2, 0xc0, v2
	s_ashr_i32 s4, s1, 5
	v_and_b32_e32 v5, 4, v5
	v_and_b32_e32 v6, 24, v6
	v_sub_u32_e32 v1, v1, v2
	s_lshl_b32 s14, s4, 3
	v_or3_b32 v4, v4, v5, v6
	v_lshlrev_b32_e32 v5, 5, v15
	v_ashrrev_i16_sdwa v1, v226, sext(v1) dst_sel:DWORD dst_unused:UNUSED_PAD src0_sel:DWORD src1_sel:BYTE_0
	s_sub_i32 s4, s65, s14
	v_and_b32_e32 v5, 32, v5
	v_bfe_i32 v16, v1, 0, 16
	s_min_i32 s15, s4, 8
	v_add_lshl_u32 v1, v5, v16, 1
	s_sext_i32_i8 s4, s15
	v_lshl_add_u32 v202, v4, 10, v1
	v_lshl_add_u32 v204, v3, 10, v1
	v_cvt_f32_i32_e32 v1, s4
	s_andn2_b32 s1, s1, 31
	s_sub_i32 s16, s0, s1
	v_cvt_f32_i32_e32 v2, s16
	v_rcp_iflag_f32_e32 v3, v1
	s_xor_b32 s0, s16, s4
	s_ashr_i32 s0, s0, 30
	s_or_b32 s4, s0, 1
	v_mul_f32_e32 v3, v2, v3
	v_trunc_f32_e32 v3, v3
	v_fma_f32 v2, -v3, v1, v2
	v_cvt_i32_f32_e32 v3, v3
	v_cmp_ge_f32_e64 s[0:1], |v2|, |v1|
	s_and_b64 s[0:1], s[0:1], exec
	s_cselect_b32 s0, s4, 0
	v_readfirstlane_b32 s1, v3
	s_add_i32 s4, s1, s0
	s_mul_i32 s0, s4, s15
	s_sub_i32 s0, s16, s0
	s_sext_i32_i8 s0, s0
	s_add_i32 s26, s14, s0
	s_ashr_i32 s27, s26, 31
	s_bfe_i64 s[14:15], s[4:5], 0x80000
	s_lshl_b64 s[0:1], s[26:27], 18
	s_lshl_b64 s[14:15], s[14:15], 18
	s_add_u32 s28, s18, s14
	s_addc_u32 s29, s19, s15
	s_add_i32 s70, s66, 0
	s_add_i32 m0, s70, 0x10000
	v_mov_b32_e32 v203, v195
	global_load_lds_dwordx4 v202, s[28:29]
	s_add_i32 m0, s70, 0x12000
	s_add_u32 s30, s40, s0
	global_load_lds_dwordx4 v198, s[28:29]
	s_addc_u32 s31, s43, s1
	s_mov_b32 m0, s70
	s_add_i32 s71, s70, 0x2000
	global_load_lds_dwordx4 v204, s[30:31]
	s_mov_b32 m0, s71
	s_add_u32 s0, s28, 0x20000
	global_load_lds_dwordx4 v200, s[30:31]
	s_addc_u32 s1, s29, 0
	s_add_i32 m0, s70, 0x14000
	v_mov_b32_e32 v199, v195
	global_load_lds_dwordx4 v202, s[0:1]
	s_add_i32 m0, s70, 0x16000
	v_mov_b32_e32 v205, v195
	global_load_lds_dwordx4 v198, s[0:1]
	s_add_u32 s0, s30, 0x20000
	s_addc_u32 s1, s31, 0
	s_add_i32 s72, s70, 0x4000
	s_mov_b32 m0, s72
	s_add_i32 s73, s70, 0x6000
	global_load_lds_dwordx4 v204, s[0:1]
	s_mov_b32 m0, s73
	v_mov_b32_e32 v201, v195
	global_load_lds_dwordx4 v200, s[0:1]
	s_waitcnt vmcnt(0)
	v_lshl_add_u64 v[8:9], s[28:29], 0, v[202:203]
	v_lshl_add_u64 v[6:7], s[28:29], 0, v[198:199]
	v_lshl_add_u64 v[4:5], s[30:31], 0, v[204:205]
	s_cmp_lg_u32 s6, 1
	v_lshl_add_u64 v[2:3], s[30:31], 0, v[200:201]
	s_setprio 1
	s_cbranch_scc1 .LBB0_1324
	s_barrier
	s_setprio 0

.LBB0_1332:
	s_add_u32 s0, s6, 0xfffe0080
	s_addc_u32 s1, s7, -1
	s_add_i32 s33, 0, 0x10000
	v_add_u32_e32 v142, s33, v237
	ds_read_b128 v[130:133], v142
	ds_read_b128 v[134:137], v142 offset:1024
	ds_read_b128 v[138:141], v142 offset:2048
	ds_read_b128 v[142:145], v142 offset:3072
	s_cmp_eq_u32 s86, 4
	s_cselect_b32 s31, s23, s1
	s_cselect_b32 s30, s22, s0
	s_cselect_b32 s29, s15, s82
	s_cselect_b32 s28, s17, s21
	v_lshl_add_u64 v[178:179], s[6:7], 0, v[214:215]
	s_add_i32 m0, s70, 0xc000
	ds_read_b128 v[146:149], v240
	ds_read_b128 v[150:153], v240 offset:1024
	ds_read_b128 v[154:157], v240 offset:2048
	ds_read_b128 v[158:161], v240 offset:3072
	ds_read_b128 v[162:165], v240 offset:4096
	ds_read_b128 v[166:169], v240 offset:5120
	ds_read_b128 v[170:173], v240 offset:6144
	ds_read_b128 v[174:177], v240 offset:7168
	global_load_lds_dwordx4 v[178:179], off
	v_lshl_add_u64 v[178:179], s[6:7], 0, v[216:217]
	s_add_i32 m0, s70, 0xe000
	s_nop 0
	global_load_lds_dwordx4 v[178:179], off
	s_waitcnt lgkmcnt(8)
	s_barrier
	s_waitcnt lgkmcnt(0)
	s_waitcnt lgkmcnt(0)
	v_mfma_f32_16x16x32_bf16 v[62:65], v[130:133], v[146:149], v[62:65]
	v_mfma_f32_16x16x32_bf16 v[58:61], v[138:141], v[146:149], v[58:61]
	v_mfma_f32_16x16x32_bf16 v[54:57], v[130:133], v[154:157], v[54:57]
	v_mfma_f32_16x16x32_bf16 v[50:53], v[138:141], v[154:157], v[50:53]
	v_mfma_f32_16x16x32_bf16 v[46:49], v[130:133], v[162:165], v[46:49]
	v_mfma_f32_16x16x32_bf16 v[42:45], v[138:141], v[162:165], v[42:45]
	v_mfma_f32_16x16x32_bf16 v[38:41], v[130:133], v[170:173], v[38:41]
	v_mfma_f32_16x16x32_bf16 v[34:37], v[138:141], v[170:173], v[34:37]
	v_mfma_f32_16x16x32_bf16 v[62:65], v[134:137], v[150:153], v[62:65]
	v_mfma_f32_16x16x32_bf16 v[58:61], v[142:145], v[150:153], v[58:61]
	v_mfma_f32_16x16x32_bf16 v[54:57], v[134:137], v[158:161], v[54:57]
	v_mfma_f32_16x16x32_bf16 v[50:53], v[142:145], v[158:161], v[50:53]
	v_mfma_f32_16x16x32_bf16 v[46:49], v[134:137], v[166:169], v[46:49]
	v_mfma_f32_16x16x32_bf16 v[42:45], v[142:145], v[166:169], v[42:45]
	v_mfma_f32_16x16x32_bf16 v[38:41], v[134:137], v[174:177], v[38:41]
	v_mfma_f32_16x16x32_bf16 v[34:37], v[142:145], v[174:177], v[34:37]
	s_barrier
	s_add_i32 s36, 0, 0x14000
	s_add_i32 s0, s33, s66
	v_add_u32_e32 v190, s36, v237
	v_lshl_add_u64 v[218:219], s[28:29], 0, v[202:203]
	s_mov_b32 m0, s0
	ds_read_b128 v[178:181], v190
	ds_read_b128 v[182:185], v190 offset:1024
	ds_read_b128 v[186:189], v190 offset:2048
	ds_read_b128 v[190:193], v190 offset:3072
	global_load_lds_dwordx4 v[218:219], off
	v_lshl_add_u64 v[220:221], s[28:29], 0, v[198:199]
	s_add_i32 m0, s0, 0x2000
	s_nop 0
	global_load_lds_dwordx4 v[220:221], off
	s_barrier
	s_waitcnt lgkmcnt(0)
	s_waitcnt lgkmcnt(0)
	v_mfma_f32_16x16x32_bf16 v[30:33], v[178:181], v[146:149], v[30:33]
	v_mfma_f32_16x16x32_bf16 v[26:29], v[186:189], v[146:149], v[26:29]
	v_mfma_f32_16x16x32_bf16 v[22:25], v[178:181], v[154:157], v[22:25]
	v_mfma_f32_16x16x32_bf16 v[18:21], v[186:189], v[154:157], v[18:21]
	v_mfma_f32_16x16x32_bf16 v[14:17], v[178:181], v[162:165], v[14:17]
	v_mfma_f32_16x16x32_bf16 v[10:13], v[186:189], v[162:165], v[10:13]
	v_mfma_f32_16x16x32_bf16 v[6:9], v[178:181], v[170:173], v[6:9]
	v_mfma_f32_16x16x32_bf16 v[2:5], v[186:189], v[170:173], v[2:5]
	v_mfma_f32_16x16x32_bf16 v[30:33], v[182:185], v[150:153], v[30:33]
	v_mfma_f32_16x16x32_bf16 v[26:29], v[190:193], v[150:153], v[26:29]
	v_mfma_f32_16x16x32_bf16 v[22:25], v[182:185], v[158:161], v[22:25]
	v_mfma_f32_16x16x32_bf16 v[18:21], v[190:193], v[158:161], v[18:21]
	v_mfma_f32_16x16x32_bf16 v[14:17], v[182:185], v[166:169], v[14:17]
	v_mfma_f32_16x16x32_bf16 v[10:13], v[190:193], v[166:169], v[10:13]
	v_mfma_f32_16x16x32_bf16 v[6:9], v[182:185], v[174:177], v[6:9]
	v_mfma_f32_16x16x32_bf16 v[2:5], v[190:193], v[174:177], v[2:5]
	s_mov_b32 m0, s70
	v_lshl_add_u64 v[224:225], s[30:31], 0, v[204:205]
	s_barrier
	ds_read_b128 v[146:149], v240 offset:16384
	ds_read_b128 v[150:153], v240 offset:17408
	ds_read_b128 v[154:157], v240 offset:18432
	ds_read_b128 v[158:161], v240 offset:19456
	ds_read_b128 v[162:165], v240 offset:20480
	ds_read_b128 v[166:169], v240 offset:21504
	ds_read_b128 v[170:173], v240 offset:22528
	ds_read_b128 v[174:177], v240 offset:23552
	global_load_lds_dwordx4 v[224:225], off
	v_lshl_add_u64 v[230:231], s[30:31], 0, v[200:201]
	s_mov_b32 m0, s71
	s_nop 0
	global_load_lds_dwordx4 v[230:231], off
	s_barrier
	s_waitcnt lgkmcnt(0)
	s_waitcnt lgkmcnt(0)
	v_mfma_f32_16x16x32_bf16 v[66:69], v[130:133], v[146:149], v[66:69]
	v_mfma_f32_16x16x32_bf16 v[70:73], v[138:141], v[146:149], v[70:73]
	v_mfma_f32_16x16x32_bf16 v[74:77], v[130:133], v[154:157], v[74:77]
	v_mfma_f32_16x16x32_bf16 v[78:81], v[138:141], v[154:157], v[78:81]
	v_mfma_f32_16x16x32_bf16 v[82:85], v[130:133], v[162:165], v[82:85]
	v_mfma_f32_16x16x32_bf16 v[86:89], v[138:141], v[162:165], v[86:89]
	v_mfma_f32_16x16x32_bf16 v[90:93], v[130:133], v[170:173], v[90:93]
	v_mfma_f32_16x16x32_bf16 v[94:97], v[138:141], v[170:173], v[94:97]
	v_mfma_f32_16x16x32_bf16 v[66:69], v[134:137], v[150:153], v[66:69]
	v_mfma_f32_16x16x32_bf16 v[70:73], v[142:145], v[150:153], v[70:73]
	v_mfma_f32_16x16x32_bf16 v[74:77], v[134:137], v[158:161], v[74:77]
	v_mfma_f32_16x16x32_bf16 v[78:81], v[142:145], v[158:161], v[78:81]
	v_mfma_f32_16x16x32_bf16 v[82:85], v[134:137], v[166:169], v[82:85]
	v_mfma_f32_16x16x32_bf16 v[86:89], v[142:145], v[166:169], v[86:89]
	v_mfma_f32_16x16x32_bf16 v[90:93], v[134:137], v[174:177], v[90:93]
	v_mfma_f32_16x16x32_bf16 v[94:97], v[142:145], v[174:177], v[94:97]
	s_barrier
	s_add_u32 s0, s28, 0x20000
	s_addc_u32 s1, s29, 0
	s_add_i32 s33, s36, s66
	v_lshl_add_u64 v[130:131], s[0:1], 0, v[202:203]
	s_mov_b32 m0, s33
	s_nop 0
	global_load_lds_dwordx4 v[130:131], off
	v_lshl_add_u64 v[130:131], s[0:1], 0, v[198:199]
	s_add_i32 m0, s33, 0x2000
	s_nop 0
	global_load_lds_dwordx4 v[130:131], off
	s_waitcnt vmcnt(6)
	s_barrier
	v_mfma_f32_16x16x32_bf16 v[98:101], v[178:181], v[146:149], v[98:101]
	v_mfma_f32_16x16x32_bf16 v[102:105], v[186:189], v[146:149], v[102:105]
	v_mfma_f32_16x16x32_bf16 v[106:109], v[178:181], v[154:157], v[106:109]
	v_mfma_f32_16x16x32_bf16 v[110:113], v[186:189], v[154:157], v[110:113]
	v_mfma_f32_16x16x32_bf16 v[114:117], v[178:181], v[162:165], v[114:117]
	v_mfma_f32_16x16x32_bf16 v[118:121], v[186:189], v[162:165], v[118:121]
	v_mfma_f32_16x16x32_bf16 v[122:125], v[178:181], v[170:173], v[122:125]
	v_mfma_f32_16x16x32_bf16 v[126:129], v[186:189], v[170:173], v[126:129]
	v_mfma_f32_16x16x32_bf16 v[98:101], v[182:185], v[150:153], v[98:101]
	v_mfma_f32_16x16x32_bf16 v[102:105], v[190:193], v[150:153], v[102:105]
	v_mfma_f32_16x16x32_bf16 v[106:109], v[182:185], v[158:161], v[106:109]
	v_mfma_f32_16x16x32_bf16 v[110:113], v[190:193], v[158:161], v[110:113]
	v_mfma_f32_16x16x32_bf16 v[114:117], v[182:185], v[166:169], v[114:117]
	v_mfma_f32_16x16x32_bf16 v[118:121], v[190:193], v[166:169], v[118:121]
	v_mfma_f32_16x16x32_bf16 v[122:125], v[182:185], v[174:177], v[122:125]
	v_mfma_f32_16x16x32_bf16 v[126:129], v[190:193], v[174:177], v[126:129]
	s_add_i32 s33, 0, 0x18000
	v_add_u32_e32 v142, s33, v237
	s_barrier
	ds_read_b128 v[130:133], v142
	ds_read_b128 v[134:137], v142 offset:1024
	ds_read_b128 v[138:141], v142 offset:2048
	ds_read_b128 v[142:145], v142 offset:3072
	s_add_u32 s0, s30, 0x20000
	s_addc_u32 s1, s31, 0
	s_mov_b32 m0, s72
	v_lshl_add_u64 v[178:179], s[0:1], 0, v[204:205]
	ds_read_b128 v[146:149], v240 offset:32768
	ds_read_b128 v[150:153], v240 offset:33792
	ds_read_b128 v[154:157], v240 offset:34816
	ds_read_b128 v[158:161], v240 offset:35840
	ds_read_b128 v[162:165], v240 offset:36864
	ds_read_b128 v[166:169], v240 offset:37888
	ds_read_b128 v[170:173], v240 offset:38912
	ds_read_b128 v[174:177], v240 offset:39936
	global_load_lds_dwordx4 v[178:179], off
	v_lshl_add_u64 v[178:179], s[0:1], 0, v[200:201]
	s_mov_b32 m0, s73
	s_nop 0
	global_load_lds_dwordx4 v[178:179], off
	s_waitcnt lgkmcnt(8)
	s_barrier
	s_waitcnt lgkmcnt(0)
	s_waitcnt lgkmcnt(0)
	v_mfma_f32_16x16x32_bf16 v[62:65], v[130:133], v[146:149], v[62:65]
	v_mfma_f32_16x16x32_bf16 v[58:61], v[138:141], v[146:149], v[58:61]
	v_mfma_f32_16x16x32_bf16 v[54:57], v[130:133], v[154:157], v[54:57]
	v_mfma_f32_16x16x32_bf16 v[50:53], v[138:141], v[154:157], v[50:53]
	v_mfma_f32_16x16x32_bf16 v[46:49], v[130:133], v[162:165], v[46:49]
	v_mfma_f32_16x16x32_bf16 v[42:45], v[138:141], v[162:165], v[42:45]
	v_mfma_f32_16x16x32_bf16 v[38:41], v[130:133], v[170:173], v[38:41]
	v_mfma_f32_16x16x32_bf16 v[34:37], v[138:141], v[170:173], v[34:37]
	v_mfma_f32_16x16x32_bf16 v[62:65], v[134:137], v[150:153], v[62:65]
	v_mfma_f32_16x16x32_bf16 v[58:61], v[142:145], v[150:153], v[58:61]
	v_mfma_f32_16x16x32_bf16 v[54:57], v[134:137], v[158:161], v[54:57]
	v_mfma_f32_16x16x32_bf16 v[50:53], v[142:145], v[158:161], v[50:53]
	v_mfma_f32_16x16x32_bf16 v[46:49], v[134:137], v[166:169], v[46:49]
	v_mfma_f32_16x16x32_bf16 v[42:45], v[142:145], v[166:169], v[42:45]
	v_mfma_f32_16x16x32_bf16 v[38:41], v[134:137], v[174:177], v[38:41]
	v_mfma_f32_16x16x32_bf16 v[34:37], v[142:145], v[174:177], v[34:37]
	s_barrier
	s_add_i32 s30, 0, 0x1c000
	s_add_i32 s0, s33, s66
	v_add_u32_e32 v190, s30, v237
	v_lshl_add_u64 v[218:219], v[218:219], 0, s[54:55]
	s_mov_b32 m0, s0
	ds_read_b128 v[178:181], v190
	ds_read_b128 v[182:185], v190 offset:1024
	ds_read_b128 v[186:189], v190 offset:2048
	ds_read_b128 v[190:193], v190 offset:3072
	global_load_lds_dwordx4 v[218:219], off
	v_lshl_add_u64 v[218:219], v[220:221], 0, s[54:55]
	s_add_i32 m0, s0, 0x2000
	s_nop 0
	global_load_lds_dwordx4 v[218:219], off
	s_barrier
	s_waitcnt lgkmcnt(0)
	s_waitcnt lgkmcnt(0)
	v_mfma_f32_16x16x32_bf16 v[30:33], v[178:181], v[146:149], v[30:33]
	v_mfma_f32_16x16x32_bf16 v[26:29], v[186:189], v[146:149], v[26:29]
	v_mfma_f32_16x16x32_bf16 v[22:25], v[178:181], v[154:157], v[22:25]
	v_mfma_f32_16x16x32_bf16 v[18:21], v[186:189], v[154:157], v[18:21]
	v_mfma_f32_16x16x32_bf16 v[14:17], v[178:181], v[162:165], v[14:17]
	v_mfma_f32_16x16x32_bf16 v[10:13], v[186:189], v[162:165], v[10:13]
	v_mfma_f32_16x16x32_bf16 v[6:9], v[178:181], v[170:173], v[6:9]
	v_mfma_f32_16x16x32_bf16 v[2:5], v[186:189], v[170:173], v[2:5]
	v_mfma_f32_16x16x32_bf16 v[30:33], v[182:185], v[150:153], v[30:33]
	v_mfma_f32_16x16x32_bf16 v[26:29], v[190:193], v[150:153], v[26:29]
	v_mfma_f32_16x16x32_bf16 v[22:25], v[182:185], v[158:161], v[22:25]
	v_mfma_f32_16x16x32_bf16 v[18:21], v[190:193], v[158:161], v[18:21]
	v_mfma_f32_16x16x32_bf16 v[14:17], v[182:185], v[166:169], v[14:17]
	v_mfma_f32_16x16x32_bf16 v[10:13], v[190:193], v[166:169], v[10:13]
	v_mfma_f32_16x16x32_bf16 v[6:9], v[182:185], v[174:177], v[6:9]
	v_mfma_f32_16x16x32_bf16 v[2:5], v[190:193], v[174:177], v[2:5]
	s_mov_b32 m0, s76
	v_lshl_add_u64 v[218:219], v[224:225], 0, s[54:55]
	s_barrier
	ds_read_b128 v[146:149], v240 offset:49152
	ds_read_b128 v[150:153], v240 offset:50176
	ds_read_b128 v[154:157], v240 offset:51200
	ds_read_b128 v[158:161], v240 offset:52224
	ds_read_b128 v[162:165], v240 offset:53248
	ds_read_b128 v[166:169], v240 offset:54272
	ds_read_b128 v[170:173], v240 offset:55296
	ds_read_b128 v[174:177], v240 offset:56320
	global_load_lds_dwordx4 v[218:219], off
	v_lshl_add_u64 v[218:219], v[230:231], 0, s[54:55]
	s_mov_b32 m0, s77
	s_nop 0
	global_load_lds_dwordx4 v[218:219], off
	s_barrier
	s_waitcnt lgkmcnt(0)
	s_waitcnt lgkmcnt(0)
	v_mfma_f32_16x16x32_bf16 v[66:69], v[130:133], v[146:149], v[66:69]
	v_mfma_f32_16x16x32_bf16 v[70:73], v[138:141], v[146:149], v[70:73]
	v_mfma_f32_16x16x32_bf16 v[74:77], v[130:133], v[154:157], v[74:77]
	v_mfma_f32_16x16x32_bf16 v[78:81], v[138:141], v[154:157], v[78:81]
	v_mfma_f32_16x16x32_bf16 v[82:85], v[130:133], v[162:165], v[82:85]
	v_mfma_f32_16x16x32_bf16 v[86:89], v[138:141], v[162:165], v[86:89]
	v_mfma_f32_16x16x32_bf16 v[90:93], v[130:133], v[170:173], v[90:93]
	v_mfma_f32_16x16x32_bf16 v[94:97], v[138:141], v[170:173], v[94:97]
	v_mfma_f32_16x16x32_bf16 v[66:69], v[134:137], v[150:153], v[66:69]
	v_mfma_f32_16x16x32_bf16 v[70:73], v[142:145], v[150:153], v[70:73]
	v_mfma_f32_16x16x32_bf16 v[74:77], v[134:137], v[158:161], v[74:77]
	v_mfma_f32_16x16x32_bf16 v[78:81], v[142:145], v[158:161], v[78:81]
	v_mfma_f32_16x16x32_bf16 v[82:85], v[134:137], v[166:169], v[82:85]
	v_mfma_f32_16x16x32_bf16 v[86:89], v[142:145], v[166:169], v[86:89]
	v_mfma_f32_16x16x32_bf16 v[90:93], v[134:137], v[174:177], v[90:93]
	v_mfma_f32_16x16x32_bf16 v[94:97], v[142:145], v[174:177], v[94:97]
	s_barrier
	s_add_u32 s0, s28, 0x20080
	s_addc_u32 s1, s29, 0
	s_add_i32 s28, s30, s66
	v_lshl_add_u64 v[130:131], s[0:1], 0, v[202:203]
	s_mov_b32 m0, s28
	s_nop 0
	global_load_lds_dwordx4 v[130:131], off
	v_lshl_add_u64 v[130:131], s[0:1], 0, v[198:199]
	s_add_i32 m0, s28, 0x2000
	s_nop 0
	global_load_lds_dwordx4 v[130:131], off
	s_waitcnt vmcnt(6)
	s_barrier
	v_mfma_f32_16x16x32_bf16 v[98:101], v[178:181], v[146:149], v[98:101]
	v_mfma_f32_16x16x32_bf16 v[102:105], v[186:189], v[146:149], v[102:105]
	v_mfma_f32_16x16x32_bf16 v[106:109], v[178:181], v[154:157], v[106:109]
	v_mfma_f32_16x16x32_bf16 v[110:113], v[186:189], v[154:157], v[110:113]
	v_mfma_f32_16x16x32_bf16 v[114:117], v[178:181], v[162:165], v[114:117]
	v_mfma_f32_16x16x32_bf16 v[118:121], v[186:189], v[162:165], v[118:121]
	v_mfma_f32_16x16x32_bf16 v[122:125], v[178:181], v[170:173], v[122:125]
	v_mfma_f32_16x16x32_bf16 v[126:129], v[186:189], v[170:173], v[126:129]
	v_mfma_f32_16x16x32_bf16 v[98:101], v[182:185], v[150:153], v[98:101]
	v_mfma_f32_16x16x32_bf16 v[102:105], v[190:193], v[150:153], v[102:105]
	v_mfma_f32_16x16x32_bf16 v[106:109], v[182:185], v[158:161], v[106:109]
	v_mfma_f32_16x16x32_bf16 v[110:113], v[190:193], v[158:161], v[110:113]
	v_mfma_f32_16x16x32_bf16 v[114:117], v[182:185], v[166:169], v[114:117]
	v_mfma_f32_16x16x32_bf16 v[118:121], v[190:193], v[166:169], v[118:121]
	v_mfma_f32_16x16x32_bf16 v[122:125], v[182:185], v[174:177], v[122:125]
	v_mfma_f32_16x16x32_bf16 v[126:129], v[190:193], v[174:177], v[126:129]
	s_add_i32 s86, s86, 2
	s_add_u32 s6, s6, 0x100
	s_addc_u32 s7, s7, 0
	s_add_u32 s21, s21, 0x100
	s_addc_u32 s82, s82, 0
	s_cmp_gt_u32 s86, 5
	s_barrier
	s_cbranch_scc0 .LBB0_1332
	s_cmp_lg_u32 s27, 0
	s_cselect_b64 s[6:7], -1, 0
	s_cmp_eq_u32 s27, 0
	v_lshl_add_u32 v218, s26, 8, v1
	s_cselect_b32 s0, 0, 0x10000
	s_add_u32 s26, s74, s0
	v_ashrrev_i32_e32 v130, 5, v218
	s_addc_u32 s27, s75, 0
	v_and_b32_e32 v136, -8, v130
	s_lshl_b32 s0, s79, 1
	v_add_u32_e32 v130, s0, v136
	v_ashrrev_i32_e32 v131, 31, v130
	v_lshlrev_b64 v[130:131], 17, v[130:131]
	v_lshl_add_u64 v[132:133], v[206:207], 1, s[26:27]
	v_lshl_add_u64 v[134:135], v[132:133], 0, v[130:131]
	s_or_b32 s1, s0, 1
	global_load_dwordx4 v[186:189], v[134:135], off
	v_add_u32_e32 v134, s1, v136
	v_ashrrev_i32_e32 v135, 31, v134
	v_lshlrev_b64 v[134:135], 17, v[134:135]
	v_lshl_add_u64 v[132:133], v[132:133], 0, v[134:135]
	global_load_dwordx4 v[178:181], v[132:133], off
	v_lshl_add_u64 v[132:133], v[208:209], 1, s[26:27]
	v_lshl_add_u64 v[136:137], v[132:133], 0, v[130:131]
	global_load_dwordx4 v[174:177], v[136:137], off
	v_lshl_add_u64 v[132:133], v[132:133], 0, v[134:135]
	global_load_dwordx4 v[170:173], v[132:133], off
	v_lshl_add_u64 v[132:133], v[210:211], 1, s[26:27]
	v_lshl_add_u64 v[136:137], v[132:133], 0, v[130:131]
	v_lshl_add_u64 v[132:133], v[132:133], 0, v[134:135]
	global_load_dwordx4 v[162:165], v[136:137], off
	global_load_dwordx4 v[150:153], v[132:133], off
	v_lshl_add_u64 v[132:133], v[212:213], 1, s[26:27]
	v_lshl_add_u64 v[130:131], v[132:133], 0, v[130:131]
	global_load_dwordx4 v[142:145], v[130:131], off
	v_lshl_add_u64 v[130:131], v[132:133], 0, v[134:135]
	v_add_u32_e32 v220, 0x80, v218
	global_load_dwordx4 v[134:137], v[130:131], off
	v_ashrrev_i32_e32 v130, 5, v220
	v_and_b32_e32 v146, -8, v130
	v_add_u32_e32 v130, s0, v146
	v_ashrrev_i32_e32 v131, 31, v130
	v_lshlrev_b64 v[182:183], 17, v[130:131]
	v_lshlrev_b32_e32 v130, 7, v220
	s_movk_i32 s0, 0x4000
	v_and_or_b32 v130, v130, s0, v238
	v_lshlrev_b32_e32 v194, 1, v130
	v_lshl_add_u64 v[130:131], s[26:27], 0, v[194:195]
	v_lshl_add_u64 v[132:133], v[130:131], 0, v[182:183]
	global_load_dwordx4 v[138:141], v[132:133], off
	v_add_u32_e32 v132, s1, v146
	v_ashrrev_i32_e32 v133, 31, v132
	v_lshlrev_b64 v[190:191], 17, v[132:133]
	v_lshl_add_u64 v[130:131], v[130:131], 0, v[190:191]
	global_load_dwordx4 v[130:133], v[130:131], off
	v_or_b32_e32 v146, 0x2000, v194
	v_mov_b32_e32 v147, v195
	v_lshl_add_u64 v[146:147], s[26:27], 0, v[146:147]
	v_lshl_add_u64 v[148:149], v[146:147], 0, v[182:183]
	global_load_dwordx4 v[166:169], v[148:149], off
	v_lshl_add_u64 v[146:147], v[146:147], 0, v[190:191]
	global_load_dwordx4 v[154:157], v[146:147], off
	v_or_b32_e32 v146, 0x4000, v194
	v_mov_b32_e32 v147, v195
	v_lshl_add_u64 v[146:147], s[26:27], 0, v[146:147]
	v_lshl_add_u64 v[148:149], v[146:147], 0, v[182:183]
	global_load_dwordx4 v[158:161], v[148:149], off
	v_or_b32_e32 v194, 0x6000, v194
	v_lshl_add_u64 v[192:193], s[26:27], 0, v[194:195]
	v_lshl_add_u64 v[146:147], v[146:147], 0, v[190:191]
	v_lshl_add_u64 v[190:191], v[192:193], 0, v[190:191]
	v_lshl_add_u64 v[182:183], v[192:193], 0, v[182:183]
	global_load_dwordx4 v[190:193], v[190:191], off
	s_and_b64 vcc, exec, s[6:7]
	global_load_dwordx4 v[146:149], v[146:147], off
	s_waitcnt vmcnt(0)
	v_lshlrev_b32_e32 v224, 16, v186
	global_load_dwordx4 v[182:185], v[182:183], off
	v_and_b32_e32 v225, 0xffff0000, v186
	v_lshlrev_b32_e32 v186, 16, v187
	v_and_b32_e32 v187, 0xffff0000, v187
	v_pk_mul_f32 v[64:65], v[64:65], v[186:187]
	v_lshlrev_b32_e32 v186, 16, v188
	v_and_b32_e32 v187, 0xffff0000, v188
	v_pk_mul_f32 v[58:59], v[58:59], v[186:187]
	v_lshlrev_b32_e32 v186, 16, v189
	v_and_b32_e32 v187, 0xffff0000, v189
	v_pk_mul_f32 v[60:61], v[60:61], v[186:187]
	v_lshlrev_b32_e32 v186, 16, v178
	v_and_b32_e32 v187, 0xffff0000, v178
	v_lshlrev_b32_e32 v178, 16, v179
	v_and_b32_e32 v179, 0xffff0000, v179
	v_pk_mul_f32 v[32:33], v[32:33], v[178:179]
	v_lshlrev_b32_e32 v178, 16, v180
	v_and_b32_e32 v179, 0xffff0000, v180
	v_pk_mul_f32 v[26:27], v[26:27], v[178:179]
	v_lshlrev_b32_e32 v178, 16, v181
	v_and_b32_e32 v179, 0xffff0000, v181
	v_pk_mul_f32 v[28:29], v[28:29], v[178:179]
	v_lshlrev_b32_e32 v178, 16, v174
	v_and_b32_e32 v179, 0xffff0000, v174
	v_lshlrev_b32_e32 v174, 16, v175
	v_and_b32_e32 v175, 0xffff0000, v175
	v_pk_mul_f32 v[56:57], v[56:57], v[174:175]
	v_lshlrev_b32_e32 v174, 16, v176
	v_and_b32_e32 v175, 0xffff0000, v176
	v_pk_mul_f32 v[50:51], v[50:51], v[174:175]
	v_lshlrev_b32_e32 v174, 16, v177
	v_and_b32_e32 v175, 0xffff0000, v177
	v_pk_mul_f32 v[52:53], v[52:53], v[174:175]
	v_lshlrev_b32_e32 v174, 16, v170
	v_and_b32_e32 v175, 0xffff0000, v170
	v_lshlrev_b32_e32 v170, 16, v171
	v_and_b32_e32 v171, 0xffff0000, v171
	v_pk_mul_f32 v[24:25], v[24:25], v[170:171]
	v_lshlrev_b32_e32 v170, 16, v172
	v_and_b32_e32 v171, 0xffff0000, v172
	v_pk_mul_f32 v[18:19], v[18:19], v[170:171]
	v_lshlrev_b32_e32 v170, 16, v173
	v_and_b32_e32 v171, 0xffff0000, v173
	v_pk_mul_f32 v[20:21], v[20:21], v[170:171]
	v_lshlrev_b32_e32 v170, 16, v162
	v_and_b32_e32 v171, 0xffff0000, v162
	v_lshlrev_b32_e32 v162, 16, v163
	v_and_b32_e32 v163, 0xffff0000, v163
	v_pk_mul_f32 v[48:49], v[48:49], v[162:163]
	v_lshlrev_b32_e32 v162, 16, v164
	v_and_b32_e32 v163, 0xffff0000, v164
	v_pk_mul_f32 v[42:43], v[42:43], v[162:163]
	v_lshlrev_b32_e32 v162, 16, v165
	v_and_b32_e32 v163, 0xffff0000, v165
	v_pk_mul_f32 v[44:45], v[44:45], v[162:163]
	v_lshlrev_b32_e32 v162, 16, v150
	v_and_b32_e32 v163, 0xffff0000, v150
	v_lshlrev_b32_e32 v150, 16, v151
	v_and_b32_e32 v151, 0xffff0000, v151
	v_pk_mul_f32 v[16:17], v[16:17], v[150:151]
	v_lshlrev_b32_e32 v150, 16, v152
	v_and_b32_e32 v151, 0xffff0000, v152
	v_pk_mul_f32 v[10:11], v[10:11], v[150:151]
	v_lshlrev_b32_e32 v150, 16, v153
	v_and_b32_e32 v151, 0xffff0000, v153
	v_pk_mul_f32 v[12:13], v[12:13], v[150:151]
	v_lshlrev_b32_e32 v150, 16, v142
	v_and_b32_e32 v151, 0xffff0000, v142
	v_lshlrev_b32_e32 v142, 16, v143
	v_and_b32_e32 v143, 0xffff0000, v143
	v_pk_mul_f32 v[40:41], v[40:41], v[142:143]
	v_lshlrev_b32_e32 v142, 16, v144
	v_and_b32_e32 v143, 0xffff0000, v144
	v_pk_mul_f32 v[34:35], v[34:35], v[142:143]
	v_lshlrev_b32_e32 v142, 16, v145
	v_and_b32_e32 v143, 0xffff0000, v145
	v_pk_mul_f32 v[36:37], v[36:37], v[142:143]
	v_lshlrev_b32_e32 v142, 16, v134
	v_and_b32_e32 v143, 0xffff0000, v134
	v_lshlrev_b32_e32 v134, 16, v135
	v_and_b32_e32 v135, 0xffff0000, v135
	v_pk_mul_f32 v[8:9], v[8:9], v[134:135]
	v_lshlrev_b32_e32 v134, 16, v136
	v_and_b32_e32 v135, 0xffff0000, v136
	v_pk_mul_f32 v[2:3], v[2:3], v[134:135]
	v_lshlrev_b32_e32 v134, 16, v137
	v_and_b32_e32 v135, 0xffff0000, v137
	v_pk_mul_f32 v[4:5], v[4:5], v[134:135]
	v_lshlrev_b32_e32 v134, 16, v138
	v_and_b32_e32 v135, 0xffff0000, v138
	v_pk_mul_f32 v[66:67], v[66:67], v[134:135]
	v_lshlrev_b32_e32 v134, 16, v139
	v_and_b32_e32 v135, 0xffff0000, v139
	v_pk_mul_f32 v[68:69], v[68:69], v[134:135]
	v_lshlrev_b32_e32 v134, 16, v140
	v_and_b32_e32 v135, 0xffff0000, v140
	v_pk_mul_f32 v[70:71], v[70:71], v[134:135]
	v_lshlrev_b32_e32 v134, 16, v141
	v_and_b32_e32 v135, 0xffff0000, v141
	v_pk_mul_f32 v[72:73], v[72:73], v[134:135]
	v_lshlrev_b32_e32 v134, 16, v130
	v_and_b32_e32 v135, 0xffff0000, v130
	v_lshlrev_b32_e32 v130, 16, v131
	v_and_b32_e32 v131, 0xffff0000, v131
	v_pk_mul_f32 v[100:101], v[100:101], v[130:131]
	v_lshlrev_b32_e32 v130, 16, v132
	v_and_b32_e32 v131, 0xffff0000, v132
	v_pk_mul_f32 v[102:103], v[102:103], v[130:131]
	v_lshlrev_b32_e32 v130, 16, v133
	v_and_b32_e32 v131, 0xffff0000, v133
	v_pk_mul_f32 v[104:105], v[104:105], v[130:131]
	v_lshlrev_b32_e32 v130, 16, v166
	v_and_b32_e32 v131, 0xffff0000, v166
	v_pk_mul_f32 v[74:75], v[74:75], v[130:131]
	v_lshlrev_b32_e32 v130, 16, v167
	v_and_b32_e32 v131, 0xffff0000, v167
	v_pk_mul_f32 v[76:77], v[76:77], v[130:131]
	v_lshlrev_b32_e32 v130, 16, v168
	v_and_b32_e32 v131, 0xffff0000, v168
	v_pk_mul_f32 v[78:79], v[78:79], v[130:131]
	v_lshlrev_b32_e32 v130, 16, v169
	v_and_b32_e32 v131, 0xffff0000, v169
	v_pk_mul_f32 v[80:81], v[80:81], v[130:131]
	v_lshlrev_b32_e32 v130, 16, v154
	v_and_b32_e32 v131, 0xffff0000, v154
	v_pk_mul_f32 v[106:107], v[106:107], v[130:131]
	v_lshlrev_b32_e32 v130, 16, v155
	v_and_b32_e32 v131, 0xffff0000, v155
	v_pk_mul_f32 v[108:109], v[108:109], v[130:131]
	v_lshlrev_b32_e32 v130, 16, v156
	v_and_b32_e32 v131, 0xffff0000, v156
	v_pk_mul_f32 v[110:111], v[110:111], v[130:131]
	v_lshlrev_b32_e32 v130, 16, v157
	v_and_b32_e32 v131, 0xffff0000, v157
	v_pk_mul_f32 v[112:113], v[112:113], v[130:131]
	v_lshlrev_b32_e32 v130, 16, v158
	v_and_b32_e32 v131, 0xffff0000, v158
	v_pk_mul_f32 v[82:83], v[82:83], v[130:131]
	v_lshlrev_b32_e32 v130, 16, v159
	v_and_b32_e32 v131, 0xffff0000, v159
	v_pk_mul_f32 v[84:85], v[84:85], v[130:131]
	v_lshlrev_b32_e32 v130, 16, v160
	v_and_b32_e32 v131, 0xffff0000, v160
	v_pk_mul_f32 v[86:87], v[86:87], v[130:131]
	v_lshlrev_b32_e32 v130, 16, v161
	v_and_b32_e32 v131, 0xffff0000, v161
	v_pk_mul_f32 v[88:89], v[88:89], v[130:131]
	v_lshlrev_b32_e32 v130, 16, v146
	v_and_b32_e32 v131, 0xffff0000, v146
	v_pk_mul_f32 v[114:115], v[114:115], v[130:131]
	v_lshlrev_b32_e32 v130, 16, v147
	v_and_b32_e32 v131, 0xffff0000, v147
	v_pk_mul_f32 v[116:117], v[116:117], v[130:131]
	v_lshlrev_b32_e32 v130, 16, v148
	v_and_b32_e32 v131, 0xffff0000, v148
	v_pk_mul_f32 v[118:119], v[118:119], v[130:131]
	v_lshlrev_b32_e32 v130, 16, v149
	v_and_b32_e32 v131, 0xffff0000, v149
	v_pk_mul_f32 v[120:121], v[120:121], v[130:131]
	s_waitcnt vmcnt(0)
	v_lshlrev_b32_e32 v130, 16, v182
	v_and_b32_e32 v131, 0xffff0000, v182
	v_pk_mul_f32 v[90:91], v[90:91], v[130:131]
	v_lshlrev_b32_e32 v130, 16, v183
	v_and_b32_e32 v131, 0xffff0000, v183
	v_pk_mul_f32 v[92:93], v[92:93], v[130:131]
	v_lshlrev_b32_e32 v130, 16, v184
	v_and_b32_e32 v131, 0xffff0000, v184
	v_pk_mul_f32 v[94:95], v[94:95], v[130:131]
	v_lshlrev_b32_e32 v130, 16, v185
	v_and_b32_e32 v131, 0xffff0000, v185
	v_pk_mul_f32 v[96:97], v[96:97], v[130:131]
	v_lshlrev_b32_e32 v130, 16, v190
	v_and_b32_e32 v131, 0xffff0000, v190
	v_pk_mul_f32 v[122:123], v[122:123], v[130:131]
	v_lshlrev_b32_e32 v130, 16, v191
	v_and_b32_e32 v131, 0xffff0000, v191
	v_pk_mul_f32 v[124:125], v[124:125], v[130:131]
	v_lshlrev_b32_e32 v130, 16, v192
	v_and_b32_e32 v131, 0xffff0000, v192
	v_pk_mul_f32 v[126:127], v[126:127], v[130:131]
	v_lshlrev_b32_e32 v130, 16, v193
	v_and_b32_e32 v131, 0xffff0000, v193
	v_pk_mul_f32 v[62:63], v[62:63], v[224:225]
	v_pk_mul_f32 v[30:31], v[30:31], v[186:187]
	v_pk_mul_f32 v[54:55], v[54:55], v[178:179]
	v_pk_mul_f32 v[22:23], v[22:23], v[174:175]
	v_pk_mul_f32 v[46:47], v[46:47], v[170:171]
	v_pk_mul_f32 v[14:15], v[14:15], v[162:163]
	v_pk_mul_f32 v[38:39], v[38:39], v[150:151]
	v_pk_mul_f32 v[6:7], v[6:7], v[142:143]
	v_pk_mul_f32 v[98:99], v[98:99], v[134:135]
	v_pk_mul_f32 v[128:129], v[128:129], v[130:131]
	s_cbranch_vccz .LBB0_1335
	v_lshl_or_b32 v134, s79, 8, v239
	v_ashrrev_i32_e32 v219, 31, v218
	v_lshlrev_b64 v[130:131], 11, v[218:219]
	v_ashrrev_i32_e32 v135, 31, v134
	v_lshl_add_u64 v[136:137], s[8:9], 0, v[130:131]
	v_lshlrev_b64 v[134:135], 1, v[134:135]
	v_cvt_pk_bf16_f32 v130, v62, v63
	v_cvt_pk_bf16_f32 v131, v64, v65
	v_cvt_pk_bf16_f32 v132, v58, v59
	v_cvt_pk_bf16_f32 v133, v60, v61
	v_lshl_add_u64 v[136:137], v[136:137], 0, v[134:135]
	global_store_dwordx4 v[136:137], v[130:133], off
	v_ashrrev_i32_e32 v221, 31, v220
	s_mov_b64 s[0:1], 0x48000
	v_cvt_pk_bf16_f32 v130, v30, v31
	v_cvt_pk_bf16_f32 v131, v32, v33
	v_cvt_pk_bf16_f32 v132, v26, v27
	v_cvt_pk_bf16_f32 v133, v28, v29
	global_store_dwordx4 v[136:137], v[130:133], off offset:256
	s_nop 1
	v_or_b32_e32 v130, 16, v218
	v_ashrrev_i32_e32 v131, 31, v130
	v_lshlrev_b64 v[130:131], 11, v[130:131]
	v_lshl_add_u64 v[138:139], s[8:9], 0, v[130:131]
	v_cvt_pk_bf16_f32 v130, v54, v55
	v_cvt_pk_bf16_f32 v131, v56, v57
	v_cvt_pk_bf16_f32 v132, v50, v51
	v_cvt_pk_bf16_f32 v133, v52, v53
	v_lshl_add_u64 v[138:139], v[138:139], 0, v[134:135]
	global_store_dwordx4 v[138:139], v[130:133], off
	s_nop 1
	v_cvt_pk_bf16_f32 v130, v22, v23
	v_cvt_pk_bf16_f32 v131, v24, v25
	v_cvt_pk_bf16_f32 v132, v18, v19
	v_cvt_pk_bf16_f32 v133, v20, v21
	global_store_dwordx4 v[138:139], v[130:133], off offset:256
	s_nop 1
	v_or_b32_e32 v130, 32, v218
	v_ashrrev_i32_e32 v131, 31, v130
	v_lshlrev_b64 v[130:131], 11, v[130:131]
	v_lshl_add_u64 v[138:139], s[8:9], 0, v[130:131]
	v_cvt_pk_bf16_f32 v130, v46, v47
	v_cvt_pk_bf16_f32 v131, v48, v49
	v_cvt_pk_bf16_f32 v132, v42, v43
	v_cvt_pk_bf16_f32 v133, v44, v45
	v_lshl_add_u64 v[138:139], v[138:139], 0, v[134:135]
	global_store_dwordx4 v[138:139], v[130:133], off
	s_nop 1
	v_cvt_pk_bf16_f32 v130, v14, v15
	v_cvt_pk_bf16_f32 v131, v16, v17
	v_cvt_pk_bf16_f32 v132, v10, v11
	v_cvt_pk_bf16_f32 v133, v12, v13
	global_store_dwordx4 v[138:139], v[130:133], off offset:256
	s_nop 1
	v_or_b32_e32 v130, 48, v218
	v_ashrrev_i32_e32 v131, 31, v130
	v_lshlrev_b64 v[130:131], 11, v[130:131]
	v_lshl_add_u64 v[138:139], s[8:9], 0, v[130:131]
	v_cvt_pk_bf16_f32 v130, v38, v39
	v_cvt_pk_bf16_f32 v131, v40, v41
	v_cvt_pk_bf16_f32 v132, v34, v35
	v_cvt_pk_bf16_f32 v133, v36, v37
	v_lshl_add_u64 v[138:139], v[138:139], 0, v[134:135]
	global_store_dwordx4 v[138:139], v[130:133], off
	s_nop 1
	v_cvt_pk_bf16_f32 v130, v6, v7
	v_cvt_pk_bf16_f32 v131, v8, v9
	v_cvt_pk_bf16_f32 v132, v2, v3
	v_cvt_pk_bf16_f32 v133, v4, v5
	global_store_dwordx4 v[138:139], v[130:133], off offset:256
	s_nop 1
	v_lshlrev_b64 v[130:131], 11, v[220:221]
	v_lshl_add_u64 v[138:139], s[8:9], 0, v[130:131]
	v_cvt_pk_bf16_f32 v130, v66, v67
	v_cvt_pk_bf16_f32 v131, v68, v69
	v_cvt_pk_bf16_f32 v132, v70, v71
	v_cvt_pk_bf16_f32 v133, v72, v73
	v_lshl_add_u64 v[134:135], v[138:139], 0, v[134:135]
	global_store_dwordx4 v[134:135], v[130:133], off
	s_nop 1
	v_cvt_pk_bf16_f32 v130, v98, v99
	v_cvt_pk_bf16_f32 v131, v100, v101
	v_cvt_pk_bf16_f32 v132, v102, v103
	v_cvt_pk_bf16_f32 v133, v104, v105
	global_store_dwordx4 v[134:135], v[130:133], off offset:256
	v_lshl_add_u64 v[134:135], v[136:137], 0, s[0:1]
	s_mov_b32 s0, 0x48000
	v_add_co_u32_e32 v138, vcc, s0, v136
	v_cvt_pk_bf16_f32 v130, v74, v75
	v_cvt_pk_bf16_f32 v131, v76, v77
	v_cvt_pk_bf16_f32 v132, v78, v79
	v_cvt_pk_bf16_f32 v133, v80, v81
	v_addc_co_u32_e32 v139, vcc, 0, v137, vcc
	global_store_dwordx4 v[138:139], v[130:133], off
	s_mov_b64 s[0:1], 0x50000
	s_nop 0
	v_cvt_pk_bf16_f32 v130, v106, v107
	v_cvt_pk_bf16_f32 v131, v108, v109
	v_cvt_pk_bf16_f32 v132, v110, v111
	v_cvt_pk_bf16_f32 v133, v112, v113
	global_store_dwordx4 v[134:135], v[130:133], off offset:256
	v_lshl_add_u64 v[134:135], v[136:137], 0, s[0:1]
	s_mov_b32 s0, 0x50000
	v_add_co_u32_e32 v138, vcc, s0, v136
	v_cvt_pk_bf16_f32 v130, v82, v83
	v_cvt_pk_bf16_f32 v131, v84, v85
	v_cvt_pk_bf16_f32 v132, v86, v87
	v_cvt_pk_bf16_f32 v133, v88, v89
	v_addc_co_u32_e32 v139, vcc, 0, v137, vcc
	global_store_dwordx4 v[138:139], v[130:133], off
	s_mov_b64 s[0:1], 0x58000
	s_nop 0
	v_cvt_pk_bf16_f32 v130, v114, v115
	v_cvt_pk_bf16_f32 v131, v116, v117
	v_cvt_pk_bf16_f32 v132, v118, v119
	v_cvt_pk_bf16_f32 v133, v120, v121
	global_store_dwordx4 v[134:135], v[130:133], off offset:256
	v_lshl_add_u64 v[134:135], v[136:137], 0, s[0:1]
	s_mov_b32 s0, 0x58000
	v_add_co_u32_e32 v136, vcc, s0, v136
	v_cvt_pk_bf16_f32 v130, v90, v91
	v_cvt_pk_bf16_f32 v131, v92, v93
	v_cvt_pk_bf16_f32 v132, v94, v95
	v_cvt_pk_bf16_f32 v133, v96, v97
	v_addc_co_u32_e32 v137, vcc, 0, v137, vcc
	global_store_dwordx4 v[136:137], v[130:133], off
	s_nop 1
	v_cvt_pk_bf16_f32 v130, v122, v123
	v_cvt_pk_bf16_f32 v131, v124, v125
	v_cvt_pk_bf16_f32 v132, v126, v127
	v_cvt_pk_bf16_f32 v133, v128, v129
	global_store_dwordx4 v[134:135], v[130:133], off offset:256

.LBB0_1696:
	s_mov_b64 s[0:1], s[12:13]
	s_load_dword s0, s[0:1], 0x110
	s_waitcnt lgkmcnt(0)
	s_cmp_gt_i32 s0, s64
	s_cbranch_scc1 .LBB0_1754
	s_mov_b64 s[0:1], s[12:13]
	s_load_dword s0, s[0:1], 0x114
	s_waitcnt lgkmcnt(0)
	s_cmp_ge_i32 s64, s0
	s_cbranch_scc1 .LBB0_1753
	v_readlane_b32 s0, v254, 2
	v_readlane_b32 s1, v254, 3
	s_load_dword s1, s[0:1], 0x110
	s_add_i32 s0, s41, 6
	s_waitcnt lgkmcnt(0)
	s_cmp_gt_i32 s1, s0
	s_cbranch_scc1 .LBB0_1753
	v_readlane_b32 s2, v254, 2
	v_readlane_b32 s3, v254, 3
	s_load_dword s1, s[2:3], 0x114
	s_waitcnt lgkmcnt(0)
	s_cmp_ge_i32 s0, s1
	s_cbranch_scc1 .LBB0_1753
	v_readlane_b32 s6, v254, 2
	v_mov_b32_e32 v1, v0
	v_readlane_b32 s7, v254, 3
	s_load_dword s0, s[6:7], 0x118
	v_readlane_b32 s1, v254, 0
	s_waitcnt lgkmcnt(0)
	s_setprio 0
	s_getreg_b32 s0, hwreg(HW_REG_XCC_ID, 0, 4)
	s_waitcnt vmcnt(0)
	s_barrier
	s_mov_b64 s[4:5], exec
	v_readlane_b32 s2, v254, 6
	v_readlane_b32 s3, v254, 7
	s_and_b64 s[2:3], s[4:5], s[2:3]
	s_mov_b64 exec, s[2:3]
	s_cbranch_execz .LBB0_1752
	s_add_i32 s3, 0, 0x26000
	v_mov_b32_e32 v1, s3
	s_load_dwordx2 s[6:7], s[6:7], 0x108
	s_waitcnt vmcnt(0) expcnt(0) lgkmcnt(0)
	ds_read_b32 v3, v1
	v_readlane_b32 s1, v254, 8
	s_and_b32 s2, s0, 15
	s_waitcnt lgkmcnt(0)
	v_cmp_ne_u32_e32 vcc, 0, v3
	v_mov_b32_e32 v1, s1
	ds_read_b32 v2, v1
	s_cbranch_vccnz .LBB0_1716
	v_readlane_b32 s8, v254, 4
	v_readlane_b32 s12, v254, 2
	v_readlane_b32 s9, v254, 5
	v_readlane_b32 s13, v254, 3
	s_load_dwordx2 s[0:1], s[8:9], 0x4
	s_nop 0
	s_load_dword s12, s[12:13], 0x118
	s_add_u32 s8, s6, 0x4200
	s_addc_u32 s9, s7, 0
	s_add_u32 s10, s6, 0x4400
	s_addc_u32 s11, s7, 0
	s_waitcnt lgkmcnt(0)
	s_mul_i32 s34, s0, s12
	s_add_u32 s12, s6, 0x4500
	s_addc_u32 s13, s7, 0
	s_add_u32 s14, s6, 0x4600
	s_addc_u32 s15, s7, 0
	s_add_u32 s16, s6, 0x4700
	s_addc_u32 s17, s7, 0
	s_add_u32 s18, s6, 0x4800
	s_addc_u32 s19, s7, 0
	s_add_u32 s20, s6, 0x4900
	s_addc_u32 s21, s7, 0
	s_add_u32 s22, s6, 0x4a00
	s_addc_u32 s23, s7, 0
	s_add_u32 s24, s6, 0x4b00
	s_addc_u32 s25, s7, 0
	s_add_u32 s26, s6, 0x4c00
	s_addc_u32 s27, s7, 0
	s_add_u32 s28, s6, 0x4d00
	s_addc_u32 s29, s7, 0
	s_add_u32 s30, s6, 0x4e00
	s_addc_u32 s31, s7, 0
	s_add_u32 s64, s6, 0x4f00
	s_addc_u32 s65, s7, 0
	s_add_u32 s66, s6, 0x5000
	s_addc_u32 s67, s7, 0
	s_add_u32 s68, s6, 0x5100
	s_addc_u32 s69, s7, 0
	s_add_u32 s70, s6, 0x5200
	s_addc_u32 s71, s7, 0
	s_add_u32 s72, s6, 0x5300
	s_mul_i32 s34, s34, s1
	s_addc_u32 s73, s7, 0
	s_mov_b32 s0, 1
	s_branch .LBB0_1704

.LBB0_1758:
	s_andn2_b64 vcc, exec, s[10:11]
	s_cbranch_vccnz .LBB0_1770
	v_lshlrev_b32_e32 v1, 4, v16
	v_add_u32_e32 v2, 0x2000, v1
	v_ashrrev_i32_e32 v3, 31, v2
	v_lshrrev_b32_e32 v3, 22, v3
	v_add_u32_e32 v3, v2, v3
	s_waitcnt vmcnt(1)
	v_ashrrev_i32_e32 v10, 10, v3
	v_mul_i32_i24_e32 v3, 0x400, v10
	v_sub_u32_e32 v2, v2, v3
	v_lshrrev_b32_e32 v3, 4, v2
	v_bitop3_b32 v2, v3, v2, 32 bitop3:0x6c
	v_ashrrev_i32_e32 v3, 31, v2
	v_lshrrev_b32_e32 v3, 26, v3
	v_add_u32_e32 v3, v2, v3
	v_lshlrev_b32_e32 v4, 3, v10
	v_ashrrev_i32_e32 v11, 6, v3
	v_and_b32_e32 v4, -16, v4
	s_lshl_b32 s10, s1, 10
	s_lshl_b32 s1, s1, 11
	v_add_u32_e32 v4, v11, v4
	s_add_u32 s35, s4, s1
	v_and_b32_e32 v5, 3, v11
	s_mov_b32 s1, 0x1fffe0
	v_lshrrev_b32_e32 v6, 2, v4
	v_lshlrev_b32_e32 v7, 1, v4
	v_and_b32_e32 v3, 0xc0, v3
	v_and_or_b32 v5, v4, s1, v5
	v_and_b32_e32 v6, 4, v6
	v_and_b32_e32 v7, 24, v7
	v_sub_u32_e32 v2, v2, v3
	v_or3_b32 v5, v5, v6, v7
	v_lshlrev_b32_e32 v6, 5, v10
	v_ashrrev_i16_sdwa v2, v226, sext(v2) dst_sel:DWORD dst_unused:UNUSED_PAD src0_sel:DWORD src1_sel:BYTE_0
	v_and_b32_e32 v6, 32, v6
	v_bfe_i32 v12, v2, 0, 16
	v_add_lshl_u32 v2, v6, v12, 1
	v_lshl_add_u32 v130, v5, 11, v2
	v_lshl_add_u32 v132, v4, 11, v2
	v_bfe_i32 v2, v16, 27, 1
	v_lshrrev_b32_e32 v2, 22, v2
	v_add_u32_e32 v2, v1, v2
	v_and_b32_e32 v2, 0xfffffc00, v2
	v_sub_u32_e32 v1, v1, v2
	v_lshrrev_b32_e32 v2, 4, v1
	v_ashrrev_i32_e32 v3, 31, v16
	v_bitop3_b32 v1, v2, v1, 32 bitop3:0x6c
	v_lshrrev_b32_e32 v3, 26, v3
	v_ashrrev_i32_e32 v2, 31, v1
	v_add_u32_e32 v3, v16, v3
	v_lshrrev_b32_e32 v2, 26, v2
	v_ashrrev_i32_e32 v14, 6, v3
	s_addc_u32 s40, s5, 0
	v_add_u32_e32 v2, v1, v2
	v_lshlrev_b32_e32 v3, 3, v14
	s_ashr_i32 s66, s31, 31
	s_lshr_b32 s43, s0, 8
	v_ashrrev_i32_e32 v13, 6, v2
	v_and_b32_e32 v3, -16, v3
	s_lshr_b32 s65, s0, 9
	s_lshr_b32 s0, s66, 29
	v_add_u32_e32 v3, v13, v3
	v_and_b32_e32 v4, 3, v13
	s_add_i32 s0, s31, s0
	s_ashr_i32 s5, s34, 6
	v_and_or_b32 v4, v3, s1, v4
	s_ashr_i32 s1, s0, 3
	s_and_b32 s0, s0, -8
	s_ashr_i32 s14, s34, 8
	s_lshl_b32 s64, s5, 10
	s_sub_i32 s0, s31, s0
	s_or_b32 s67, s65, 1
	s_cmp_lt_i32 s0, 0
	s_cselect_b32 s4, s67, s65
	s_mul_i32 s0, s4, s0
	s_add_i32 s0, s0, s1
	s_ashr_i32 s1, s0, 31
	s_lshr_b32 s1, s1, 27
	s_add_i32 s1, s0, s1
	v_lshrrev_b32_e32 v5, 2, v3
	v_lshlrev_b32_e32 v6, 1, v3
	v_and_b32_e32 v2, 0xc0, v2
	s_ashr_i32 s4, s1, 5
	v_and_b32_e32 v5, 4, v5
	v_and_b32_e32 v6, 24, v6
	v_sub_u32_e32 v1, v1, v2
	s_lshl_b32 s11, s4, 3
	v_or3_b32 v4, v4, v5, v6
	v_lshlrev_b32_e32 v5, 5, v14
	v_ashrrev_i16_sdwa v1, v226, sext(v1) dst_sel:DWORD dst_unused:UNUSED_PAD src0_sel:DWORD src1_sel:BYTE_0
	s_sub_i32 s4, s43, s11
	v_and_b32_e32 v5, 32, v5
	v_bfe_i32 v15, v1, 0, 16
	s_min_i32 s12, s4, 8
	v_add_lshl_u32 v1, v5, v15, 1
	s_sext_i32_i8 s4, s12
	v_lshl_add_u32 v194, v4, 11, v1
	v_lshl_add_u32 v134, v3, 11, v1
	v_cvt_f32_i32_e32 v1, s4
	s_andn2_b32 s1, s1, 31
	s_sub_i32 s13, s0, s1
	v_cvt_f32_i32_e32 v2, s13
	v_rcp_iflag_f32_e32 v3, v1
	s_xor_b32 s0, s13, s4
	s_ashr_i32 s0, s0, 30
	s_or_b32 s4, s0, 1
	v_mul_f32_e32 v3, v2, v3
	v_trunc_f32_e32 v3, v3
	v_fma_f32 v2, -v3, v1, v2
	v_cvt_i32_f32_e32 v3, v3
	v_cmp_ge_f32_e64 s[0:1], |v2|, |v1|
	s_and_b64 s[0:1], s[0:1], exec
	s_cselect_b32 s0, s4, 0
	v_readfirstlane_b32 s1, v3
	s_add_i32 s4, s1, s0
	s_mul_i32 s0, s4, s12
	s_sub_i32 s0, s13, s0
	s_sext_i32_i8 s0, s0
	s_add_i32 s12, s11, s0
	s_ashr_i32 s13, s12, 31
	s_bfe_i64 s[18:19], s[4:5], 0x80000
	s_lshl_b64 s[0:1], s[12:13], 19
	s_lshl_b64 s[18:19], s[18:19], 19
	s_add_u32 s26, s16, s18
	s_addc_u32 s27, s17, s19
	s_add_i32 s13, s64, 0
	s_add_i32 m0, s13, 0x10000
	v_mov_b32_e32 v131, v195
	global_load_lds_dwordx4 v194, s[26:27]
	s_add_i32 m0, s13, 0x12000
	s_add_u32 s24, s35, s0
	global_load_lds_dwordx4 v130, s[26:27]
	s_addc_u32 s25, s40, s1
	s_mov_b32 m0, s13
	s_add_i32 s68, s13, 0x2000
	global_load_lds_dwordx4 v134, s[24:25]
	s_mov_b32 m0, s68
	s_add_u32 s0, s26, 0x40000
	global_load_lds_dwordx4 v132, s[24:25]
	s_addc_u32 s1, s27, 0
	s_add_i32 m0, s13, 0x14000
	v_mov_b32_e32 v135, v195
	global_load_lds_dwordx4 v194, s[0:1]
	s_add_i32 m0, s13, 0x16000
	v_mov_b32_e32 v133, v195
	global_load_lds_dwordx4 v130, s[0:1]
	s_add_u32 s0, s24, 0x40000
	s_addc_u32 s1, s25, 0
	s_add_i32 s69, s13, 0x4000
	s_mov_b32 m0, s69
	s_add_i32 s70, s13, 0x6000
	global_load_lds_dwordx4 v134, s[0:1]
	s_mov_b32 m0, s70
	s_waitcnt vmcnt(0)
	v_lshl_add_u64 v[8:9], s[26:27], 0, v[194:195]
	global_load_lds_dwordx4 v132, s[0:1]
	v_lshl_add_u64 v[6:7], s[26:27], 0, v[130:131]
	v_lshl_add_u64 v[4:5], s[24:25], 0, v[134:135]
	s_cmp_lg_u32 s14, 1
	v_lshl_add_u64 v[2:3], s[24:25], 0, v[132:133]
	s_setprio 1
	s_cbranch_scc1 .LBB0_1761
	s_barrier
	s_setprio 0

.LBB0_1765:
	s_add_u32 s0, s24, 0xfffc0080
	s_addc_u32 s1, s25, -1
	s_add_i32 s33, 0, 0x10000
	v_add_u32_e32 v156, s33, v141
	ds_read_b128 v[144:147], v156
	ds_read_b128 v[148:151], v156 offset:1024
	ds_read_b128 v[152:155], v156 offset:2048
	ds_read_b128 v[156:159], v156 offset:3072
	s_cmp_eq_u32 s82, 12
	s_cselect_b32 s29, s19, s1
	s_cselect_b32 s28, s76, s0
	s_cselect_b32 s27, s15, s79
	s_cselect_b32 s26, s77, s78
	v_lshl_add_u64 v[192:193], s[24:25], 0, v[136:137]
	s_add_i32 m0, s13, 0xc000
	ds_read_b128 v[160:163], v143
	ds_read_b128 v[164:167], v143 offset:1024
	ds_read_b128 v[168:171], v143 offset:2048
	ds_read_b128 v[172:175], v143 offset:3072
	ds_read_b128 v[176:179], v143 offset:4096
	ds_read_b128 v[180:183], v143 offset:5120
	ds_read_b128 v[184:187], v143 offset:6144
	ds_read_b128 v[188:191], v143 offset:7168
	global_load_lds_dwordx4 v[192:193], off
	v_lshl_add_u64 v[192:193], s[24:25], 0, v[138:139]
	s_add_i32 m0, s13, 0xe000
	s_nop 0
	global_load_lds_dwordx4 v[192:193], off
	s_waitcnt lgkmcnt(8)
	s_barrier
	s_waitcnt lgkmcnt(0)
	s_waitcnt lgkmcnt(0)
	v_mfma_f32_16x16x32_bf16 v[126:129], v[144:147], v[160:163], v[126:129]
	v_mfma_f32_16x16x32_bf16 v[122:125], v[152:155], v[160:163], v[122:125]
	v_mfma_f32_16x16x32_bf16 v[118:121], v[144:147], v[168:171], v[118:121]
	v_mfma_f32_16x16x32_bf16 v[114:117], v[152:155], v[168:171], v[114:117]
	v_mfma_f32_16x16x32_bf16 v[102:105], v[144:147], v[176:179], v[102:105]
	v_mfma_f32_16x16x32_bf16 v[98:101], v[152:155], v[176:179], v[98:101]
	v_mfma_f32_16x16x32_bf16 v[86:89], v[144:147], v[184:187], v[86:89]
	v_mfma_f32_16x16x32_bf16 v[82:85], v[152:155], v[184:187], v[82:85]
	v_mfma_f32_16x16x32_bf16 v[126:129], v[148:151], v[164:167], v[126:129]
	v_mfma_f32_16x16x32_bf16 v[122:125], v[156:159], v[164:167], v[122:125]
	v_mfma_f32_16x16x32_bf16 v[118:121], v[148:151], v[172:175], v[118:121]
	v_mfma_f32_16x16x32_bf16 v[114:117], v[156:159], v[172:175], v[114:117]
	v_mfma_f32_16x16x32_bf16 v[102:105], v[148:151], v[180:183], v[102:105]
	v_mfma_f32_16x16x32_bf16 v[98:101], v[156:159], v[180:183], v[98:101]
	v_mfma_f32_16x16x32_bf16 v[86:89], v[148:151], v[188:191], v[86:89]
	v_mfma_f32_16x16x32_bf16 v[82:85], v[156:159], v[188:191], v[82:85]
	s_barrier
	s_add_i32 s36, 0, 0x14000
	v_add_u32_e32 v192, s36, v141
	s_add_i32 s0, s33, s64
	ds_read_b128 v[198:201], v192
	ds_read_b128 v[202:205], v192 offset:1024
	ds_read_b128 v[206:209], v192 offset:2048
	ds_read_b128 v[210:213], v192 offset:3072
	v_lshl_add_u64 v[192:193], s[26:27], 0, v[194:195]
	s_mov_b32 m0, s0
	v_lshl_add_u64 v[214:215], s[26:27], 0, v[130:131]
	global_load_lds_dwordx4 v[192:193], off
	s_add_i32 m0, s0, 0x2000
	s_nop 0
	global_load_lds_dwordx4 v[214:215], off
	s_barrier
	s_waitcnt lgkmcnt(0)
	s_waitcnt lgkmcnt(0)
	v_mfma_f32_16x16x32_bf16 v[110:113], v[198:201], v[160:163], v[110:113]
	v_mfma_f32_16x16x32_bf16 v[106:109], v[206:209], v[160:163], v[106:109]
	v_mfma_f32_16x16x32_bf16 v[94:97], v[198:201], v[168:171], v[94:97]
	v_mfma_f32_16x16x32_bf16 v[90:93], v[206:209], v[168:171], v[90:93]
	v_mfma_f32_16x16x32_bf16 v[78:81], v[198:201], v[176:179], v[78:81]
	v_mfma_f32_16x16x32_bf16 v[74:77], v[206:209], v[176:179], v[74:77]
	v_mfma_f32_16x16x32_bf16 v[70:73], v[198:201], v[184:187], v[70:73]
	v_mfma_f32_16x16x32_bf16 v[66:69], v[206:209], v[184:187], v[66:69]
	v_mfma_f32_16x16x32_bf16 v[110:113], v[202:205], v[164:167], v[110:113]
	v_mfma_f32_16x16x32_bf16 v[106:109], v[210:213], v[164:167], v[106:109]
	v_mfma_f32_16x16x32_bf16 v[94:97], v[202:205], v[172:175], v[94:97]
	v_mfma_f32_16x16x32_bf16 v[90:93], v[210:213], v[172:175], v[90:93]
	v_mfma_f32_16x16x32_bf16 v[78:81], v[202:205], v[180:183], v[78:81]
	v_mfma_f32_16x16x32_bf16 v[74:77], v[210:213], v[180:183], v[74:77]
	v_mfma_f32_16x16x32_bf16 v[70:73], v[202:205], v[188:191], v[70:73]
	v_mfma_f32_16x16x32_bf16 v[66:69], v[210:213], v[188:191], v[66:69]
	s_mov_b32 m0, s13
	v_lshl_add_u64 v[216:217], s[28:29], 0, v[134:135]
	s_barrier
	ds_read_b128 v[160:163], v143 offset:16384
	ds_read_b128 v[164:167], v143 offset:17408
	ds_read_b128 v[168:171], v143 offset:18432
	ds_read_b128 v[172:175], v143 offset:19456
	ds_read_b128 v[176:179], v143 offset:20480
	ds_read_b128 v[180:183], v143 offset:21504
	ds_read_b128 v[184:187], v143 offset:22528
	ds_read_b128 v[188:191], v143 offset:23552
	global_load_lds_dwordx4 v[216:217], off
	v_lshl_add_u64 v[218:219], s[28:29], 0, v[132:133]
	s_mov_b32 m0, s68
	s_nop 0
	global_load_lds_dwordx4 v[218:219], off
	s_barrier
	s_waitcnt lgkmcnt(0)
	s_waitcnt lgkmcnt(0)
	v_mfma_f32_16x16x32_bf16 v[62:65], v[144:147], v[160:163], v[62:65]
	v_mfma_f32_16x16x32_bf16 v[58:61], v[152:155], v[160:163], v[58:61]
	v_mfma_f32_16x16x32_bf16 v[54:57], v[144:147], v[168:171], v[54:57]
	v_mfma_f32_16x16x32_bf16 v[50:53], v[152:155], v[168:171], v[50:53]
	v_mfma_f32_16x16x32_bf16 v[38:41], v[144:147], v[176:179], v[38:41]
	v_mfma_f32_16x16x32_bf16 v[34:37], v[152:155], v[176:179], v[34:37]
	v_mfma_f32_16x16x32_bf16 v[22:25], v[144:147], v[184:187], v[22:25]
	v_mfma_f32_16x16x32_bf16 v[18:21], v[152:155], v[184:187], v[18:21]
	v_mfma_f32_16x16x32_bf16 v[62:65], v[148:151], v[164:167], v[62:65]
	v_mfma_f32_16x16x32_bf16 v[58:61], v[156:159], v[164:167], v[58:61]
	v_mfma_f32_16x16x32_bf16 v[54:57], v[148:151], v[172:175], v[54:57]
	v_mfma_f32_16x16x32_bf16 v[50:53], v[156:159], v[172:175], v[50:53]
	v_mfma_f32_16x16x32_bf16 v[38:41], v[148:151], v[180:183], v[38:41]
	v_mfma_f32_16x16x32_bf16 v[34:37], v[156:159], v[180:183], v[34:37]
	v_mfma_f32_16x16x32_bf16 v[22:25], v[148:151], v[188:191], v[22:25]
	v_mfma_f32_16x16x32_bf16 v[18:21], v[156:159], v[188:191], v[18:21]
	s_barrier
	s_add_u32 s0, s26, 0x40000
	s_addc_u32 s1, s27, 0
	s_add_i32 s33, s36, s64
	v_lshl_add_u64 v[144:145], s[0:1], 0, v[194:195]
	s_mov_b32 m0, s33
	s_nop 0
	global_load_lds_dwordx4 v[144:145], off
	v_lshl_add_u64 v[144:145], s[0:1], 0, v[130:131]
	s_add_i32 m0, s33, 0x2000
	s_nop 0
	global_load_lds_dwordx4 v[144:145], off
	s_waitcnt vmcnt(6)
	s_barrier
	v_mfma_f32_16x16x32_bf16 v[46:49], v[198:201], v[160:163], v[46:49]
	v_mfma_f32_16x16x32_bf16 v[42:45], v[206:209], v[160:163], v[42:45]
	v_mfma_f32_16x16x32_bf16 v[30:33], v[198:201], v[168:171], v[30:33]
	v_mfma_f32_16x16x32_bf16 v[26:29], v[206:209], v[168:171], v[26:29]
	v_mfma_f32_16x16x32_bf16 v[14:17], v[198:201], v[176:179], v[14:17]
	v_mfma_f32_16x16x32_bf16 v[10:13], v[206:209], v[176:179], v[10:13]
	v_mfma_f32_16x16x32_bf16 v[6:9], v[198:201], v[184:187], v[6:9]
	v_mfma_f32_16x16x32_bf16 v[2:5], v[206:209], v[184:187], v[2:5]
	v_mfma_f32_16x16x32_bf16 v[46:49], v[202:205], v[164:167], v[46:49]
	v_mfma_f32_16x16x32_bf16 v[42:45], v[210:213], v[164:167], v[42:45]
	v_mfma_f32_16x16x32_bf16 v[30:33], v[202:205], v[172:175], v[30:33]
	v_mfma_f32_16x16x32_bf16 v[26:29], v[210:213], v[172:175], v[26:29]
	v_mfma_f32_16x16x32_bf16 v[14:17], v[202:205], v[180:183], v[14:17]
	v_mfma_f32_16x16x32_bf16 v[10:13], v[210:213], v[180:183], v[10:13]
	v_mfma_f32_16x16x32_bf16 v[6:9], v[202:205], v[188:191], v[6:9]
	v_mfma_f32_16x16x32_bf16 v[2:5], v[210:213], v[188:191], v[2:5]
	s_add_i32 s33, 0, 0x18000
	v_add_u32_e32 v156, s33, v141
	s_barrier
	ds_read_b128 v[144:147], v156
	ds_read_b128 v[148:151], v156 offset:1024
	ds_read_b128 v[152:155], v156 offset:2048
	ds_read_b128 v[156:159], v156 offset:3072
	s_add_u32 s0, s28, 0x40000
	s_addc_u32 s1, s29, 0
	s_mov_b32 m0, s69
	v_lshl_add_u64 v[198:199], s[0:1], 0, v[134:135]
	ds_read_b128 v[160:163], v143 offset:32768
	ds_read_b128 v[164:167], v143 offset:33792
	ds_read_b128 v[168:171], v143 offset:34816
	ds_read_b128 v[172:175], v143 offset:35840
	ds_read_b128 v[176:179], v143 offset:36864
	ds_read_b128 v[180:183], v143 offset:37888
	ds_read_b128 v[184:187], v143 offset:38912
	ds_read_b128 v[188:191], v143 offset:39936
	global_load_lds_dwordx4 v[198:199], off
	v_lshl_add_u64 v[198:199], s[0:1], 0, v[132:133]
	s_mov_b32 m0, s70
	s_nop 0
	global_load_lds_dwordx4 v[198:199], off
	s_waitcnt lgkmcnt(8)
	s_barrier
	s_waitcnt lgkmcnt(0)
	s_waitcnt lgkmcnt(0)
	v_mfma_f32_16x16x32_bf16 v[126:129], v[144:147], v[160:163], v[126:129]
	v_mfma_f32_16x16x32_bf16 v[122:125], v[152:155], v[160:163], v[122:125]
	v_mfma_f32_16x16x32_bf16 v[118:121], v[144:147], v[168:171], v[118:121]
	v_mfma_f32_16x16x32_bf16 v[114:117], v[152:155], v[168:171], v[114:117]
	v_mfma_f32_16x16x32_bf16 v[102:105], v[144:147], v[176:179], v[102:105]
	v_mfma_f32_16x16x32_bf16 v[98:101], v[152:155], v[176:179], v[98:101]
	v_mfma_f32_16x16x32_bf16 v[86:89], v[144:147], v[184:187], v[86:89]
	v_mfma_f32_16x16x32_bf16 v[82:85], v[152:155], v[184:187], v[82:85]
	v_mfma_f32_16x16x32_bf16 v[126:129], v[148:151], v[164:167], v[126:129]
	v_mfma_f32_16x16x32_bf16 v[122:125], v[156:159], v[164:167], v[122:125]
	v_mfma_f32_16x16x32_bf16 v[118:121], v[148:151], v[172:175], v[118:121]
	v_mfma_f32_16x16x32_bf16 v[114:117], v[156:159], v[172:175], v[114:117]
	v_mfma_f32_16x16x32_bf16 v[102:105], v[148:151], v[180:183], v[102:105]
	v_mfma_f32_16x16x32_bf16 v[98:101], v[156:159], v[180:183], v[98:101]
	v_mfma_f32_16x16x32_bf16 v[86:89], v[148:151], v[188:191], v[86:89]
	v_mfma_f32_16x16x32_bf16 v[82:85], v[156:159], v[188:191], v[82:85]
	s_barrier
	s_add_i32 s28, 0, 0x1c000
	s_add_i32 s0, s33, s64
	v_add_u32_e32 v196, s28, v141
	v_lshl_add_u64 v[192:193], v[192:193], 0, s[54:55]
	s_mov_b32 m0, s0
	ds_read_b128 v[198:201], v196
	ds_read_b128 v[202:205], v196 offset:1024
	ds_read_b128 v[206:209], v196 offset:2048
	ds_read_b128 v[210:213], v196 offset:3072
	global_load_lds_dwordx4 v[192:193], off
	v_lshl_add_u64 v[192:193], v[214:215], 0, s[54:55]
	s_add_i32 m0, s0, 0x2000
	s_nop 0
	global_load_lds_dwordx4 v[192:193], off
	s_barrier
	s_waitcnt lgkmcnt(0)
	s_waitcnt lgkmcnt(0)
	v_mfma_f32_16x16x32_bf16 v[110:113], v[198:201], v[160:163], v[110:113]
	v_mfma_f32_16x16x32_bf16 v[106:109], v[206:209], v[160:163], v[106:109]
	v_mfma_f32_16x16x32_bf16 v[94:97], v[198:201], v[168:171], v[94:97]
	v_mfma_f32_16x16x32_bf16 v[90:93], v[206:209], v[168:171], v[90:93]
	v_mfma_f32_16x16x32_bf16 v[78:81], v[198:201], v[176:179], v[78:81]
	v_mfma_f32_16x16x32_bf16 v[74:77], v[206:209], v[176:179], v[74:77]
	v_mfma_f32_16x16x32_bf16 v[70:73], v[198:201], v[184:187], v[70:73]
	v_mfma_f32_16x16x32_bf16 v[66:69], v[206:209], v[184:187], v[66:69]
	v_mfma_f32_16x16x32_bf16 v[110:113], v[202:205], v[164:167], v[110:113]
	v_mfma_f32_16x16x32_bf16 v[106:109], v[210:213], v[164:167], v[106:109]
	v_mfma_f32_16x16x32_bf16 v[94:97], v[202:205], v[172:175], v[94:97]
	v_mfma_f32_16x16x32_bf16 v[90:93], v[210:213], v[172:175], v[90:93]
	v_mfma_f32_16x16x32_bf16 v[78:81], v[202:205], v[180:183], v[78:81]
	v_mfma_f32_16x16x32_bf16 v[74:77], v[210:213], v[180:183], v[74:77]
	v_mfma_f32_16x16x32_bf16 v[70:73], v[202:205], v[188:191], v[70:73]
	v_mfma_f32_16x16x32_bf16 v[66:69], v[210:213], v[188:191], v[66:69]
	s_mov_b32 m0, s71
	v_lshl_add_u64 v[192:193], v[216:217], 0, s[54:55]
	s_barrier
	ds_read_b128 v[160:163], v143 offset:49152
	ds_read_b128 v[164:167], v143 offset:50176
	ds_read_b128 v[168:171], v143 offset:51200
	ds_read_b128 v[172:175], v143 offset:52224
	ds_read_b128 v[176:179], v143 offset:53248
	ds_read_b128 v[180:183], v143 offset:54272
	ds_read_b128 v[184:187], v143 offset:55296
	ds_read_b128 v[188:191], v143 offset:56320
	global_load_lds_dwordx4 v[192:193], off
	v_lshl_add_u64 v[192:193], v[218:219], 0, s[54:55]
	s_mov_b32 m0, s72
	s_nop 0
	global_load_lds_dwordx4 v[192:193], off
	s_barrier
	s_waitcnt lgkmcnt(0)
	s_waitcnt lgkmcnt(0)
	v_mfma_f32_16x16x32_bf16 v[62:65], v[144:147], v[160:163], v[62:65]
	v_mfma_f32_16x16x32_bf16 v[58:61], v[152:155], v[160:163], v[58:61]
	v_mfma_f32_16x16x32_bf16 v[54:57], v[144:147], v[168:171], v[54:57]
	v_mfma_f32_16x16x32_bf16 v[50:53], v[152:155], v[168:171], v[50:53]
	v_mfma_f32_16x16x32_bf16 v[38:41], v[144:147], v[176:179], v[38:41]
	v_mfma_f32_16x16x32_bf16 v[34:37], v[152:155], v[176:179], v[34:37]
	v_mfma_f32_16x16x32_bf16 v[22:25], v[144:147], v[184:187], v[22:25]
	v_mfma_f32_16x16x32_bf16 v[18:21], v[152:155], v[184:187], v[18:21]
	v_mfma_f32_16x16x32_bf16 v[62:65], v[148:151], v[164:167], v[62:65]
	v_mfma_f32_16x16x32_bf16 v[58:61], v[156:159], v[164:167], v[58:61]
	v_mfma_f32_16x16x32_bf16 v[54:57], v[148:151], v[172:175], v[54:57]
	v_mfma_f32_16x16x32_bf16 v[50:53], v[156:159], v[172:175], v[50:53]
	v_mfma_f32_16x16x32_bf16 v[38:41], v[148:151], v[180:183], v[38:41]
	v_mfma_f32_16x16x32_bf16 v[34:37], v[156:159], v[180:183], v[34:37]
	v_mfma_f32_16x16x32_bf16 v[22:25], v[148:151], v[188:191], v[22:25]
	v_mfma_f32_16x16x32_bf16 v[18:21], v[156:159], v[188:191], v[18:21]
	s_barrier
	s_add_u32 s0, s26, 0x40080
	s_addc_u32 s1, s27, 0
	s_add_i32 s26, s28, s64
	v_lshl_add_u64 v[144:145], s[0:1], 0, v[194:195]
	s_mov_b32 m0, s26
	s_nop 0
	global_load_lds_dwordx4 v[144:145], off
	v_lshl_add_u64 v[144:145], s[0:1], 0, v[130:131]
	s_add_i32 m0, s26, 0x2000
	s_nop 0
	global_load_lds_dwordx4 v[144:145], off
	s_waitcnt vmcnt(6)
	s_barrier
	v_mfma_f32_16x16x32_bf16 v[46:49], v[198:201], v[160:163], v[46:49]
	v_mfma_f32_16x16x32_bf16 v[42:45], v[206:209], v[160:163], v[42:45]
	v_mfma_f32_16x16x32_bf16 v[30:33], v[198:201], v[168:171], v[30:33]
	v_mfma_f32_16x16x32_bf16 v[26:29], v[206:209], v[168:171], v[26:29]
	v_mfma_f32_16x16x32_bf16 v[14:17], v[198:201], v[176:179], v[14:17]
	v_mfma_f32_16x16x32_bf16 v[10:13], v[206:209], v[176:179], v[10:13]
	v_mfma_f32_16x16x32_bf16 v[6:9], v[198:201], v[184:187], v[6:9]
	v_mfma_f32_16x16x32_bf16 v[2:5], v[206:209], v[184:187], v[2:5]
	v_mfma_f32_16x16x32_bf16 v[46:49], v[202:205], v[164:167], v[46:49]
	v_mfma_f32_16x16x32_bf16 v[42:45], v[210:213], v[164:167], v[42:45]
	v_mfma_f32_16x16x32_bf16 v[30:33], v[202:205], v[172:175], v[30:33]
	v_mfma_f32_16x16x32_bf16 v[26:29], v[210:213], v[172:175], v[26:29]
	v_mfma_f32_16x16x32_bf16 v[14:17], v[202:205], v[180:183], v[14:17]
	v_mfma_f32_16x16x32_bf16 v[10:13], v[210:213], v[180:183], v[10:13]
	v_mfma_f32_16x16x32_bf16 v[6:9], v[202:205], v[188:191], v[6:9]
	v_mfma_f32_16x16x32_bf16 v[2:5], v[210:213], v[188:191], v[2:5]
	s_add_i32 s82, s82, 2
	s_add_u32 s24, s24, 0x100
	s_addc_u32 s25, s25, 0
	s_add_u32 s78, s78, 0x100
	s_addc_u32 s79, s79, 0
	s_cmp_gt_u32 s82, 13
	s_barrier
	s_cbranch_scc0 .LBB0_1765
	v_lshl_add_u32 v144, s12, 8, v1
	v_lshl_or_b32 v146, s75, 8, v142
	v_ashrrev_i32_e32 v145, 31, v144
	v_lshlrev_b64 v[148:149], 11, v[144:145]
	v_ashrrev_i32_e32 v147, 31, v146
	v_lshl_add_u64 v[148:149], s[10:11], 0, v[148:149]
	v_cvt_pk_bf16_f32 v126, v126, v127
	v_cvt_pk_bf16_f32 v127, v128, v129
	v_cvt_pk_bf16_f32 v128, v122, v123
	v_lshlrev_b64 v[122:123], 1, v[146:147]
	v_cvt_pk_bf16_f32 v129, v124, v125
	v_lshl_add_u64 v[124:125], v[148:149], 0, v[122:123]
	s_mov_b64 s[0:1], 0x40000
	v_cvt_pk_bf16_f32 v62, v62, v63
	v_cvt_pk_bf16_f32 v63, v64, v65
	v_cvt_pk_bf16_f32 v64, v58, v59
	v_lshl_add_u64 v[58:59], v[124:125], 0, s[0:1]
	s_mov_b32 s0, 0x40000
	v_cvt_pk_bf16_f32 v110, v110, v111
	v_cvt_pk_bf16_f32 v111, v112, v113
	v_cvt_pk_bf16_f32 v112, v106, v107
	v_or_b32_e32 v106, 16, v144
	v_cvt_pk_bf16_f32 v65, v60, v61
	v_add_co_u32_e32 v60, vcc, s0, v124
	v_cvt_pk_bf16_f32 v46, v46, v47
	v_cvt_pk_bf16_f32 v47, v48, v49
	v_cvt_pk_bf16_f32 v48, v42, v43
	v_cvt_pk_bf16_f32 v49, v44, v45
	s_mov_b64 s[0:1], 0x48000
	v_ashrrev_i32_e32 v107, 31, v106
	v_addc_co_u32_e32 v61, vcc, 0, v125, vcc
	global_store_dwordx4 v[58:59], v[46:49], off offset:256
	v_cvt_pk_bf16_f32 v113, v108, v109
	v_lshlrev_b64 v[106:107], 11, v[106:107]
	v_lshl_add_u64 v[46:47], v[124:125], 0, s[0:1]
	s_mov_b32 s0, 0x48000
	v_cvt_pk_bf16_f32 v94, v94, v95
	v_cvt_pk_bf16_f32 v95, v96, v97
	v_cvt_pk_bf16_f32 v96, v90, v91
	v_or_b32_e32 v90, 32, v144
	v_add_co_u32_e32 v48, vcc, s0, v124
	v_cvt_pk_bf16_f32 v30, v30, v31
	v_cvt_pk_bf16_f32 v31, v32, v33
	v_cvt_pk_bf16_f32 v32, v26, v27
	v_cvt_pk_bf16_f32 v33, v28, v29
	s_mov_b64 s[0:1], 0x50000
	global_store_dwordx4 v[124:125], v[110:113], off offset:256
	v_ashrrev_i32_e32 v91, 31, v90
	v_addc_co_u32_e32 v49, vcc, 0, v125, vcc
	v_lshl_add_u64 v[110:111], s[10:11], 0, v[106:107]
	global_store_dwordx4 v[46:47], v[30:33], off offset:256
	v_lshl_add_u64 v[110:111], v[110:111], 0, v[122:123]
	v_cvt_pk_bf16_f32 v97, v92, v93
	v_lshl_add_u64 v[30:31], v[124:125], 0, s[0:1]
	s_mov_b32 s0, 0x50000
	v_lshlrev_b64 v[90:91], 11, v[90:91]
	v_cvt_pk_bf16_f32 v78, v78, v79
	v_cvt_pk_bf16_f32 v79, v80, v81
	v_cvt_pk_bf16_f32 v80, v74, v75
	v_or_b32_e32 v74, 48, v144
	v_add_co_u32_e32 v32, vcc, s0, v124
	v_cvt_pk_bf16_f32 v14, v14, v15
	v_cvt_pk_bf16_f32 v15, v16, v17
	v_cvt_pk_bf16_f32 v16, v10, v11
	v_cvt_pk_bf16_f32 v17, v12, v13
	s_mov_b64 s[0:1], 0x58000
	global_store_dwordx4 v[110:111], v[94:97], off offset:256
	v_ashrrev_i32_e32 v75, 31, v74
	v_addc_co_u32_e32 v33, vcc, 0, v125, vcc
	v_lshl_add_u64 v[94:95], s[10:11], 0, v[90:91]
	global_store_dwordx4 v[30:31], v[14:17], off offset:256
	v_lshl_add_u64 v[94:95], v[94:95], 0, v[122:123]
	v_cvt_pk_bf16_f32 v81, v76, v77
	v_lshl_add_u64 v[14:15], v[124:125], 0, s[0:1]
	s_mov_b32 s0, 0x58000
	v_lshlrev_b64 v[74:75], 11, v[74:75]
	v_add_co_u32_e32 v16, vcc, s0, v124
	global_store_dwordx4 v[94:95], v[78:81], off offset:256
	s_nop 0
	v_addc_co_u32_e32 v17, vcc, 0, v125, vcc
	v_lshl_add_u64 v[78:79], s[10:11], 0, v[74:75]
	v_cvt_pk_bf16_f32 v106, v118, v119
	v_cvt_pk_bf16_f32 v107, v120, v121
	v_cvt_pk_bf16_f32 v108, v114, v115
	v_cvt_pk_bf16_f32 v109, v116, v117
	v_cvt_pk_bf16_f32 v90, v102, v103
	v_cvt_pk_bf16_f32 v91, v104, v105
	v_cvt_pk_bf16_f32 v92, v98, v99
	v_cvt_pk_bf16_f32 v93, v100, v101
	v_cvt_pk_bf16_f32 v74, v86, v87
	v_cvt_pk_bf16_f32 v75, v88, v89
	v_cvt_pk_bf16_f32 v76, v82, v83
	v_cvt_pk_bf16_f32 v77, v84, v85
	v_lshl_add_u64 v[78:79], v[78:79], 0, v[122:123]
	v_cvt_pk_bf16_f32 v70, v70, v71
	v_cvt_pk_bf16_f32 v71, v72, v73
	v_cvt_pk_bf16_f32 v72, v66, v67
	v_cvt_pk_bf16_f32 v73, v68, v69
	v_cvt_pk_bf16_f32 v42, v54, v55
	v_cvt_pk_bf16_f32 v43, v56, v57
	v_cvt_pk_bf16_f32 v44, v50, v51
	v_cvt_pk_bf16_f32 v45, v52, v53
	v_cvt_pk_bf16_f32 v26, v38, v39
	v_cvt_pk_bf16_f32 v27, v40, v41
	v_cvt_pk_bf16_f32 v28, v34, v35
	v_cvt_pk_bf16_f32 v29, v36, v37
	v_cvt_pk_bf16_f32 v10, v22, v23
	v_cvt_pk_bf16_f32 v11, v24, v25
	v_cvt_pk_bf16_f32 v12, v18, v19
	v_cvt_pk_bf16_f32 v13, v20, v21
	v_cvt_pk_bf16_f32 v6, v6, v7
	v_cvt_pk_bf16_f32 v7, v8, v9
	v_cvt_pk_bf16_f32 v8, v2, v3
	v_cvt_pk_bf16_f32 v9, v4, v5
	s_and_b64 vcc, exec, s[4:5]
	s_mov_b32 s75, s14
	s_mov_b32 s12, s18
	s_mov_b64 s[26:27], s[22:23]
	s_mov_b64 s[24:25], s[20:21]
	global_store_dwordx4 v[124:125], v[126:129], off
	global_store_dwordx4 v[110:111], v[106:109], off
	global_store_dwordx4 v[94:95], v[90:93], off
	global_store_dwordx4 v[78:79], v[74:77], off
	global_store_dwordx4 v[78:79], v[70:73], off offset:256
	global_store_dwordx4 v[60:61], v[62:65], off
	global_store_dwordx4 v[48:49], v[42:45], off
	global_store_dwordx4 v[32:33], v[26:29], off
	global_store_dwordx4 v[16:17], v[10:13], off
	global_store_dwordx4 v[14:15], v[6:9], off offset:256
	s_cbranch_vccz .LBB0_1762
	s_waitcnt vmcnt(0)
	s_cmpk_gt_u32 s34, 0xff
	s_cbranch_scc1 .LBB0_1769
	s_barrier

.LBB0_2193:
	s_mov_b64 s[0:1], s[8:9]
	s_load_dword s0, s[0:1], 0x110
	s_waitcnt lgkmcnt(0)
	s_cmp_gt_i32 s0, s2
	s_cbranch_scc1 .LBB0_2251
	s_mov_b64 s[0:1], s[8:9]
	s_load_dword s0, s[0:1], 0x114
	s_waitcnt lgkmcnt(0)
	s_cmp_ge_i32 s2, s0
	s_cbranch_scc1 .LBB0_2250
	v_readlane_b32 s0, v254, 2
	v_readlane_b32 s1, v254, 3
	s_load_dword s1, s[0:1], 0x110
	s_add_i32 s0, s41, 7
	s_waitcnt lgkmcnt(0)
	s_cmp_gt_i32 s1, s0
	s_cbranch_scc1 .LBB0_2250
	v_readlane_b32 s2, v254, 2
	v_readlane_b32 s3, v254, 3
	s_load_dword s1, s[2:3], 0x114
	s_waitcnt lgkmcnt(0)
	s_cmp_ge_i32 s0, s1
	s_cbranch_scc1 .LBB0_2250
	v_readlane_b32 s6, v254, 2
	v_mov_b32_e32 v1, v0
	v_readlane_b32 s7, v254, 3
	v_readlane_b32 s0, v254, 0
	s_load_dword s1, s[6:7], 0x118
	s_waitcnt lgkmcnt(0)
	s_setprio 0
	s_getreg_b32 s0, hwreg(HW_REG_XCC_ID, 0, 4)
	s_waitcnt vmcnt(0)
	s_barrier
	s_mov_b64 s[4:5], exec
	v_readlane_b32 s2, v254, 6
	v_readlane_b32 s3, v254, 7
	s_and_b64 s[2:3], s[4:5], s[2:3]
	s_mov_b64 exec, s[2:3]
	s_cbranch_execz .LBB0_2249
	s_add_i32 s3, 0, 0x26000
	v_mov_b32_e32 v1, s3
	s_load_dwordx2 s[6:7], s[6:7], 0x108
	s_waitcnt vmcnt(0) expcnt(0) lgkmcnt(0)
	ds_read_b32 v3, v1
	v_readlane_b32 s1, v254, 8
	s_and_b32 s2, s0, 15
	s_waitcnt lgkmcnt(0)
	v_cmp_ne_u32_e32 vcc, 0, v3
	v_mov_b32_e32 v1, s1
	ds_read_b32 v2, v1
	s_cbranch_vccnz .LBB0_2213
	v_readlane_b32 s8, v254, 4
	v_readlane_b32 s12, v254, 2
	v_readlane_b32 s9, v254, 5
	v_readlane_b32 s13, v254, 3
	s_load_dwordx2 s[0:1], s[8:9], 0x4
	s_nop 0
	s_load_dword s12, s[12:13], 0x118
	s_add_u32 s8, s6, 0x4200
	s_addc_u32 s9, s7, 0
	s_add_u32 s10, s6, 0x4400
	s_addc_u32 s11, s7, 0
	s_waitcnt lgkmcnt(0)
	s_mul_i32 s34, s0, s12
	s_add_u32 s12, s6, 0x4500
	s_addc_u32 s13, s7, 0
	s_add_u32 s14, s6, 0x4600
	s_addc_u32 s15, s7, 0
	s_add_u32 s16, s6, 0x4700
	s_addc_u32 s17, s7, 0
	s_add_u32 s18, s6, 0x4800
	s_addc_u32 s19, s7, 0
	s_add_u32 s20, s6, 0x4900
	s_addc_u32 s21, s7, 0
	s_add_u32 s22, s6, 0x4a00
	s_addc_u32 s23, s7, 0
	s_add_u32 s24, s6, 0x4b00
	s_addc_u32 s25, s7, 0
	s_add_u32 s26, s6, 0x4c00
	s_addc_u32 s27, s7, 0
	s_add_u32 s28, s6, 0x4d00
	s_addc_u32 s29, s7, 0
	s_add_u32 s30, s6, 0x4e00
	s_addc_u32 s31, s7, 0
	s_add_u32 s64, s6, 0x4f00
	s_addc_u32 s65, s7, 0
	s_add_u32 s66, s6, 0x5000
	s_addc_u32 s67, s7, 0
	s_add_u32 s68, s6, 0x5100
	s_addc_u32 s69, s7, 0
	s_add_u32 s70, s6, 0x5200
	s_addc_u32 s71, s7, 0
	s_add_u32 s72, s6, 0x5300
	s_mul_i32 s34, s34, s1
	s_addc_u32 s73, s7, 0
	s_mov_b32 s0, 1
	s_branch .LBB0_2201

.LBB0_2263:
	s_mov_b64 s[0:1], s[6:7]
	s_load_dword s0, s[0:1], 0x110
	s_waitcnt lgkmcnt(0)
	s_cmp_gt_i32 s0, s2
	s_cbranch_scc1 .LBB0_2321
	s_mov_b64 s[0:1], s[6:7]
	s_load_dword s0, s[0:1], 0x114
	s_waitcnt lgkmcnt(0)
	s_cmp_ge_i32 s2, s0
	s_cbranch_scc1 .LBB0_2320
	v_readlane_b32 s0, v254, 2
	v_readlane_b32 s1, v254, 3
	s_load_dword s1, s[0:1], 0x110
	s_add_i32 s0, s41, 8
	s_waitcnt lgkmcnt(0)
	s_cmp_gt_i32 s1, s0
	s_cbranch_scc1 .LBB0_2320
	v_readlane_b32 s2, v254, 2
	v_readlane_b32 s3, v254, 3
	s_load_dword s1, s[2:3], 0x114
	s_waitcnt lgkmcnt(0)
	s_cmp_ge_i32 s0, s1
	s_cbranch_scc1 .LBB0_2320
	v_readlane_b32 s6, v254, 2
	v_mov_b32_e32 v1, v0
	v_readlane_b32 s7, v254, 3
	s_load_dword s0, s[6:7], 0x118
	v_readlane_b32 s1, v254, 0
	s_waitcnt lgkmcnt(0)
	s_setprio 0
	s_getreg_b32 s0, hwreg(HW_REG_XCC_ID, 0, 4)
	s_waitcnt vmcnt(0)
	s_barrier
	s_mov_b64 s[4:5], exec
	v_readlane_b32 s2, v254, 6
	v_readlane_b32 s3, v254, 7
	s_and_b64 s[2:3], s[4:5], s[2:3]
	s_mov_b64 exec, s[2:3]
	s_cbranch_execz .LBB0_2319
	s_add_i32 s3, 0, 0x26000
	v_mov_b32_e32 v1, s3
	s_load_dwordx2 s[6:7], s[6:7], 0x108
	s_waitcnt vmcnt(0) expcnt(0) lgkmcnt(0)
	ds_read_b32 v3, v1
	v_readlane_b32 s1, v254, 8
	s_and_b32 s2, s0, 15
	s_waitcnt lgkmcnt(0)
	v_cmp_ne_u32_e32 vcc, 0, v3
	v_mov_b32_e32 v1, s1
	ds_read_b32 v2, v1
	s_cbranch_vccnz .LBB0_2283
	v_readlane_b32 s8, v254, 4
	v_readlane_b32 s12, v254, 2
	v_readlane_b32 s9, v254, 5
	v_readlane_b32 s13, v254, 3
	s_load_dwordx2 s[0:1], s[8:9], 0x4
	s_nop 0
	s_load_dword s12, s[12:13], 0x118
	s_add_u32 s8, s6, 0x4200
	s_addc_u32 s9, s7, 0
	s_add_u32 s10, s6, 0x4400
	s_addc_u32 s11, s7, 0
	s_waitcnt lgkmcnt(0)
	s_mul_i32 s34, s0, s12
	s_add_u32 s12, s6, 0x4500
	s_addc_u32 s13, s7, 0
	s_add_u32 s14, s6, 0x4600
	s_addc_u32 s15, s7, 0
	s_add_u32 s16, s6, 0x4700
	s_addc_u32 s17, s7, 0
	s_add_u32 s18, s6, 0x4800
	s_addc_u32 s19, s7, 0
	s_add_u32 s20, s6, 0x4900
	s_addc_u32 s21, s7, 0
	s_add_u32 s22, s6, 0x4a00
	s_addc_u32 s23, s7, 0
	s_add_u32 s24, s6, 0x4b00
	s_addc_u32 s25, s7, 0
	s_add_u32 s26, s6, 0x4c00
	s_addc_u32 s27, s7, 0
	s_add_u32 s28, s6, 0x4d00
	s_addc_u32 s29, s7, 0
	s_add_u32 s30, s6, 0x4e00
	s_addc_u32 s31, s7, 0
	s_add_u32 s64, s6, 0x4f00
	s_addc_u32 s65, s7, 0
	s_add_u32 s66, s6, 0x5000
	s_addc_u32 s67, s7, 0
	s_add_u32 s68, s6, 0x5100
	s_addc_u32 s69, s7, 0
	s_add_u32 s70, s6, 0x5200
	s_addc_u32 s71, s7, 0
	s_add_u32 s72, s6, 0x5300
	s_mul_i32 s34, s34, s1
	s_addc_u32 s73, s7, 0
	s_mov_b32 s0, 1
	s_branch .LBB0_2271

.LBB0_2391:
	s_mov_b64 s[0:1], s[4:5]
	s_load_dword s0, s[0:1], 0x110
	s_waitcnt lgkmcnt(0)
	s_cmp_gt_i32 s0, s2
	s_cbranch_scc1 .LBB0_2449
	s_mov_b64 s[0:1], s[4:5]
	s_load_dword s0, s[0:1], 0x114
	s_waitcnt lgkmcnt(0)
	s_cmp_ge_i32 s2, s0
	s_cbranch_scc1 .LBB0_2448
	v_readlane_b32 s0, v254, 2
	v_readlane_b32 s1, v254, 3
	s_load_dword s1, s[0:1], 0x110
	s_add_i32 s0, s41, 9
	s_waitcnt lgkmcnt(0)
	s_cmp_gt_i32 s1, s0
	s_cbranch_scc1 .LBB0_2448
	v_readlane_b32 s2, v254, 2
	v_readlane_b32 s3, v254, 3
	s_load_dword s1, s[2:3], 0x114
	s_waitcnt lgkmcnt(0)
	s_cmp_ge_i32 s0, s1
	s_cbranch_scc1 .LBB0_2448
	v_readlane_b32 s6, v254, 2
	v_mov_b32_e32 v1, v0
	v_readlane_b32 s7, v254, 3
	v_readlane_b32 s0, v254, 0
	s_load_dword s1, s[6:7], 0x118
	s_waitcnt lgkmcnt(0)
	s_setprio 0
	s_getreg_b32 s0, hwreg(HW_REG_XCC_ID, 0, 4)
	s_waitcnt vmcnt(0)
	s_barrier
	s_mov_b64 s[4:5], exec
	v_readlane_b32 s2, v254, 6
	v_readlane_b32 s3, v254, 7
	s_and_b64 s[2:3], s[4:5], s[2:3]
	s_mov_b64 exec, s[2:3]
	s_cbranch_execz .LBB0_2447
	s_add_i32 s3, 0, 0x26000
	v_mov_b32_e32 v1, s3
	s_load_dwordx2 s[6:7], s[6:7], 0x108
	s_waitcnt vmcnt(0) expcnt(0) lgkmcnt(0)
	ds_read_b32 v3, v1
	v_readlane_b32 s1, v254, 8
	s_and_b32 s2, s0, 15
	s_waitcnt lgkmcnt(0)
	v_cmp_ne_u32_e32 vcc, 0, v3
	v_mov_b32_e32 v1, s1
	ds_read_b32 v2, v1
	s_cbranch_vccnz .LBB0_2411
	v_readlane_b32 s8, v254, 4
	v_readlane_b32 s12, v254, 2
	v_readlane_b32 s9, v254, 5
	v_readlane_b32 s13, v254, 3
	s_load_dwordx2 s[0:1], s[8:9], 0x4
	s_nop 0
	s_load_dword s12, s[12:13], 0x118
	s_add_u32 s8, s6, 0x4200
	s_addc_u32 s9, s7, 0
	s_add_u32 s10, s6, 0x4400
	s_addc_u32 s11, s7, 0
	s_waitcnt lgkmcnt(0)
	s_mul_i32 s34, s0, s12
	s_add_u32 s12, s6, 0x4500
	s_addc_u32 s13, s7, 0
	s_add_u32 s14, s6, 0x4600
	s_addc_u32 s15, s7, 0
	s_add_u32 s16, s6, 0x4700
	s_addc_u32 s17, s7, 0
	s_add_u32 s18, s6, 0x4800
	s_addc_u32 s19, s7, 0
	s_add_u32 s20, s6, 0x4900
	s_addc_u32 s21, s7, 0
	s_add_u32 s22, s6, 0x4a00
	s_addc_u32 s23, s7, 0
	s_add_u32 s24, s6, 0x4b00
	s_addc_u32 s25, s7, 0
	s_add_u32 s26, s6, 0x4c00
	s_addc_u32 s27, s7, 0
	s_add_u32 s28, s6, 0x4d00
	s_addc_u32 s29, s7, 0
	s_add_u32 s30, s6, 0x4e00
	s_addc_u32 s31, s7, 0
	s_add_u32 s64, s6, 0x4f00
	s_addc_u32 s65, s7, 0
	s_add_u32 s66, s6, 0x5000
	s_addc_u32 s67, s7, 0
	s_add_u32 s68, s6, 0x5100
	s_addc_u32 s69, s7, 0
	s_add_u32 s70, s6, 0x5200
	s_addc_u32 s71, s7, 0
	s_add_u32 s72, s6, 0x5300
	s_mul_i32 s34, s34, s1
	s_addc_u32 s73, s7, 0
	s_mov_b32 s0, 1
	s_branch .LBB0_2399

.LBB0_2461:
	s_and_b64 vcc, exec, s[10:11]
	s_cbranch_vccz .LBB0_2480
	v_ashrrev_i32_e32 v1, 31, v10
	v_lshrrev_b32_e32 v1, 26, v1
	v_add_u32_e32 v1, v10, v1
	v_ashrrev_i32_e32 v11, 6, v1
	v_bfe_i32 v1, v10, 27, 1
	v_lshlrev_b32_e32 v2, 4, v10
	v_lshrrev_b32_e32 v1, 22, v1
	v_add_u32_e32 v1, v2, v1
	v_and_b32_e32 v1, 0xfffffc00, v1
	v_sub_u32_e32 v1, v2, v1
	v_lshrrev_b32_e32 v3, 4, v1
	v_bitop3_b32 v12, v3, v1, 32 bitop3:0x6c
	v_ashrrev_i32_e32 v3, 31, v12
	v_lshrrev_b32_e32 v3, 26, v3
	v_add_u32_e32 v2, 0x2000, v2
	v_add_u32_e32 v13, v12, v3
	v_ashrrev_i32_e32 v3, 31, v2
	v_lshrrev_b32_e32 v3, 22, v3
	v_add_u32_e32 v3, v2, v3
	v_ashrrev_i32_e32 v15, 10, v3
	v_mul_i32_i24_e32 v3, 0x400, v15
	v_sub_u32_e32 v2, v2, v3
	v_lshrrev_b32_e32 v3, 4, v2
	v_bitop3_b32 v16, v3, v2, 32 bitop3:0x6c
	s_add_u32 s31, s6, 0xa700000
	v_ashrrev_i32_e32 v3, 31, v16
	s_addc_u32 s34, s7, 0
	v_lshrrev_b32_e32 v3, 26, v3
	s_add_u32 s10, s6, 0x700000
	v_lshlrev_b32_e32 v1, 3, v11
	v_lshlrev_b32_e32 v2, 3, v15
	v_add_u32_e32 v17, v16, v3
	s_addc_u32 s11, s7, 0
	v_and_b32_e32 v1, -16, v1
	v_ashrrev_i32_e32 v14, 6, v13
	v_and_b32_e32 v2, -16, v2
	v_ashrrev_i32_e32 v18, 6, v17
	s_ashr_i32 s73, s12, 2
	v_add_u32_e32 v1, v14, v1
	v_add_u32_e32 v148, v18, v2
	s_lshl_b32 s0, s73, 8
	v_add_u32_e32 v2, s0, v1
	v_add_u32_e32 v4, s0, v148
	s_bitset1_b32 s0, 7
	v_ashrrev_i32_e32 v3, 31, v2
	v_ashrrev_i32_e32 v5, 31, v4
	v_add_u32_e32 v6, s0, v1
	v_add_u32_e32 v8, s0, v148
	v_lshl_add_u64 v[2:3], v[2:3], 2, s[10:11]
	v_lshl_add_u64 v[4:5], v[4:5], 2, s[10:11]
	v_ashrrev_i32_e32 v7, 31, v6
	s_waitcnt vmcnt(0)
	v_ashrrev_i32_e32 v9, 31, v8
	v_lshl_add_u64 v[6:7], v[6:7], 2, s[10:11]
	v_lshl_add_u64 v[8:9], v[8:9], 2, s[10:11]
	global_load_dword v2, v[2:3], off
	s_nop 0
	global_load_dword v3, v[4:5], off
	s_nop 0
	global_load_dword v4, v[6:7], off
	global_load_dword v5, v[8:9], off
	v_and_b32_e32 v7, 0xc0, v13
	v_sub_u32_e32 v7, v12, v7
	v_lshlrev_b32_e32 v6, 5, v11
	v_ashrrev_i16_sdwa v7, v226, sext(v7) dst_sel:DWORD dst_unused:UNUSED_PAD src0_sel:DWORD src1_sel:BYTE_0
	v_lshlrev_b32_e32 v8, 1, v1
	v_lshrrev_b32_e32 v9, 2, v1
	v_and_b32_e32 v11, 3, v14
	s_mov_b32 s1, 0x1fffe0
	v_and_b32_e32 v6, 32, v6
	v_bfe_i32 v7, v7, 0, 16
	v_and_b32_e32 v8, 24, v8
	v_and_b32_e32 v9, 4, v9
	v_and_or_b32 v11, v1, s1, v11
	v_or3_b32 v8, v11, v9, v8
	v_add_lshl_u32 v149, v6, v7, 1
	v_and_b32_e32 v7, 0xc0, v17
	v_and_b32_e32 v11, 3, v18
	v_sub_u32_e32 v7, v16, v7
	v_and_or_b32 v11, v148, s1, v11
	s_and_b32 s1, s12, -4
	v_lshlrev_b32_e32 v6, 5, v15
	v_ashrrev_i16_sdwa v7, v226, sext(v7) dst_sel:DWORD dst_unused:UNUSED_PAD src0_sel:DWORD src1_sel:BYTE_0
	s_add_i32 s1, s1, 0
	v_and_b32_e32 v6, 32, v6
	v_bfe_i32 v7, v7, 0, 16
	s_add_i32 s1, s1, 0x26200
	v_add_lshl_u32 v150, v6, v7, 1
	v_mov_b32_e32 v6, s1
	ds_read_b32 v6, v6
	s_and_b32 s74, s12, 3
	s_ashr_i32 s1, s29, 6
	s_ashr_i32 s0, s29, 8
	s_lshl_b32 s35, s1, 10
	s_waitcnt lgkmcnt(0)
	v_readfirstlane_b32 s12, v6
	s_ashr_i32 s13, s12, 31
	s_lshl_b64 s[12:13], s[12:13], 21
	s_lshl_b32 s15, s74, 19
	s_add_u32 s12, s31, s12
	s_addc_u32 s13, s34, s13
	v_lshl_add_u32 v130, v8, 11, v149
	v_lshlrev_b32_e32 v8, 1, v148
	v_lshrrev_b32_e32 v9, 2, v148
	s_add_u32 s20, s12, s15
	v_and_b32_e32 v8, 24, v8
	v_and_b32_e32 v9, 4, v9
	s_addc_u32 s21, s13, 0
	s_add_i32 s38, s35, 0
	v_or3_b32 v8, v11, v9, v8
	s_add_i32 m0, s38, 0x10000
	v_lshl_add_u32 v132, v8, 11, v150
	global_load_lds_dwordx4 v130, s[20:21]
	s_add_i32 m0, s38, 0x12000
	s_add_i32 s40, s38, 0x2000
	global_load_lds_dwordx4 v132, s[20:21]
	s_mov_b32 m0, s38
	s_add_u32 s12, s20, 0x40000
	s_addc_u32 s13, s21, 0
	s_add_i32 s43, s38, 0x4000
	s_add_i32 s64, s38, 0x6000
	v_mov_b32_e32 v131, v195
	v_mov_b32_e32 v133, v195
	v_mov_b32_e32 v137, v195
	v_mov_b32_e32 v139, v195
	v_lshl_add_u64 v[8:9], s[20:21], 0, v[130:131]
	v_lshl_add_u64 v[6:7], s[20:21], 0, v[132:133]
	s_waitcnt vmcnt(0)
	v_lshl_add_u32 v136, v2, 11, v149
	v_lshl_add_u32 v138, v3, 11, v150
	global_load_lds_dwordx4 v136, s[4:5]
	s_mov_b32 m0, s40
	v_lshl_add_u32 v140, v4, 11, v149
	global_load_lds_dwordx4 v138, s[4:5]
	s_add_i32 m0, s38, 0x14000
	v_lshl_add_u32 v142, v5, 11, v150
	global_load_lds_dwordx4 v130, s[12:13]
	s_add_i32 m0, s38, 0x16000
	v_lshl_add_u64 v[4:5], s[4:5], 0, v[136:137]
	global_load_lds_dwordx4 v132, s[12:13]
	s_mov_b32 m0, s43
	s_cmp_lg_u32 s0, 1
	global_load_lds_dwordx4 v140, s[4:5]
	s_mov_b32 m0, s64
	v_lshl_add_u64 v[2:3], s[4:5], 0, v[138:139]
	global_load_lds_dwordx4 v142, s[4:5]
	s_setprio 1
	s_cbranch_scc1 .LBB0_2464
	s_barrier
	s_setprio 0

.LBB0_2475:
	s_add_u32 s22, s20, 0x100
	s_addc_u32 s23, s21, 0
	s_add_u32 s24, s75, s20
	s_addc_u32 s25, s76, s21
	s_cmpk_eq_i32 s20, 0x700
	s_cselect_b64 vcc, -1, 0
	s_and_b64 s[0:1], vcc, exec
	s_cselect_b32 s0, 0, s22
	s_cselect_b32 s25, s13, s25
	s_cselect_b32 s24, s15, s24
	s_add_i32 s1, 0, 0x10000
	v_add_u32_e32 v141, s1, v139
	ds_read_b128 v[160:163], v141
	ds_read_b128 v[164:167], v141 offset:1024
	ds_read_b128 v[168:171], v141 offset:2048
	ds_read_b128 v[172:175], v141 offset:3072
	s_add_u32 s26, s4, s0
	v_cndmask_b32_e32 v194, v136, v155, vcc
	v_cndmask_b32_e32 v192, v138, v156, vcc
	v_cndmask_b32_e32 v141, v140, v157, vcc
	v_cndmask_b32_e32 v143, v142, v158, vcc
	s_addc_u32 s27, s5, 0
	v_lshl_add_u64 v[214:215], v[146:147], 0, s[20:21]
	s_add_i32 m0, s38, 0xc000
	ds_read_b128 v[176:179], v154
	ds_read_b128 v[180:183], v154 offset:1024
	ds_read_b128 v[184:187], v154 offset:2048
	ds_read_b128 v[188:191], v154 offset:3072
	ds_read_b128 v[198:201], v154 offset:4096
	ds_read_b128 v[202:205], v154 offset:5120
	ds_read_b128 v[206:209], v154 offset:6144
	ds_read_b128 v[210:213], v154 offset:7168
	global_load_lds_dwordx4 v[214:215], off
	v_lshl_add_u64 v[214:215], v[144:145], 0, s[20:21]
	s_add_i32 m0, s38, 0xe000
	s_nop 0
	global_load_lds_dwordx4 v[214:215], off
	s_waitcnt lgkmcnt(8)
	s_barrier
	s_waitcnt lgkmcnt(0)
	s_waitcnt lgkmcnt(0)
	v_mfma_f32_16x16x32_bf16 v[126:129], v[160:163], v[176:179], v[126:129]
	v_mfma_f32_16x16x32_bf16 v[122:125], v[168:171], v[176:179], v[122:125]
	v_mfma_f32_16x16x32_bf16 v[118:121], v[160:163], v[184:187], v[118:121]
	v_mfma_f32_16x16x32_bf16 v[114:117], v[168:171], v[184:187], v[114:117]
	v_mfma_f32_16x16x32_bf16 v[94:97], v[160:163], v[198:201], v[94:97]
	v_mfma_f32_16x16x32_bf16 v[90:93], v[168:171], v[198:201], v[90:93]
	v_mfma_f32_16x16x32_bf16 v[86:89], v[160:163], v[206:209], v[86:89]
	v_mfma_f32_16x16x32_bf16 v[82:85], v[168:171], v[206:209], v[82:85]
	v_mfma_f32_16x16x32_bf16 v[126:129], v[164:167], v[180:183], v[126:129]
	v_mfma_f32_16x16x32_bf16 v[122:125], v[172:175], v[180:183], v[122:125]
	v_mfma_f32_16x16x32_bf16 v[118:121], v[164:167], v[188:191], v[118:121]
	v_mfma_f32_16x16x32_bf16 v[114:117], v[172:175], v[188:191], v[114:117]
	v_mfma_f32_16x16x32_bf16 v[94:97], v[164:167], v[202:205], v[94:97]
	v_mfma_f32_16x16x32_bf16 v[90:93], v[172:175], v[202:205], v[90:93]
	v_mfma_f32_16x16x32_bf16 v[86:89], v[164:167], v[210:213], v[86:89]
	v_mfma_f32_16x16x32_bf16 v[82:85], v[172:175], v[210:213], v[82:85]
	s_barrier
	s_add_i32 s20, 0, 0x14000
	s_add_i32 s0, s1, s35
	v_add_u32_e32 v159, s20, v139
	v_lshl_add_u64 v[224:225], s[24:25], 0, v[130:131]
	s_mov_b32 m0, s0
	ds_read_b128 v[214:217], v159
	ds_read_b128 v[218:221], v159 offset:1024
	ds_read_b128 v[238:241], v159 offset:2048
	ds_read_b128 v[242:245], v159 offset:3072
	global_load_lds_dwordx4 v[224:225], off
	v_lshl_add_u64 v[230:231], s[24:25], 0, v[132:133]
	s_add_i32 m0, s0, 0x2000
	s_nop 0
	global_load_lds_dwordx4 v[230:231], off
	s_barrier
	s_waitcnt lgkmcnt(0)
	s_waitcnt lgkmcnt(0)
	v_mfma_f32_16x16x32_bf16 v[110:113], v[214:217], v[176:179], v[110:113]
	v_mfma_f32_16x16x32_bf16 v[106:109], v[238:241], v[176:179], v[106:109]
	v_mfma_f32_16x16x32_bf16 v[102:105], v[214:217], v[184:187], v[102:105]
	v_mfma_f32_16x16x32_bf16 v[98:101], v[238:241], v[184:187], v[98:101]
	v_mfma_f32_16x16x32_bf16 v[78:81], v[214:217], v[198:201], v[78:81]
	v_mfma_f32_16x16x32_bf16 v[74:77], v[238:241], v[198:201], v[74:77]
	v_mfma_f32_16x16x32_bf16 v[70:73], v[214:217], v[206:209], v[70:73]
	v_mfma_f32_16x16x32_bf16 v[66:69], v[238:241], v[206:209], v[66:69]
	v_mfma_f32_16x16x32_bf16 v[110:113], v[218:221], v[180:183], v[110:113]
	v_mfma_f32_16x16x32_bf16 v[106:109], v[242:245], v[180:183], v[106:109]
	v_mfma_f32_16x16x32_bf16 v[102:105], v[218:221], v[188:191], v[102:105]
	v_mfma_f32_16x16x32_bf16 v[98:101], v[242:245], v[188:191], v[98:101]
	v_mfma_f32_16x16x32_bf16 v[78:81], v[218:221], v[202:205], v[78:81]
	v_mfma_f32_16x16x32_bf16 v[74:77], v[242:245], v[202:205], v[74:77]
	v_mfma_f32_16x16x32_bf16 v[70:73], v[218:221], v[210:213], v[70:73]
	v_mfma_f32_16x16x32_bf16 v[66:69], v[242:245], v[210:213], v[66:69]
	s_mov_b32 m0, s38
	s_barrier
	ds_read_b128 v[176:179], v154 offset:16384
	ds_read_b128 v[180:183], v154 offset:17408
	ds_read_b128 v[184:187], v154 offset:18432
	ds_read_b128 v[188:191], v154 offset:19456
	ds_read_b128 v[198:201], v154 offset:20480
	ds_read_b128 v[202:205], v154 offset:21504
	ds_read_b128 v[206:209], v154 offset:22528
	ds_read_b128 v[210:213], v154 offset:23552
	global_load_lds_dwordx4 v194, s[26:27]
	s_mov_b32 m0, s40
	v_mov_b32_e32 v193, v195
	global_load_lds_dwordx4 v192, s[26:27]
	s_barrier
	s_waitcnt lgkmcnt(0)
	v_lshl_add_u64 v[232:233], s[26:27], 0, v[194:195]
	v_lshl_add_u64 v[192:193], s[26:27], 0, v[192:193]
	s_waitcnt lgkmcnt(0)
	v_mfma_f32_16x16x32_bf16 v[62:65], v[160:163], v[176:179], v[62:65]
	v_mfma_f32_16x16x32_bf16 v[58:61], v[168:171], v[176:179], v[58:61]
	v_mfma_f32_16x16x32_bf16 v[54:57], v[160:163], v[184:187], v[54:57]
	v_mfma_f32_16x16x32_bf16 v[50:53], v[168:171], v[184:187], v[50:53]
	v_mfma_f32_16x16x32_bf16 v[30:33], v[160:163], v[198:201], v[30:33]
	v_mfma_f32_16x16x32_bf16 v[26:29], v[168:171], v[198:201], v[26:29]
	v_mfma_f32_16x16x32_bf16 v[22:25], v[160:163], v[206:209], v[22:25]
	v_mfma_f32_16x16x32_bf16 v[18:21], v[168:171], v[206:209], v[18:21]
	v_mfma_f32_16x16x32_bf16 v[62:65], v[164:167], v[180:183], v[62:65]
	v_mfma_f32_16x16x32_bf16 v[58:61], v[172:175], v[180:183], v[58:61]
	v_mfma_f32_16x16x32_bf16 v[54:57], v[164:167], v[188:191], v[54:57]
	v_mfma_f32_16x16x32_bf16 v[50:53], v[172:175], v[188:191], v[50:53]
	v_mfma_f32_16x16x32_bf16 v[30:33], v[164:167], v[202:205], v[30:33]
	v_mfma_f32_16x16x32_bf16 v[26:29], v[172:175], v[202:205], v[26:29]
	v_mfma_f32_16x16x32_bf16 v[22:25], v[164:167], v[210:213], v[22:25]
	v_mfma_f32_16x16x32_bf16 v[18:21], v[172:175], v[210:213], v[18:21]
	s_barrier
	s_add_u32 s0, s24, 0x40000
	s_addc_u32 s1, s25, 0
	s_add_i32 s20, s20, s35
	v_lshl_add_u64 v[160:161], s[0:1], 0, v[130:131]
	s_mov_b32 m0, s20
	s_nop 0
	global_load_lds_dwordx4 v[160:161], off
	v_lshl_add_u64 v[160:161], s[0:1], 0, v[132:133]
	s_add_i32 m0, s20, 0x2000
	s_nop 0
	global_load_lds_dwordx4 v[160:161], off
	s_waitcnt vmcnt(6)
	s_barrier
	v_mfma_f32_16x16x32_bf16 v[46:49], v[214:217], v[176:179], v[46:49]
	v_mfma_f32_16x16x32_bf16 v[42:45], v[238:241], v[176:179], v[42:45]
	v_mfma_f32_16x16x32_bf16 v[38:41], v[214:217], v[184:187], v[38:41]
	v_mfma_f32_16x16x32_bf16 v[34:37], v[238:241], v[184:187], v[34:37]
	v_mfma_f32_16x16x32_bf16 v[14:17], v[214:217], v[198:201], v[14:17]
	v_mfma_f32_16x16x32_bf16 v[10:13], v[238:241], v[198:201], v[10:13]
	v_mfma_f32_16x16x32_bf16 v[6:9], v[214:217], v[206:209], v[6:9]
	v_mfma_f32_16x16x32_bf16 v[2:5], v[238:241], v[206:209], v[2:5]
	v_mfma_f32_16x16x32_bf16 v[46:49], v[218:221], v[180:183], v[46:49]
	v_mfma_f32_16x16x32_bf16 v[42:45], v[242:245], v[180:183], v[42:45]
	v_mfma_f32_16x16x32_bf16 v[38:41], v[218:221], v[188:191], v[38:41]
	v_mfma_f32_16x16x32_bf16 v[34:37], v[242:245], v[188:191], v[34:37]
	v_mfma_f32_16x16x32_bf16 v[14:17], v[218:221], v[202:205], v[14:17]
	v_mfma_f32_16x16x32_bf16 v[10:13], v[242:245], v[202:205], v[10:13]
	v_mfma_f32_16x16x32_bf16 v[6:9], v[218:221], v[210:213], v[6:9]
	v_mfma_f32_16x16x32_bf16 v[2:5], v[242:245], v[210:213], v[2:5]
	s_add_i32 s0, 0, 0x18000
	v_add_u32_e32 v159, s0, v139
	s_barrier
	ds_read_b128 v[160:163], v159
	ds_read_b128 v[164:167], v159 offset:1024
	ds_read_b128 v[168:171], v159 offset:2048
	ds_read_b128 v[172:175], v159 offset:3072
	s_mov_b32 m0, s43
	ds_read_b128 v[176:179], v154 offset:32768
	ds_read_b128 v[180:183], v154 offset:33792
	ds_read_b128 v[184:187], v154 offset:34816
	ds_read_b128 v[188:191], v154 offset:35840
	ds_read_b128 v[198:201], v154 offset:36864
	ds_read_b128 v[202:205], v154 offset:37888
	ds_read_b128 v[206:209], v154 offset:38912
	ds_read_b128 v[210:213], v154 offset:39936
	global_load_lds_dwordx4 v141, s[26:27]
	s_mov_b32 m0, s64
	s_nop 0
	global_load_lds_dwordx4 v143, s[26:27]
	s_waitcnt lgkmcnt(8)
	s_barrier
	s_waitcnt lgkmcnt(0)
	s_waitcnt lgkmcnt(0)
	v_mfma_f32_16x16x32_bf16 v[126:129], v[160:163], v[176:179], v[126:129]
	v_mfma_f32_16x16x32_bf16 v[122:125], v[168:171], v[176:179], v[122:125]
	v_mfma_f32_16x16x32_bf16 v[118:121], v[160:163], v[184:187], v[118:121]
	v_mfma_f32_16x16x32_bf16 v[114:117], v[168:171], v[184:187], v[114:117]
	v_mfma_f32_16x16x32_bf16 v[94:97], v[160:163], v[198:201], v[94:97]
	v_mfma_f32_16x16x32_bf16 v[90:93], v[168:171], v[198:201], v[90:93]
	v_mfma_f32_16x16x32_bf16 v[86:89], v[160:163], v[206:209], v[86:89]
	v_mfma_f32_16x16x32_bf16 v[82:85], v[168:171], v[206:209], v[82:85]
	v_mfma_f32_16x16x32_bf16 v[126:129], v[164:167], v[180:183], v[126:129]
	v_mfma_f32_16x16x32_bf16 v[122:125], v[172:175], v[180:183], v[122:125]
	v_mfma_f32_16x16x32_bf16 v[118:121], v[164:167], v[188:191], v[118:121]
	v_mfma_f32_16x16x32_bf16 v[114:117], v[172:175], v[188:191], v[114:117]
	v_mfma_f32_16x16x32_bf16 v[94:97], v[164:167], v[202:205], v[94:97]
	v_mfma_f32_16x16x32_bf16 v[90:93], v[172:175], v[202:205], v[90:93]
	v_mfma_f32_16x16x32_bf16 v[86:89], v[164:167], v[210:213], v[86:89]
	v_mfma_f32_16x16x32_bf16 v[82:85], v[172:175], v[210:213], v[82:85]
	s_barrier
	s_add_i32 s20, 0, 0x1c000
	s_add_i32 s0, s0, s35
	v_add_u32_e32 v141, s20, v139
	v_lshl_add_u64 v[224:225], v[224:225], 0, s[54:55]
	s_mov_b32 m0, s0
	ds_read_b128 v[214:217], v141
	ds_read_b128 v[218:221], v141 offset:1024
	ds_read_b128 v[238:241], v141 offset:2048
	ds_read_b128 v[242:245], v141 offset:3072
	global_load_lds_dwordx4 v[224:225], off
	v_lshl_add_u64 v[224:225], v[230:231], 0, s[54:55]
	s_add_i32 m0, s0, 0x2000
	s_nop 0
	global_load_lds_dwordx4 v[224:225], off
	s_barrier
	s_waitcnt lgkmcnt(0)
	s_waitcnt lgkmcnt(0)
	v_mfma_f32_16x16x32_bf16 v[110:113], v[214:217], v[176:179], v[110:113]
	v_mfma_f32_16x16x32_bf16 v[106:109], v[238:241], v[176:179], v[106:109]
	v_mfma_f32_16x16x32_bf16 v[102:105], v[214:217], v[184:187], v[102:105]
	v_mfma_f32_16x16x32_bf16 v[98:101], v[238:241], v[184:187], v[98:101]
	v_mfma_f32_16x16x32_bf16 v[78:81], v[214:217], v[198:201], v[78:81]
	v_mfma_f32_16x16x32_bf16 v[74:77], v[238:241], v[198:201], v[74:77]
	v_mfma_f32_16x16x32_bf16 v[70:73], v[214:217], v[206:209], v[70:73]
	v_mfma_f32_16x16x32_bf16 v[66:69], v[238:241], v[206:209], v[66:69]
	v_mfma_f32_16x16x32_bf16 v[110:113], v[218:221], v[180:183], v[110:113]
	v_mfma_f32_16x16x32_bf16 v[106:109], v[242:245], v[180:183], v[106:109]
	v_mfma_f32_16x16x32_bf16 v[102:105], v[218:221], v[188:191], v[102:105]
	v_mfma_f32_16x16x32_bf16 v[98:101], v[242:245], v[188:191], v[98:101]
	v_mfma_f32_16x16x32_bf16 v[78:81], v[218:221], v[202:205], v[78:81]
	v_mfma_f32_16x16x32_bf16 v[74:77], v[242:245], v[202:205], v[74:77]
	v_mfma_f32_16x16x32_bf16 v[70:73], v[218:221], v[210:213], v[70:73]
	v_mfma_f32_16x16x32_bf16 v[66:69], v[242:245], v[210:213], v[66:69]
	s_mov_b32 m0, s65
	v_lshl_add_u64 v[224:225], v[232:233], 0, s[54:55]
	s_barrier
	ds_read_b128 v[176:179], v154 offset:49152
	ds_read_b128 v[180:183], v154 offset:50176
	ds_read_b128 v[184:187], v154 offset:51200
	ds_read_b128 v[188:191], v154 offset:52224
	ds_read_b128 v[198:201], v154 offset:53248
	ds_read_b128 v[202:205], v154 offset:54272
	ds_read_b128 v[206:209], v154 offset:55296
	ds_read_b128 v[210:213], v154 offset:56320
	global_load_lds_dwordx4 v[224:225], off
	v_lshl_add_u64 v[192:193], v[192:193], 0, s[54:55]
	s_mov_b32 m0, s66
	s_nop 0
	global_load_lds_dwordx4 v[192:193], off
	s_barrier
	s_waitcnt lgkmcnt(0)
	s_waitcnt lgkmcnt(0)
	v_mfma_f32_16x16x32_bf16 v[62:65], v[160:163], v[176:179], v[62:65]
	v_mfma_f32_16x16x32_bf16 v[58:61], v[168:171], v[176:179], v[58:61]
	v_mfma_f32_16x16x32_bf16 v[54:57], v[160:163], v[184:187], v[54:57]
	v_mfma_f32_16x16x32_bf16 v[50:53], v[168:171], v[184:187], v[50:53]
	v_mfma_f32_16x16x32_bf16 v[30:33], v[160:163], v[198:201], v[30:33]
	v_mfma_f32_16x16x32_bf16 v[26:29], v[168:171], v[198:201], v[26:29]
	v_mfma_f32_16x16x32_bf16 v[22:25], v[160:163], v[206:209], v[22:25]
	v_mfma_f32_16x16x32_bf16 v[18:21], v[168:171], v[206:209], v[18:21]
	v_mfma_f32_16x16x32_bf16 v[62:65], v[164:167], v[180:183], v[62:65]
	v_mfma_f32_16x16x32_bf16 v[58:61], v[172:175], v[180:183], v[58:61]
	v_mfma_f32_16x16x32_bf16 v[54:57], v[164:167], v[188:191], v[54:57]
	v_mfma_f32_16x16x32_bf16 v[50:53], v[172:175], v[188:191], v[50:53]
	v_mfma_f32_16x16x32_bf16 v[30:33], v[164:167], v[202:205], v[30:33]
	v_mfma_f32_16x16x32_bf16 v[26:29], v[172:175], v[202:205], v[26:29]
	v_mfma_f32_16x16x32_bf16 v[22:25], v[164:167], v[210:213], v[22:25]
	v_mfma_f32_16x16x32_bf16 v[18:21], v[172:175], v[210:213], v[18:21]
	s_barrier
	s_add_u32 s0, s24, 0x40080
	s_addc_u32 s1, s25, 0
	s_add_i32 s20, s20, s35
	v_lshl_add_u64 v[160:161], s[0:1], 0, v[130:131]
	s_mov_b32 m0, s20
	s_nop 0
	global_load_lds_dwordx4 v[160:161], off
	v_lshl_add_u64 v[160:161], s[0:1], 0, v[132:133]
	s_add_i32 m0, s20, 0x2000
	s_nop 0
	global_load_lds_dwordx4 v[160:161], off
	s_waitcnt vmcnt(6)
	s_barrier
	v_mfma_f32_16x16x32_bf16 v[46:49], v[214:217], v[176:179], v[46:49]
	v_mfma_f32_16x16x32_bf16 v[42:45], v[238:241], v[176:179], v[42:45]
	v_mfma_f32_16x16x32_bf16 v[38:41], v[214:217], v[184:187], v[38:41]
	v_mfma_f32_16x16x32_bf16 v[34:37], v[238:241], v[184:187], v[34:37]
	v_mfma_f32_16x16x32_bf16 v[14:17], v[214:217], v[198:201], v[14:17]
	v_mfma_f32_16x16x32_bf16 v[10:13], v[238:241], v[198:201], v[10:13]
	v_mfma_f32_16x16x32_bf16 v[6:9], v[214:217], v[206:209], v[6:9]
	v_mfma_f32_16x16x32_bf16 v[2:5], v[238:241], v[206:209], v[2:5]
	v_mfma_f32_16x16x32_bf16 v[46:49], v[218:221], v[180:183], v[46:49]
	v_mfma_f32_16x16x32_bf16 v[42:45], v[242:245], v[180:183], v[42:45]
	v_mfma_f32_16x16x32_bf16 v[38:41], v[218:221], v[188:191], v[38:41]
	v_mfma_f32_16x16x32_bf16 v[34:37], v[242:245], v[188:191], v[34:37]
	v_mfma_f32_16x16x32_bf16 v[14:17], v[218:221], v[202:205], v[14:17]
	v_mfma_f32_16x16x32_bf16 v[10:13], v[242:245], v[202:205], v[10:13]
	v_mfma_f32_16x16x32_bf16 v[6:9], v[218:221], v[210:213], v[6:9]
	v_mfma_f32_16x16x32_bf16 v[2:5], v[242:245], v[210:213], v[2:5]
	s_add_i32 s77, s77, 2
	s_cmp_gt_u32 s77, 13
	s_mov_b64 s[20:21], s[22:23]
	s_barrier
	s_cbranch_scc0 .LBB0_2475
	v_mul_f32_e32 v142, 0xbfb8aa3b, v126
	v_mul_f32_e32 v143, 0xbfb8aa3b, v127
	v_exp_f32_e32 v142, v142
	v_exp_f32_e32 v143, v143
	v_lshl_add_u32 v136, s73, 8, v137
	v_lshl_or_b32 v138, s74, 8, v153
	v_add_f32_e32 v142, 1.0, v142
	v_add_f32_e32 v143, 1.0, v143
	v_rcp_f32_e32 v142, v142
	v_rcp_f32_e32 v143, v143
	v_or_b32_e32 v140, v136, v151
	v_ashrrev_i32_e32 v141, 31, v140
	v_lshlrev_b64 v[140:141], 10, v[140:141]
	v_pk_mul_f32 v[126:127], v[126:127], v[142:143]
	v_lshl_add_u64 v[140:141], v[134:135], 0, v[140:141]
	v_pk_mul_f32 v[122:123], v[122:123], v[126:127]
	s_and_b64 vcc, exec, s[16:17]
	v_cvt_pk_bf16_f32 v122, v122, v123
	v_mul_f32_e32 v123, 0xbfb8aa3b, v128
	v_exp_f32_e32 v123, v123
	v_mov_b32_e32 v142, v158
	s_mov_b32 s74, s14
	s_mov_b32 s73, s72
	v_add_f32_e32 v123, 1.0, v123
	v_rcp_f32_e32 v126, v123
	v_mul_f32_e32 v123, 0xbfb8aa3b, v129
	v_exp_f32_e32 v123, v123
	s_mov_b64 s[20:21], s[18:19]
	v_add_f32_e32 v123, 1.0, v123
	v_rcp_f32_e32 v127, v123
	s_nop 0
	v_pk_mul_f32 v[126:127], v[128:129], v[126:127]
	s_nop 0
	v_pk_mul_f32 v[124:125], v[124:125], v[126:127]
	s_nop 0
	v_cvt_pk_bf16_f32 v123, v124, v125
	v_mul_f32_e32 v124, 0xbfb8aa3b, v118
	v_mul_f32_e32 v125, 0xbfb8aa3b, v119
	v_exp_f32_e32 v124, v124
	v_exp_f32_e32 v125, v125
	v_add_f32_e32 v124, 1.0, v124
	v_add_f32_e32 v125, 1.0, v125
	v_rcp_f32_e32 v124, v124
	v_rcp_f32_e32 v125, v125
	s_nop 0
	v_pk_mul_f32 v[118:119], v[118:119], v[124:125]
	s_nop 0
	v_pk_mul_f32 v[114:115], v[114:115], v[118:119]
	v_mul_f32_e32 v118, 0xbfb8aa3b, v110
	v_mul_f32_e32 v119, 0xbfb8aa3b, v111
	v_exp_f32_e32 v118, v118
	v_exp_f32_e32 v119, v119
	v_cvt_pk_bf16_f32 v124, v114, v115
	v_mul_f32_e32 v114, 0xbfb8aa3b, v120
	v_add_f32_e32 v118, 1.0, v118
	v_add_f32_e32 v119, 1.0, v119
	v_rcp_f32_e32 v118, v118
	v_rcp_f32_e32 v119, v119
	v_mul_f32_e32 v115, 0xbfb8aa3b, v121
	v_exp_f32_e32 v114, v114
	v_exp_f32_e32 v115, v115
	v_pk_mul_f32 v[110:111], v[110:111], v[118:119]
	v_permlane16_swap_b32_e32 v122, v124
	v_pk_mul_f32 v[106:107], v[106:107], v[110:111]
	v_add_f32_e32 v114, 1.0, v114
	v_cvt_pk_bf16_f32 v106, v106, v107
	v_mul_f32_e32 v107, 0xbfb8aa3b, v112
	v_exp_f32_e32 v107, v107
	v_add_f32_e32 v115, 1.0, v115
	v_rcp_f32_e32 v114, v114
	v_rcp_f32_e32 v115, v115
	v_add_f32_e32 v107, 1.0, v107
	v_rcp_f32_e32 v110, v107
	v_mul_f32_e32 v107, 0xbfb8aa3b, v113
	v_exp_f32_e32 v107, v107
	v_pk_mul_f32 v[114:115], v[120:121], v[114:115]
	v_add_f32_e32 v107, 1.0, v107
	v_rcp_f32_e32 v111, v107
	v_pk_mul_f32 v[114:115], v[116:117], v[114:115]
	v_pk_mul_f32 v[110:111], v[112:113], v[110:111]
	s_nop 0
	v_pk_mul_f32 v[108:109], v[108:109], v[110:111]
	v_cvt_pk_bf16_f32 v125, v114, v115
	v_cvt_pk_bf16_f32 v107, v108, v109
	v_mul_f32_e32 v108, 0xbfb8aa3b, v102
	v_mul_f32_e32 v109, 0xbfb8aa3b, v103
	v_exp_f32_e32 v108, v108
	v_exp_f32_e32 v109, v109
	v_ashrrev_i32_e32 v114, 1, v138
	v_ashrrev_i32_e32 v115, 31, v114
	v_add_f32_e32 v108, 1.0, v108
	v_add_f32_e32 v109, 1.0, v109
	v_rcp_f32_e32 v108, v108
	v_rcp_f32_e32 v109, v109
	v_lshlrev_b64 v[114:115], 1, v[114:115]
	v_permlane16_swap_b32_e32 v123, v125
	v_pk_mul_f32 v[102:103], v[102:103], v[108:109]
	v_lshl_add_u64 v[116:117], v[140:141], 0, v[114:115]
	v_pk_mul_f32 v[98:99], v[98:99], v[102:103]
	v_mov_b32_e32 v138, v156
	v_cvt_pk_bf16_f32 v108, v98, v99
	v_mul_f32_e32 v98, 0xbfb8aa3b, v104
	v_mul_f32_e32 v99, 0xbfb8aa3b, v105
	v_exp_f32_e32 v98, v98
	v_exp_f32_e32 v99, v99
	v_permlane16_swap_b32_e32 v106, v108
	v_add_f32_e32 v98, 1.0, v98
	v_add_f32_e32 v99, 1.0, v99
	v_rcp_f32_e32 v98, v98
	v_rcp_f32_e32 v99, v99
	v_mov_b32_e32 v140, v157
	global_store_dwordx4 v[116:117], v[122:125], off
	v_pk_mul_f32 v[98:99], v[104:105], v[98:99]
	s_nop 0
	v_pk_mul_f32 v[98:99], v[100:101], v[98:99]
	v_mul_f32_e32 v100, 0xbfb8aa3b, v94
	v_mul_f32_e32 v101, 0xbfb8aa3b, v95
	v_exp_f32_e32 v100, v100
	v_exp_f32_e32 v101, v101
	v_cvt_pk_bf16_f32 v109, v98, v99
	v_or_b32_e32 v98, v136, v152
	v_add_f32_e32 v100, 1.0, v100
	v_add_f32_e32 v101, 1.0, v101
	v_rcp_f32_e32 v100, v100
	v_rcp_f32_e32 v101, v101
	v_ashrrev_i32_e32 v99, 31, v98
	v_lshlrev_b64 v[98:99], 10, v[98:99]
	v_lshl_add_u64 v[98:99], v[134:135], 0, v[98:99]
	v_pk_mul_f32 v[94:95], v[94:95], v[100:101]
	v_permlane16_swap_b32_e32 v107, v109
	v_pk_mul_f32 v[90:91], v[90:91], v[94:95]
	global_store_dwordx4 v[116:117], v[106:109], off offset:128
	v_cvt_pk_bf16_f32 v90, v90, v91
	v_mul_f32_e32 v91, 0xbfb8aa3b, v96
	v_exp_f32_e32 v91, v91
	s_nop 0
	v_add_f32_e32 v91, 1.0, v91
	v_rcp_f32_e32 v94, v91
	v_mul_f32_e32 v91, 0xbfb8aa3b, v97
	v_exp_f32_e32 v91, v91
	s_nop 0
	v_add_f32_e32 v91, 1.0, v91
	v_rcp_f32_e32 v95, v91
	s_nop 0
	v_pk_mul_f32 v[94:95], v[96:97], v[94:95]
	s_nop 0
	v_pk_mul_f32 v[92:93], v[92:93], v[94:95]
	s_nop 0
	v_cvt_pk_bf16_f32 v91, v92, v93
	v_mul_f32_e32 v92, 0xbfb8aa3b, v86
	v_mul_f32_e32 v93, 0xbfb8aa3b, v87
	v_exp_f32_e32 v92, v92
	v_exp_f32_e32 v93, v93
	v_add_f32_e32 v92, 1.0, v92
	v_add_f32_e32 v93, 1.0, v93
	v_rcp_f32_e32 v92, v92
	v_rcp_f32_e32 v93, v93
	s_nop 0
	v_pk_mul_f32 v[86:87], v[86:87], v[92:93]
	s_nop 0
	v_pk_mul_f32 v[82:83], v[82:83], v[86:87]
	s_nop 0
	v_cvt_pk_bf16_f32 v92, v82, v83
	v_mul_f32_e32 v82, 0xbfb8aa3b, v88
	v_mul_f32_e32 v83, 0xbfb8aa3b, v89
	v_exp_f32_e32 v82, v82
	v_exp_f32_e32 v83, v83
	v_permlane16_swap_b32_e32 v90, v92
	v_add_f32_e32 v82, 1.0, v82
	v_add_f32_e32 v83, 1.0, v83
	v_rcp_f32_e32 v82, v82
	v_rcp_f32_e32 v83, v83
	s_nop 0
	v_pk_mul_f32 v[82:83], v[88:89], v[82:83]
	s_nop 0
	v_pk_mul_f32 v[82:83], v[84:85], v[82:83]
	v_mul_f32_e32 v84, 0xbfb8aa3b, v78
	v_mul_f32_e32 v85, 0xbfb8aa3b, v79
	v_exp_f32_e32 v84, v84
	v_exp_f32_e32 v85, v85
	v_cvt_pk_bf16_f32 v93, v82, v83
	s_nop 1
	v_permlane16_swap_b32_e32 v91, v93
	v_add_f32_e32 v84, 1.0, v84
	v_add_f32_e32 v85, 1.0, v85
	v_rcp_f32_e32 v84, v84
	v_rcp_f32_e32 v85, v85
	v_lshl_add_u64 v[82:83], v[98:99], 0, v[114:115]
	global_store_dwordx4 v[82:83], v[90:93], off
	v_pk_mul_f32 v[78:79], v[78:79], v[84:85]
	s_nop 0
	v_pk_mul_f32 v[74:75], v[74:75], v[78:79]
	s_nop 0
	v_cvt_pk_bf16_f32 v74, v74, v75
	v_mul_f32_e32 v75, 0xbfb8aa3b, v80
	v_exp_f32_e32 v75, v75
	s_nop 0
	v_add_f32_e32 v75, 1.0, v75
	v_rcp_f32_e32 v78, v75
	v_mul_f32_e32 v75, 0xbfb8aa3b, v81
	v_exp_f32_e32 v75, v75
	s_nop 0
	v_add_f32_e32 v75, 1.0, v75
	v_rcp_f32_e32 v79, v75
	s_nop 0
	v_pk_mul_f32 v[78:79], v[80:81], v[78:79]
	s_nop 0
	v_pk_mul_f32 v[76:77], v[76:77], v[78:79]
	s_nop 0
	v_cvt_pk_bf16_f32 v75, v76, v77
	v_mul_f32_e32 v76, 0xbfb8aa3b, v70
	v_mul_f32_e32 v77, 0xbfb8aa3b, v71
	v_exp_f32_e32 v76, v76
	v_exp_f32_e32 v77, v77
	v_add_f32_e32 v76, 1.0, v76
	v_add_f32_e32 v77, 1.0, v77
	v_rcp_f32_e32 v76, v76
	v_rcp_f32_e32 v77, v77
	s_nop 0
	v_pk_mul_f32 v[70:71], v[70:71], v[76:77]
	s_nop 0
	v_pk_mul_f32 v[66:67], v[66:67], v[70:71]
	v_add_u32_e32 v70, 0x80, v136
	v_cvt_pk_bf16_f32 v76, v66, v67
	v_mul_f32_e32 v66, 0xbfb8aa3b, v72
	v_mul_f32_e32 v67, 0xbfb8aa3b, v73
	v_exp_f32_e32 v66, v66
	v_exp_f32_e32 v67, v67
	v_permlane16_swap_b32_e32 v74, v76
	v_add_f32_e32 v66, 1.0, v66
	v_add_f32_e32 v67, 1.0, v67
	v_rcp_f32_e32 v66, v66
	v_rcp_f32_e32 v67, v67
	v_mov_b32_e32 v136, v155
	v_pk_mul_f32 v[66:67], v[72:73], v[66:67]
	s_nop 0
	v_pk_mul_f32 v[66:67], v[68:69], v[66:67]
	v_mul_f32_e32 v68, 0xbfb8aa3b, v62
	v_mul_f32_e32 v69, 0xbfb8aa3b, v63
	v_exp_f32_e32 v68, v68
	v_exp_f32_e32 v69, v69
	v_cvt_pk_bf16_f32 v77, v66, v67
	v_or_b32_e32 v66, v70, v151
	v_add_f32_e32 v68, 1.0, v68
	v_add_f32_e32 v69, 1.0, v69
	v_rcp_f32_e32 v68, v68
	v_rcp_f32_e32 v69, v69
	v_ashrrev_i32_e32 v67, 31, v66
	v_lshlrev_b64 v[66:67], 10, v[66:67]
	v_lshl_add_u64 v[66:67], v[134:135], 0, v[66:67]
	v_pk_mul_f32 v[62:63], v[62:63], v[68:69]
	v_permlane16_swap_b32_e32 v75, v77
	v_pk_mul_f32 v[58:59], v[58:59], v[62:63]
	global_store_dwordx4 v[82:83], v[74:77], off offset:128
	v_cvt_pk_bf16_f32 v58, v58, v59
	v_mul_f32_e32 v59, 0xbfb8aa3b, v64
	v_exp_f32_e32 v59, v59
	s_nop 0
	v_add_f32_e32 v59, 1.0, v59
	v_rcp_f32_e32 v62, v59
	v_mul_f32_e32 v59, 0xbfb8aa3b, v65
	v_exp_f32_e32 v59, v59
	s_nop 0
	v_add_f32_e32 v59, 1.0, v59
	v_rcp_f32_e32 v63, v59
	s_nop 0
	v_pk_mul_f32 v[62:63], v[64:65], v[62:63]
	s_nop 0
	v_pk_mul_f32 v[60:61], v[60:61], v[62:63]
	s_nop 0
	v_cvt_pk_bf16_f32 v59, v60, v61
	v_mul_f32_e32 v60, 0xbfb8aa3b, v54
	v_mul_f32_e32 v61, 0xbfb8aa3b, v55
	v_exp_f32_e32 v60, v60
	v_exp_f32_e32 v61, v61
	v_add_f32_e32 v60, 1.0, v60
	v_add_f32_e32 v61, 1.0, v61
	v_rcp_f32_e32 v60, v60
	v_rcp_f32_e32 v61, v61
	s_nop 0
	v_pk_mul_f32 v[54:55], v[54:55], v[60:61]
	s_nop 0
	v_pk_mul_f32 v[50:51], v[50:51], v[54:55]
	s_nop 0
	v_cvt_pk_bf16_f32 v60, v50, v51
	v_mul_f32_e32 v50, 0xbfb8aa3b, v56
	v_mul_f32_e32 v51, 0xbfb8aa3b, v57
	v_exp_f32_e32 v50, v50
	v_exp_f32_e32 v51, v51
	v_permlane16_swap_b32_e32 v58, v60
	v_add_f32_e32 v50, 1.0, v50
	v_add_f32_e32 v51, 1.0, v51
	v_rcp_f32_e32 v50, v50
	v_rcp_f32_e32 v51, v51
	s_nop 0
	v_pk_mul_f32 v[50:51], v[56:57], v[50:51]
	s_nop 0
	v_pk_mul_f32 v[50:51], v[52:53], v[50:51]
	v_mul_f32_e32 v52, 0xbfb8aa3b, v46
	v_mul_f32_e32 v53, 0xbfb8aa3b, v47
	v_exp_f32_e32 v52, v52
	v_exp_f32_e32 v53, v53
	v_cvt_pk_bf16_f32 v61, v50, v51
	s_nop 1
	v_permlane16_swap_b32_e32 v59, v61
	v_add_f32_e32 v52, 1.0, v52
	v_add_f32_e32 v53, 1.0, v53
	v_rcp_f32_e32 v52, v52
	v_rcp_f32_e32 v53, v53
	v_lshl_add_u64 v[50:51], v[66:67], 0, v[114:115]
	global_store_dwordx4 v[50:51], v[58:61], off
	v_pk_mul_f32 v[46:47], v[46:47], v[52:53]
	s_nop 0
	v_pk_mul_f32 v[42:43], v[42:43], v[46:47]
	s_nop 0
	v_cvt_pk_bf16_f32 v42, v42, v43
	v_mul_f32_e32 v43, 0xbfb8aa3b, v48
	v_exp_f32_e32 v43, v43
	s_nop 0
	v_add_f32_e32 v43, 1.0, v43
	v_rcp_f32_e32 v46, v43
	v_mul_f32_e32 v43, 0xbfb8aa3b, v49
	v_exp_f32_e32 v43, v43
	s_nop 0
	v_add_f32_e32 v43, 1.0, v43
	v_rcp_f32_e32 v47, v43
	s_nop 0
	v_pk_mul_f32 v[46:47], v[48:49], v[46:47]
	s_nop 0
	v_pk_mul_f32 v[44:45], v[44:45], v[46:47]
	s_nop 0
	v_cvt_pk_bf16_f32 v43, v44, v45
	v_mul_f32_e32 v44, 0xbfb8aa3b, v38
	v_mul_f32_e32 v45, 0xbfb8aa3b, v39
	v_exp_f32_e32 v44, v44
	v_exp_f32_e32 v45, v45
	v_add_f32_e32 v44, 1.0, v44
	v_add_f32_e32 v45, 1.0, v45
	v_rcp_f32_e32 v44, v44
	v_rcp_f32_e32 v45, v45
	s_nop 0
	v_pk_mul_f32 v[38:39], v[38:39], v[44:45]
	s_nop 0
	v_pk_mul_f32 v[34:35], v[34:35], v[38:39]
	s_nop 0
	v_cvt_pk_bf16_f32 v44, v34, v35
	v_mul_f32_e32 v34, 0xbfb8aa3b, v40
	v_mul_f32_e32 v35, 0xbfb8aa3b, v41
	v_exp_f32_e32 v34, v34
	v_exp_f32_e32 v35, v35
	v_permlane16_swap_b32_e32 v42, v44
	v_add_f32_e32 v34, 1.0, v34
	v_add_f32_e32 v35, 1.0, v35
	v_rcp_f32_e32 v34, v34
	v_rcp_f32_e32 v35, v35
	s_nop 0
	v_pk_mul_f32 v[34:35], v[40:41], v[34:35]
	s_nop 0
	v_pk_mul_f32 v[34:35], v[36:37], v[34:35]
	v_mul_f32_e32 v36, 0xbfb8aa3b, v30
	v_mul_f32_e32 v37, 0xbfb8aa3b, v31
	v_exp_f32_e32 v36, v36
	v_exp_f32_e32 v37, v37
	v_cvt_pk_bf16_f32 v45, v34, v35
	v_or_b32_e32 v34, v70, v152
	v_add_f32_e32 v36, 1.0, v36
	v_add_f32_e32 v37, 1.0, v37
	v_rcp_f32_e32 v36, v36
	v_rcp_f32_e32 v37, v37
	v_ashrrev_i32_e32 v35, 31, v34
	v_lshlrev_b64 v[34:35], 10, v[34:35]
	v_lshl_add_u64 v[34:35], v[134:135], 0, v[34:35]
	v_pk_mul_f32 v[30:31], v[30:31], v[36:37]
	v_permlane16_swap_b32_e32 v43, v45
	v_pk_mul_f32 v[26:27], v[26:27], v[30:31]
	global_store_dwordx4 v[50:51], v[42:45], off offset:128
	v_cvt_pk_bf16_f32 v26, v26, v27
	v_mul_f32_e32 v27, 0xbfb8aa3b, v32
	v_exp_f32_e32 v27, v27
	s_nop 0
	v_add_f32_e32 v27, 1.0, v27
	v_rcp_f32_e32 v30, v27
	v_mul_f32_e32 v27, 0xbfb8aa3b, v33
	v_exp_f32_e32 v27, v27
	s_nop 0
	v_add_f32_e32 v27, 1.0, v27
	v_rcp_f32_e32 v31, v27
	s_nop 0
	v_pk_mul_f32 v[30:31], v[32:33], v[30:31]
	s_nop 0
	v_pk_mul_f32 v[28:29], v[28:29], v[30:31]
	s_nop 0
	v_cvt_pk_bf16_f32 v27, v28, v29
	v_mul_f32_e32 v28, 0xbfb8aa3b, v22
	v_mul_f32_e32 v29, 0xbfb8aa3b, v23
	v_exp_f32_e32 v28, v28
	v_exp_f32_e32 v29, v29
	v_add_f32_e32 v28, 1.0, v28
	v_add_f32_e32 v29, 1.0, v29
	v_rcp_f32_e32 v28, v28
	v_rcp_f32_e32 v29, v29
	s_nop 0
	v_pk_mul_f32 v[22:23], v[22:23], v[28:29]
	s_nop 0
	v_pk_mul_f32 v[18:19], v[18:19], v[22:23]
	s_nop 0
	v_cvt_pk_bf16_f32 v28, v18, v19
	v_mul_f32_e32 v18, 0xbfb8aa3b, v24
	v_mul_f32_e32 v19, 0xbfb8aa3b, v25
	v_exp_f32_e32 v18, v18
	v_exp_f32_e32 v19, v19
	v_permlane16_swap_b32_e32 v26, v28
	v_add_f32_e32 v18, 1.0, v18
	v_add_f32_e32 v19, 1.0, v19
	v_rcp_f32_e32 v18, v18
	v_rcp_f32_e32 v19, v19
	s_nop 0
	v_pk_mul_f32 v[18:19], v[24:25], v[18:19]
	s_nop 0
	v_pk_mul_f32 v[18:19], v[20:21], v[18:19]
	v_mul_f32_e32 v20, 0xbfb8aa3b, v14
	v_mul_f32_e32 v21, 0xbfb8aa3b, v15
	v_exp_f32_e32 v20, v20
	v_exp_f32_e32 v21, v21
	v_cvt_pk_bf16_f32 v29, v18, v19
	s_nop 1
	v_permlane16_swap_b32_e32 v27, v29
	v_add_f32_e32 v20, 1.0, v20
	v_add_f32_e32 v21, 1.0, v21
	v_rcp_f32_e32 v20, v20
	v_rcp_f32_e32 v21, v21
	v_lshl_add_u64 v[18:19], v[34:35], 0, v[114:115]
	global_store_dwordx4 v[18:19], v[26:29], off
	v_pk_mul_f32 v[14:15], v[14:15], v[20:21]
	s_nop 0
	v_pk_mul_f32 v[10:11], v[10:11], v[14:15]
	s_nop 0
	v_cvt_pk_bf16_f32 v10, v10, v11
	v_mul_f32_e32 v11, 0xbfb8aa3b, v16
	v_exp_f32_e32 v11, v11
	s_nop 0
	v_add_f32_e32 v11, 1.0, v11
	v_rcp_f32_e32 v14, v11
	v_mul_f32_e32 v11, 0xbfb8aa3b, v17
	v_exp_f32_e32 v11, v11
	s_nop 0
	v_add_f32_e32 v11, 1.0, v11
	v_rcp_f32_e32 v15, v11
	s_nop 0
	v_pk_mul_f32 v[14:15], v[16:17], v[14:15]
	s_nop 0
	v_pk_mul_f32 v[12:13], v[12:13], v[14:15]
	s_nop 0
	v_cvt_pk_bf16_f32 v11, v12, v13
	v_mul_f32_e32 v12, 0xbfb8aa3b, v6
	v_mul_f32_e32 v13, 0xbfb8aa3b, v7
	v_exp_f32_e32 v12, v12
	v_exp_f32_e32 v13, v13
	v_add_f32_e32 v12, 1.0, v12
	v_add_f32_e32 v13, 1.0, v13
	v_rcp_f32_e32 v12, v12
	v_rcp_f32_e32 v13, v13
	s_nop 0
	v_pk_mul_f32 v[6:7], v[6:7], v[12:13]
	s_nop 0
	v_pk_mul_f32 v[2:3], v[2:3], v[6:7]
	s_nop 0
	v_cvt_pk_bf16_f32 v12, v2, v3
	v_mul_f32_e32 v2, 0xbfb8aa3b, v8
	v_mul_f32_e32 v3, 0xbfb8aa3b, v9
	v_exp_f32_e32 v2, v2
	v_exp_f32_e32 v3, v3
	v_permlane16_swap_b32_e32 v10, v12
	v_add_f32_e32 v2, 1.0, v2
	v_add_f32_e32 v3, 1.0, v3
	v_rcp_f32_e32 v2, v2
	v_rcp_f32_e32 v3, v3
	s_nop 0
	v_pk_mul_f32 v[2:3], v[8:9], v[2:3]
	s_nop 0
	v_pk_mul_f32 v[2:3], v[4:5], v[2:3]
	s_nop 0
	v_cvt_pk_bf16_f32 v13, v2, v3
	s_nop 1
	v_permlane16_swap_b32_e32 v11, v13
	global_store_dwordx4 v[18:19], v[10:13], off offset:128
	s_cbranch_vccz .LBB0_2465
	s_waitcnt vmcnt(0)
	s_cmpk_gt_u32 s29, 0xff
	s_cbranch_scc1 .LBB0_2479
	s_barrier

.LBB0_2481:
	s_mov_b64 s[0:1], s[4:5]
	s_load_dword s0, s[0:1], 0x110
	s_waitcnt lgkmcnt(0)
	s_cmp_gt_i32 s0, s2
	s_cbranch_scc1 .LBB0_2539
	s_mov_b64 s[0:1], s[4:5]
	s_load_dword s0, s[0:1], 0x114
	s_waitcnt lgkmcnt(0)
	s_cmp_ge_i32 s2, s0
	s_cbranch_scc1 .LBB0_2538
	v_readlane_b32 s0, v254, 2
	v_readlane_b32 s1, v254, 3
	s_load_dword s1, s[0:1], 0x110
	s_add_i32 s0, s41, 10
	s_waitcnt lgkmcnt(0)
	s_cmp_gt_i32 s1, s0
	s_cbranch_scc1 .LBB0_2538
	v_readlane_b32 s2, v254, 2
	v_readlane_b32 s3, v254, 3
	s_load_dword s1, s[2:3], 0x114
	s_waitcnt lgkmcnt(0)
	s_cmp_ge_i32 s0, s1
	s_cbranch_scc1 .LBB0_2538
	v_readlane_b32 s6, v254, 2
	v_mov_b32_e32 v1, v0
	v_readlane_b32 s7, v254, 3
	s_load_dword s0, s[6:7], 0x118
	v_readlane_b32 s1, v254, 0
	s_waitcnt lgkmcnt(0)
	s_setprio 0
	s_getreg_b32 s0, hwreg(HW_REG_XCC_ID, 0, 4)
	s_waitcnt vmcnt(0)
	s_barrier
	s_mov_b64 s[4:5], exec
	v_readlane_b32 s2, v254, 6
	v_readlane_b32 s3, v254, 7
	s_and_b64 s[2:3], s[4:5], s[2:3]
	s_mov_b64 exec, s[2:3]
	s_cbranch_execz .LBB0_2537
	s_add_i32 s3, 0, 0x26000
	v_mov_b32_e32 v1, s3
	s_load_dwordx2 s[6:7], s[6:7], 0x108
	s_waitcnt vmcnt(0) expcnt(0) lgkmcnt(0)
	ds_read_b32 v3, v1
	v_readlane_b32 s1, v254, 8
	s_and_b32 s2, s0, 15
	s_waitcnt lgkmcnt(0)
	v_cmp_ne_u32_e32 vcc, 0, v3
	v_mov_b32_e32 v1, s1
	ds_read_b32 v2, v1
	s_cbranch_vccnz .LBB0_2501
	v_readlane_b32 s8, v254, 4
	v_readlane_b32 s12, v254, 2
	v_readlane_b32 s9, v254, 5
	v_readlane_b32 s13, v254, 3
	s_load_dwordx2 s[0:1], s[8:9], 0x4
	s_nop 0
	s_load_dword s12, s[12:13], 0x118
	s_add_u32 s8, s6, 0x4200
	s_addc_u32 s9, s7, 0
	s_add_u32 s10, s6, 0x4400
	s_addc_u32 s11, s7, 0
	s_waitcnt lgkmcnt(0)
	s_mul_i32 s34, s0, s12
	s_add_u32 s12, s6, 0x4500
	s_addc_u32 s13, s7, 0
	s_add_u32 s14, s6, 0x4600
	s_addc_u32 s15, s7, 0
	s_add_u32 s16, s6, 0x4700
	s_addc_u32 s17, s7, 0
	s_add_u32 s18, s6, 0x4800
	s_addc_u32 s19, s7, 0
	s_add_u32 s20, s6, 0x4900
	s_addc_u32 s21, s7, 0
	s_add_u32 s22, s6, 0x4a00
	s_addc_u32 s23, s7, 0
	s_add_u32 s24, s6, 0x4b00
	s_addc_u32 s25, s7, 0
	s_add_u32 s26, s6, 0x4c00
	s_addc_u32 s27, s7, 0
	s_add_u32 s28, s6, 0x4d00
	s_addc_u32 s29, s7, 0
	s_add_u32 s30, s6, 0x4e00
	s_addc_u32 s31, s7, 0
	s_add_u32 s64, s6, 0x4f00
	s_addc_u32 s65, s7, 0
	s_add_u32 s66, s6, 0x5000
	s_addc_u32 s67, s7, 0
	s_add_u32 s68, s6, 0x5100
	s_addc_u32 s69, s7, 0
	s_add_u32 s70, s6, 0x5200
	s_addc_u32 s71, s7, 0
	s_add_u32 s72, s6, 0x5300
	s_mul_i32 s34, s34, s1
	s_addc_u32 s73, s7, 0
	s_mov_b32 s0, 1
	s_branch .LBB0_2489

.LBB0_2551:
	s_and_b64 vcc, exec, s[8:9]
	s_cbranch_vccz .LBB0_2568
	v_ashrrev_i32_e32 v2, 31, v14
	v_lshrrev_b32_e32 v2, 26, v2
	v_add_u32_e32 v2, v14, v2
	s_waitcnt vmcnt(1)
	v_ashrrev_i32_e32 v10, 6, v2
	v_bfe_i32 v2, v14, 27, 1
	v_lshlrev_b32_e32 v1, 4, v14
	v_lshrrev_b32_e32 v2, 22, v2
	v_add_u32_e32 v2, v1, v2
	v_and_b32_e32 v2, 0xfffffc00, v2
	v_sub_u32_e32 v2, v1, v2
	v_lshrrev_b32_e32 v3, 4, v2
	v_bitop3_b32 v2, v3, v2, 32 bitop3:0x6c
	v_ashrrev_i32_e32 v4, 31, v2
	v_lshrrev_b32_e32 v4, 26, v4
	v_add_u32_e32 v4, v2, v4
	v_lshlrev_b32_e32 v3, 3, v10
	v_ashrrev_i32_e32 v11, 6, v4
	v_and_b32_e32 v4, 0xc0, v4
	v_and_b32_e32 v3, -16, v3
	v_sub_u32_e32 v2, v2, v4
	v_add_u32_e32 v3, v11, v3
	v_ashrrev_i16_sdwa v2, v226, sext(v2) dst_sel:DWORD dst_unused:UNUSED_PAD src0_sel:DWORD src1_sel:BYTE_0
	v_lshlrev_b32_e32 v5, 5, v10
	v_bfe_i32 v12, v2, 0, 16
	v_lshlrev_b32_e32 v2, 1, v3
	v_lshrrev_b32_e32 v4, 2, v3
	v_and_b32_e32 v6, 3, v11
	s_mov_b32 s0, 0x3fffe0
	v_and_b32_e32 v5, 32, v5
	v_and_b32_e32 v2, 24, v2
	v_and_b32_e32 v4, 4, v4
	v_and_or_b32 v6, v3, s0, v6
	v_or3_b32 v2, v6, v4, v2
	v_add_lshl_u32 v4, v5, v12, 1
	v_add_u32_e32 v1, 0x2000, v1
	v_lshl_add_u32 v194, v2, 10, v4
	v_ashrrev_i32_e32 v2, 31, v1
	v_lshrrev_b32_e32 v2, 22, v2
	v_add_u32_e32 v2, v1, v2
	v_ashrrev_i32_e32 v13, 10, v2
	v_mul_i32_i24_e32 v2, 0x400, v13
	v_sub_u32_e32 v1, v1, v2
	v_lshrrev_b32_e32 v2, 4, v1
	v_bitop3_b32 v1, v2, v1, 32 bitop3:0x6c
	v_lshl_add_u32 v130, v3, 10, v4
	v_ashrrev_i32_e32 v3, 31, v1
	v_lshrrev_b32_e32 v3, 26, v3
	v_add_u32_e32 v3, v1, v3
	s_add_u32 s31, s6, 0x1a800000
	v_lshlrev_b32_e32 v2, 3, v13
	v_ashrrev_i32_e32 v15, 6, v3
	v_and_b32_e32 v3, 0xc0, v3
	s_addc_u32 s34, s7, 0
	v_and_b32_e32 v2, -16, v2
	v_sub_u32_e32 v1, v1, v3
	s_add_u32 s35, s6, 0xe700000
	v_add_u32_e32 v2, v15, v2
	v_ashrrev_i16_sdwa v1, v226, sext(v1) dst_sel:DWORD dst_unused:UNUSED_PAD src0_sel:DWORD src1_sel:BYTE_0
	v_and_b32_e32 v5, 3, v15
	s_addc_u32 s38, s7, 0
	v_lshlrev_b32_e32 v4, 5, v13
	v_bfe_i32 v16, v1, 0, 16
	v_lshlrev_b32_e32 v1, 1, v2
	v_lshrrev_b32_e32 v3, 2, v2
	v_and_or_b32 v5, v2, s0, v5
	s_and_b32 s0, s1, -4
	v_and_b32_e32 v4, 32, v4
	v_and_b32_e32 v1, 24, v1
	v_and_b32_e32 v3, 4, v3
	s_add_i32 s0, s0, 0
	v_or3_b32 v1, v5, v3, v1
	v_add_lshl_u32 v3, v4, v16, 1
	s_add_i32 s0, s0, 0x26200
	v_lshl_add_u32 v134, v1, 10, v3
	v_mov_b32_e32 v1, s0
	ds_read_b32 v1, v1
	s_ashr_i32 s8, s1, 2
	s_ashr_i32 s0, s29, 6
	s_ashr_i32 s9, s8, 31
	s_ashr_i32 s10, s29, 8
	s_waitcnt lgkmcnt(0)
	v_readfirstlane_b32 s14, v1
	s_ashr_i32 s15, s14, 31
	s_lshl_b32 s40, s0, 10
	s_and_b32 s68, s1, 3
	s_lshl_b64 s[14:15], s[14:15], 20
	s_lshl_b64 s[16:17], s[8:9], 18
	s_add_u32 s1, s35, s14
	s_addc_u32 s9, s38, s15
	s_lshl_b32 s11, s68, 18
	s_add_u32 s24, s1, s11
	s_addc_u32 s25, s9, 0
	s_add_i32 s9, s40, 0
	s_add_i32 m0, s9, 0x10000
	v_lshl_add_u32 v132, v2, 10, v3
	global_load_lds_dwordx4 v194, s[24:25]
	s_add_i32 m0, s9, 0x12000
	s_add_u32 s22, s31, s16
	global_load_lds_dwordx4 v134, s[24:25]
	s_addc_u32 s23, s34, s17
	s_mov_b32 m0, s9
	s_add_i32 s43, s9, 0x2000
	global_load_lds_dwordx4 v130, s[22:23]
	s_mov_b32 m0, s43
	s_add_u32 s14, s24, 0x20000
	global_load_lds_dwordx4 v132, s[22:23]
	s_addc_u32 s15, s25, 0
	s_add_i32 m0, s9, 0x14000
	v_mov_b32_e32 v135, v195
	global_load_lds_dwordx4 v194, s[14:15]
	s_add_i32 m0, s9, 0x16000
	v_mov_b32_e32 v131, v195
	global_load_lds_dwordx4 v134, s[14:15]
	s_add_u32 s14, s22, 0x20000
	s_addc_u32 s15, s23, 0
	s_add_i32 s64, s9, 0x4000
	s_mov_b32 m0, s64
	s_add_i32 s65, s9, 0x6000
	global_load_lds_dwordx4 v130, s[14:15]
	s_mov_b32 m0, s65
	v_mov_b32_e32 v133, v195
	global_load_lds_dwordx4 v132, s[14:15]
	s_waitcnt vmcnt(0)
	v_lshl_add_u64 v[8:9], s[24:25], 0, v[194:195]
	v_lshl_add_u64 v[6:7], s[24:25], 0, v[134:135]
	v_lshl_add_u64 v[4:5], s[22:23], 0, v[130:131]
	s_cmp_lg_u32 s10, 1
	v_lshl_add_u64 v[2:3], s[22:23], 0, v[132:133]
	s_setprio 1
	s_cbranch_scc1 .LBB0_2554
	s_barrier
	s_setprio 0

.LBB0_2563:
	s_add_u32 s0, s22, 0xfffe0080
	s_addc_u32 s1, s23, -1
	s_add_i32 s33, 0, 0x10000
	v_add_u32_e32 v143, s33, v140
	ds_read_b128 v[144:147], v143
	ds_read_b128 v[148:151], v143 offset:1024
	ds_read_b128 v[152:155], v143 offset:2048
	ds_read_b128 v[156:159], v143 offset:3072
	s_cmp_eq_u32 s77, 4
	s_cselect_b32 s27, s11, s1
	s_cselect_b32 s26, s74, s0
	s_cselect_b32 s25, s13, s76
	s_cselect_b32 s24, s15, s75
	v_lshl_add_u64 v[192:193], s[22:23], 0, v[136:137]
	s_add_i32 m0, s9, 0xc000
	ds_read_b128 v[160:163], v142
	ds_read_b128 v[164:167], v142 offset:1024
	ds_read_b128 v[168:171], v142 offset:2048
	ds_read_b128 v[172:175], v142 offset:3072
	ds_read_b128 v[176:179], v142 offset:4096
	ds_read_b128 v[180:183], v142 offset:5120
	ds_read_b128 v[184:187], v142 offset:6144
	ds_read_b128 v[188:191], v142 offset:7168
	global_load_lds_dwordx4 v[192:193], off
	v_lshl_add_u64 v[192:193], s[22:23], 0, v[138:139]
	s_add_i32 m0, s9, 0xe000
	s_nop 0
	global_load_lds_dwordx4 v[192:193], off
	s_waitcnt lgkmcnt(8)
	s_barrier
	s_waitcnt lgkmcnt(0)
	s_waitcnt lgkmcnt(0)
	v_mfma_f32_16x16x32_bf16 v[126:129], v[144:147], v[160:163], v[126:129]
	v_mfma_f32_16x16x32_bf16 v[122:125], v[152:155], v[160:163], v[122:125]
	v_mfma_f32_16x16x32_bf16 v[118:121], v[144:147], v[168:171], v[118:121]
	v_mfma_f32_16x16x32_bf16 v[114:117], v[152:155], v[168:171], v[114:117]
	v_mfma_f32_16x16x32_bf16 v[102:105], v[144:147], v[176:179], v[102:105]
	v_mfma_f32_16x16x32_bf16 v[98:101], v[152:155], v[176:179], v[98:101]
	v_mfma_f32_16x16x32_bf16 v[86:89], v[144:147], v[184:187], v[86:89]
	v_mfma_f32_16x16x32_bf16 v[82:85], v[152:155], v[184:187], v[82:85]
	v_mfma_f32_16x16x32_bf16 v[126:129], v[148:151], v[164:167], v[126:129]
	v_mfma_f32_16x16x32_bf16 v[122:125], v[156:159], v[164:167], v[122:125]
	v_mfma_f32_16x16x32_bf16 v[118:121], v[148:151], v[172:175], v[118:121]
	v_mfma_f32_16x16x32_bf16 v[114:117], v[156:159], v[172:175], v[114:117]
	v_mfma_f32_16x16x32_bf16 v[102:105], v[148:151], v[180:183], v[102:105]
	v_mfma_f32_16x16x32_bf16 v[98:101], v[156:159], v[180:183], v[98:101]
	v_mfma_f32_16x16x32_bf16 v[86:89], v[148:151], v[188:191], v[86:89]
	v_mfma_f32_16x16x32_bf16 v[82:85], v[156:159], v[188:191], v[82:85]
	s_barrier
	s_add_i32 s36, 0, 0x14000
	s_add_i32 s0, s33, s40
	v_add_u32_e32 v143, s36, v140
	v_lshl_add_u64 v[192:193], s[24:25], 0, v[194:195]
	s_mov_b32 m0, s0
	ds_read_b128 v[198:201], v143
	ds_read_b128 v[202:205], v143 offset:1024
	ds_read_b128 v[206:209], v143 offset:2048
	ds_read_b128 v[210:213], v143 offset:3072
	global_load_lds_dwordx4 v[192:193], off
	v_lshl_add_u64 v[214:215], s[24:25], 0, v[134:135]
	s_add_i32 m0, s0, 0x2000
	s_nop 0
	global_load_lds_dwordx4 v[214:215], off
	s_barrier
	s_waitcnt lgkmcnt(0)
	s_waitcnt lgkmcnt(0)
	v_mfma_f32_16x16x32_bf16 v[110:113], v[198:201], v[160:163], v[110:113]
	v_mfma_f32_16x16x32_bf16 v[106:109], v[206:209], v[160:163], v[106:109]
	v_mfma_f32_16x16x32_bf16 v[94:97], v[198:201], v[168:171], v[94:97]
	v_mfma_f32_16x16x32_bf16 v[90:93], v[206:209], v[168:171], v[90:93]
	v_mfma_f32_16x16x32_bf16 v[78:81], v[198:201], v[176:179], v[78:81]
	v_mfma_f32_16x16x32_bf16 v[74:77], v[206:209], v[176:179], v[74:77]
	v_mfma_f32_16x16x32_bf16 v[70:73], v[198:201], v[184:187], v[70:73]
	v_mfma_f32_16x16x32_bf16 v[66:69], v[206:209], v[184:187], v[66:69]
	v_mfma_f32_16x16x32_bf16 v[110:113], v[202:205], v[164:167], v[110:113]
	v_mfma_f32_16x16x32_bf16 v[106:109], v[210:213], v[164:167], v[106:109]
	v_mfma_f32_16x16x32_bf16 v[94:97], v[202:205], v[172:175], v[94:97]
	v_mfma_f32_16x16x32_bf16 v[90:93], v[210:213], v[172:175], v[90:93]
	v_mfma_f32_16x16x32_bf16 v[78:81], v[202:205], v[180:183], v[78:81]
	v_mfma_f32_16x16x32_bf16 v[74:77], v[210:213], v[180:183], v[74:77]
	v_mfma_f32_16x16x32_bf16 v[70:73], v[202:205], v[188:191], v[70:73]
	v_mfma_f32_16x16x32_bf16 v[66:69], v[210:213], v[188:191], v[66:69]
	s_mov_b32 m0, s9
	v_lshl_add_u64 v[216:217], s[26:27], 0, v[130:131]
	s_barrier
	ds_read_b128 v[160:163], v142 offset:16384
	ds_read_b128 v[164:167], v142 offset:17408
	ds_read_b128 v[168:171], v142 offset:18432
	ds_read_b128 v[172:175], v142 offset:19456
	ds_read_b128 v[176:179], v142 offset:20480
	ds_read_b128 v[180:183], v142 offset:21504
	ds_read_b128 v[184:187], v142 offset:22528
	ds_read_b128 v[188:191], v142 offset:23552
	global_load_lds_dwordx4 v[216:217], off
	v_lshl_add_u64 v[218:219], s[26:27], 0, v[132:133]
	s_mov_b32 m0, s43
	s_nop 0
	global_load_lds_dwordx4 v[218:219], off
	s_barrier
	s_waitcnt lgkmcnt(0)
	s_waitcnt lgkmcnt(0)
	v_mfma_f32_16x16x32_bf16 v[62:65], v[144:147], v[160:163], v[62:65]
	v_mfma_f32_16x16x32_bf16 v[58:61], v[152:155], v[160:163], v[58:61]
	v_mfma_f32_16x16x32_bf16 v[54:57], v[144:147], v[168:171], v[54:57]
	v_mfma_f32_16x16x32_bf16 v[50:53], v[152:155], v[168:171], v[50:53]
	v_mfma_f32_16x16x32_bf16 v[38:41], v[144:147], v[176:179], v[38:41]
	v_mfma_f32_16x16x32_bf16 v[34:37], v[152:155], v[176:179], v[34:37]
	v_mfma_f32_16x16x32_bf16 v[22:25], v[144:147], v[184:187], v[22:25]
	v_mfma_f32_16x16x32_bf16 v[18:21], v[152:155], v[184:187], v[18:21]
	v_mfma_f32_16x16x32_bf16 v[62:65], v[148:151], v[164:167], v[62:65]
	v_mfma_f32_16x16x32_bf16 v[58:61], v[156:159], v[164:167], v[58:61]
	v_mfma_f32_16x16x32_bf16 v[54:57], v[148:151], v[172:175], v[54:57]
	v_mfma_f32_16x16x32_bf16 v[50:53], v[156:159], v[172:175], v[50:53]
	v_mfma_f32_16x16x32_bf16 v[38:41], v[148:151], v[180:183], v[38:41]
	v_mfma_f32_16x16x32_bf16 v[34:37], v[156:159], v[180:183], v[34:37]
	v_mfma_f32_16x16x32_bf16 v[22:25], v[148:151], v[188:191], v[22:25]
	v_mfma_f32_16x16x32_bf16 v[18:21], v[156:159], v[188:191], v[18:21]
	s_barrier
	s_add_u32 s0, s24, 0x20000
	s_addc_u32 s1, s25, 0
	s_add_i32 s33, s36, s40
	v_lshl_add_u64 v[144:145], s[0:1], 0, v[194:195]
	s_mov_b32 m0, s33
	s_nop 0
	global_load_lds_dwordx4 v[144:145], off
	v_lshl_add_u64 v[144:145], s[0:1], 0, v[134:135]
	s_add_i32 m0, s33, 0x2000
	s_nop 0
	global_load_lds_dwordx4 v[144:145], off
	s_waitcnt vmcnt(6)
	s_barrier
	v_mfma_f32_16x16x32_bf16 v[46:49], v[198:201], v[160:163], v[46:49]
	v_mfma_f32_16x16x32_bf16 v[42:45], v[206:209], v[160:163], v[42:45]
	v_mfma_f32_16x16x32_bf16 v[30:33], v[198:201], v[168:171], v[30:33]
	v_mfma_f32_16x16x32_bf16 v[26:29], v[206:209], v[168:171], v[26:29]
	v_mfma_f32_16x16x32_bf16 v[14:17], v[198:201], v[176:179], v[14:17]
	v_mfma_f32_16x16x32_bf16 v[10:13], v[206:209], v[176:179], v[10:13]
	v_mfma_f32_16x16x32_bf16 v[6:9], v[198:201], v[184:187], v[6:9]
	v_mfma_f32_16x16x32_bf16 v[2:5], v[206:209], v[184:187], v[2:5]
	v_mfma_f32_16x16x32_bf16 v[46:49], v[202:205], v[164:167], v[46:49]
	v_mfma_f32_16x16x32_bf16 v[42:45], v[210:213], v[164:167], v[42:45]
	v_mfma_f32_16x16x32_bf16 v[30:33], v[202:205], v[172:175], v[30:33]
	v_mfma_f32_16x16x32_bf16 v[26:29], v[210:213], v[172:175], v[26:29]
	v_mfma_f32_16x16x32_bf16 v[14:17], v[202:205], v[180:183], v[14:17]
	v_mfma_f32_16x16x32_bf16 v[10:13], v[210:213], v[180:183], v[10:13]
	v_mfma_f32_16x16x32_bf16 v[6:9], v[202:205], v[188:191], v[6:9]
	v_mfma_f32_16x16x32_bf16 v[2:5], v[210:213], v[188:191], v[2:5]
	s_add_i32 s33, 0, 0x18000
	v_add_u32_e32 v143, s33, v140
	s_barrier
	ds_read_b128 v[144:147], v143
	ds_read_b128 v[148:151], v143 offset:1024
	ds_read_b128 v[152:155], v143 offset:2048
	ds_read_b128 v[156:159], v143 offset:3072
	s_add_u32 s0, s26, 0x20000
	s_addc_u32 s1, s27, 0
	s_mov_b32 m0, s64
	v_lshl_add_u64 v[198:199], s[0:1], 0, v[130:131]
	ds_read_b128 v[160:163], v142 offset:32768
	ds_read_b128 v[164:167], v142 offset:33792
	ds_read_b128 v[168:171], v142 offset:34816
	ds_read_b128 v[172:175], v142 offset:35840
	ds_read_b128 v[176:179], v142 offset:36864
	ds_read_b128 v[180:183], v142 offset:37888
	ds_read_b128 v[184:187], v142 offset:38912
	ds_read_b128 v[188:191], v142 offset:39936
	global_load_lds_dwordx4 v[198:199], off
	v_lshl_add_u64 v[198:199], s[0:1], 0, v[132:133]
	s_mov_b32 m0, s65
	s_nop 0
	global_load_lds_dwordx4 v[198:199], off
	s_waitcnt lgkmcnt(8)
	s_barrier
	s_waitcnt lgkmcnt(0)
	s_waitcnt lgkmcnt(0)
	v_mfma_f32_16x16x32_bf16 v[126:129], v[144:147], v[160:163], v[126:129]
	v_mfma_f32_16x16x32_bf16 v[122:125], v[152:155], v[160:163], v[122:125]
	v_mfma_f32_16x16x32_bf16 v[118:121], v[144:147], v[168:171], v[118:121]
	v_mfma_f32_16x16x32_bf16 v[114:117], v[152:155], v[168:171], v[114:117]
	v_mfma_f32_16x16x32_bf16 v[102:105], v[144:147], v[176:179], v[102:105]
	v_mfma_f32_16x16x32_bf16 v[98:101], v[152:155], v[176:179], v[98:101]
	v_mfma_f32_16x16x32_bf16 v[86:89], v[144:147], v[184:187], v[86:89]
	v_mfma_f32_16x16x32_bf16 v[82:85], v[152:155], v[184:187], v[82:85]
	v_mfma_f32_16x16x32_bf16 v[126:129], v[148:151], v[164:167], v[126:129]
	v_mfma_f32_16x16x32_bf16 v[122:125], v[156:159], v[164:167], v[122:125]
	v_mfma_f32_16x16x32_bf16 v[118:121], v[148:151], v[172:175], v[118:121]
	v_mfma_f32_16x16x32_bf16 v[114:117], v[156:159], v[172:175], v[114:117]
	v_mfma_f32_16x16x32_bf16 v[102:105], v[148:151], v[180:183], v[102:105]
	v_mfma_f32_16x16x32_bf16 v[98:101], v[156:159], v[180:183], v[98:101]
	v_mfma_f32_16x16x32_bf16 v[86:89], v[148:151], v[188:191], v[86:89]
	v_mfma_f32_16x16x32_bf16 v[82:85], v[156:159], v[188:191], v[82:85]
	s_barrier
	s_add_i32 s26, 0, 0x1c000
	s_add_i32 s0, s33, s40
	v_add_u32_e32 v143, s26, v140
	v_lshl_add_u64 v[192:193], v[192:193], 0, s[54:55]
	s_mov_b32 m0, s0
	ds_read_b128 v[198:201], v143
	ds_read_b128 v[202:205], v143 offset:1024
	ds_read_b128 v[206:209], v143 offset:2048
	ds_read_b128 v[210:213], v143 offset:3072
	global_load_lds_dwordx4 v[192:193], off
	v_lshl_add_u64 v[192:193], v[214:215], 0, s[54:55]
	s_add_i32 m0, s0, 0x2000
	s_nop 0
	global_load_lds_dwordx4 v[192:193], off
	s_barrier
	s_waitcnt lgkmcnt(0)
	s_waitcnt lgkmcnt(0)
	v_mfma_f32_16x16x32_bf16 v[110:113], v[198:201], v[160:163], v[110:113]
	v_mfma_f32_16x16x32_bf16 v[106:109], v[206:209], v[160:163], v[106:109]
	v_mfma_f32_16x16x32_bf16 v[94:97], v[198:201], v[168:171], v[94:97]
	v_mfma_f32_16x16x32_bf16 v[90:93], v[206:209], v[168:171], v[90:93]
	v_mfma_f32_16x16x32_bf16 v[78:81], v[198:201], v[176:179], v[78:81]
	v_mfma_f32_16x16x32_bf16 v[74:77], v[206:209], v[176:179], v[74:77]
	v_mfma_f32_16x16x32_bf16 v[70:73], v[198:201], v[184:187], v[70:73]
	v_mfma_f32_16x16x32_bf16 v[66:69], v[206:209], v[184:187], v[66:69]
	v_mfma_f32_16x16x32_bf16 v[110:113], v[202:205], v[164:167], v[110:113]
	v_mfma_f32_16x16x32_bf16 v[106:109], v[210:213], v[164:167], v[106:109]
	v_mfma_f32_16x16x32_bf16 v[94:97], v[202:205], v[172:175], v[94:97]
	v_mfma_f32_16x16x32_bf16 v[90:93], v[210:213], v[172:175], v[90:93]
	v_mfma_f32_16x16x32_bf16 v[78:81], v[202:205], v[180:183], v[78:81]
	v_mfma_f32_16x16x32_bf16 v[74:77], v[210:213], v[180:183], v[74:77]
	v_mfma_f32_16x16x32_bf16 v[70:73], v[202:205], v[188:191], v[70:73]
	v_mfma_f32_16x16x32_bf16 v[66:69], v[210:213], v[188:191], v[66:69]
	s_mov_b32 m0, s66
	v_lshl_add_u64 v[192:193], v[216:217], 0, s[54:55]
	s_barrier
	ds_read_b128 v[160:163], v142 offset:49152
	ds_read_b128 v[164:167], v142 offset:50176
	ds_read_b128 v[168:171], v142 offset:51200
	ds_read_b128 v[172:175], v142 offset:52224
	ds_read_b128 v[176:179], v142 offset:53248
	ds_read_b128 v[180:183], v142 offset:54272
	ds_read_b128 v[184:187], v142 offset:55296
	ds_read_b128 v[188:191], v142 offset:56320
	global_load_lds_dwordx4 v[192:193], off
	v_lshl_add_u64 v[192:193], v[218:219], 0, s[54:55]
	s_mov_b32 m0, s67
	s_nop 0
	global_load_lds_dwordx4 v[192:193], off
	s_barrier
	s_waitcnt lgkmcnt(0)
	s_waitcnt lgkmcnt(0)
	v_mfma_f32_16x16x32_bf16 v[62:65], v[144:147], v[160:163], v[62:65]
	v_mfma_f32_16x16x32_bf16 v[58:61], v[152:155], v[160:163], v[58:61]
	v_mfma_f32_16x16x32_bf16 v[54:57], v[144:147], v[168:171], v[54:57]
	v_mfma_f32_16x16x32_bf16 v[50:53], v[152:155], v[168:171], v[50:53]
	v_mfma_f32_16x16x32_bf16 v[38:41], v[144:147], v[176:179], v[38:41]
	v_mfma_f32_16x16x32_bf16 v[34:37], v[152:155], v[176:179], v[34:37]
	v_mfma_f32_16x16x32_bf16 v[22:25], v[144:147], v[184:187], v[22:25]
	v_mfma_f32_16x16x32_bf16 v[18:21], v[152:155], v[184:187], v[18:21]
	v_mfma_f32_16x16x32_bf16 v[62:65], v[148:151], v[164:167], v[62:65]
	v_mfma_f32_16x16x32_bf16 v[58:61], v[156:159], v[164:167], v[58:61]
	v_mfma_f32_16x16x32_bf16 v[54:57], v[148:151], v[172:175], v[54:57]
	v_mfma_f32_16x16x32_bf16 v[50:53], v[156:159], v[172:175], v[50:53]
	v_mfma_f32_16x16x32_bf16 v[38:41], v[148:151], v[180:183], v[38:41]
	v_mfma_f32_16x16x32_bf16 v[34:37], v[156:159], v[180:183], v[34:37]
	v_mfma_f32_16x16x32_bf16 v[22:25], v[148:151], v[188:191], v[22:25]
	v_mfma_f32_16x16x32_bf16 v[18:21], v[156:159], v[188:191], v[18:21]
	s_barrier
	s_add_u32 s0, s24, 0x20080
	s_addc_u32 s1, s25, 0
	s_add_i32 s24, s26, s40
	v_lshl_add_u64 v[144:145], s[0:1], 0, v[194:195]
	s_mov_b32 m0, s24
	s_nop 0
	global_load_lds_dwordx4 v[144:145], off
	v_lshl_add_u64 v[144:145], s[0:1], 0, v[134:135]
	s_add_i32 m0, s24, 0x2000
	s_nop 0
	global_load_lds_dwordx4 v[144:145], off
	s_waitcnt vmcnt(6)
	s_barrier
	v_mfma_f32_16x16x32_bf16 v[46:49], v[198:201], v[160:163], v[46:49]
	v_mfma_f32_16x16x32_bf16 v[42:45], v[206:209], v[160:163], v[42:45]
	v_mfma_f32_16x16x32_bf16 v[30:33], v[198:201], v[168:171], v[30:33]
	v_mfma_f32_16x16x32_bf16 v[26:29], v[206:209], v[168:171], v[26:29]
	v_mfma_f32_16x16x32_bf16 v[14:17], v[198:201], v[176:179], v[14:17]
	v_mfma_f32_16x16x32_bf16 v[10:13], v[206:209], v[176:179], v[10:13]
	v_mfma_f32_16x16x32_bf16 v[6:9], v[198:201], v[184:187], v[6:9]
	v_mfma_f32_16x16x32_bf16 v[2:5], v[206:209], v[184:187], v[2:5]
	v_mfma_f32_16x16x32_bf16 v[46:49], v[202:205], v[164:167], v[46:49]
	v_mfma_f32_16x16x32_bf16 v[42:45], v[210:213], v[164:167], v[42:45]
	v_mfma_f32_16x16x32_bf16 v[30:33], v[202:205], v[172:175], v[30:33]
	v_mfma_f32_16x16x32_bf16 v[26:29], v[210:213], v[172:175], v[26:29]
	v_mfma_f32_16x16x32_bf16 v[14:17], v[202:205], v[180:183], v[14:17]
	v_mfma_f32_16x16x32_bf16 v[10:13], v[210:213], v[180:183], v[10:13]
	v_mfma_f32_16x16x32_bf16 v[6:9], v[202:205], v[188:191], v[6:9]
	v_mfma_f32_16x16x32_bf16 v[2:5], v[210:213], v[188:191], v[2:5]
	s_add_i32 s77, s77, 2
	s_add_u32 s22, s22, 0x100
	s_addc_u32 s23, s23, 0
	s_add_u32 s75, s75, 0x100
	s_addc_u32 s76, s76, 0
	s_cmp_gt_u32 s77, 5
	s_barrier
	s_cbranch_scc0 .LBB0_2563
	v_lshl_add_u32 v144, s8, 8, v1
	v_lshl_or_b32 v146, s68, 8, v141
	v_ashrrev_i32_e32 v145, 31, v144
	v_lshlrev_b64 v[148:149], 11, v[144:145]
	v_ashrrev_i32_e32 v147, 31, v146
	v_lshl_add_u64 v[148:149], s[6:7], 0, v[148:149]
	v_cvt_pk_bf16_f32 v126, v126, v127
	v_cvt_pk_bf16_f32 v127, v128, v129
	v_cvt_pk_bf16_f32 v128, v122, v123
	v_lshlrev_b64 v[122:123], 1, v[146:147]
	v_cvt_pk_bf16_f32 v129, v124, v125
	v_lshl_add_u64 v[124:125], v[148:149], 0, v[122:123]
	s_mov_b64 s[0:1], 0x40000
	v_cvt_pk_bf16_f32 v62, v62, v63
	v_cvt_pk_bf16_f32 v63, v64, v65
	v_cvt_pk_bf16_f32 v64, v58, v59
	v_lshl_add_u64 v[58:59], v[124:125], 0, s[0:1]
	s_mov_b32 s0, 0x40000
	v_cvt_pk_bf16_f32 v110, v110, v111
	v_cvt_pk_bf16_f32 v111, v112, v113
	v_cvt_pk_bf16_f32 v112, v106, v107
	v_or_b32_e32 v106, 16, v144
	v_cvt_pk_bf16_f32 v65, v60, v61
	v_add_co_u32_e32 v60, vcc, s0, v124
	v_cvt_pk_bf16_f32 v46, v46, v47
	v_cvt_pk_bf16_f32 v47, v48, v49
	v_cvt_pk_bf16_f32 v48, v42, v43
	v_cvt_pk_bf16_f32 v49, v44, v45
	s_mov_b64 s[0:1], 0x48000
	v_ashrrev_i32_e32 v107, 31, v106
	v_addc_co_u32_e32 v61, vcc, 0, v125, vcc
	global_store_dwordx4 v[58:59], v[46:49], off offset:256
	v_cvt_pk_bf16_f32 v113, v108, v109
	v_lshlrev_b64 v[106:107], 11, v[106:107]
	v_lshl_add_u64 v[46:47], v[124:125], 0, s[0:1]
	s_mov_b32 s0, 0x48000
	v_cvt_pk_bf16_f32 v94, v94, v95
	v_cvt_pk_bf16_f32 v95, v96, v97
	v_cvt_pk_bf16_f32 v96, v90, v91
	v_or_b32_e32 v90, 32, v144
	v_add_co_u32_e32 v48, vcc, s0, v124
	v_cvt_pk_bf16_f32 v30, v30, v31
	v_cvt_pk_bf16_f32 v31, v32, v33
	v_cvt_pk_bf16_f32 v32, v26, v27
	v_cvt_pk_bf16_f32 v33, v28, v29
	s_mov_b64 s[0:1], 0x50000
	global_store_dwordx4 v[124:125], v[110:113], off offset:256
	v_ashrrev_i32_e32 v91, 31, v90
	v_addc_co_u32_e32 v49, vcc, 0, v125, vcc
	v_lshl_add_u64 v[110:111], s[6:7], 0, v[106:107]
	global_store_dwordx4 v[46:47], v[30:33], off offset:256
	v_lshl_add_u64 v[110:111], v[110:111], 0, v[122:123]
	v_cvt_pk_bf16_f32 v97, v92, v93
	v_lshl_add_u64 v[30:31], v[124:125], 0, s[0:1]
	s_mov_b32 s0, 0x50000
	v_lshlrev_b64 v[90:91], 11, v[90:91]
	v_cvt_pk_bf16_f32 v78, v78, v79
	v_cvt_pk_bf16_f32 v79, v80, v81
	v_cvt_pk_bf16_f32 v80, v74, v75
	v_or_b32_e32 v74, 48, v144
	v_add_co_u32_e32 v32, vcc, s0, v124
	v_cvt_pk_bf16_f32 v14, v14, v15
	v_cvt_pk_bf16_f32 v15, v16, v17
	v_cvt_pk_bf16_f32 v16, v10, v11
	v_cvt_pk_bf16_f32 v17, v12, v13
	s_mov_b64 s[0:1], 0x58000
	global_store_dwordx4 v[110:111], v[94:97], off offset:256
	v_ashrrev_i32_e32 v75, 31, v74
	v_addc_co_u32_e32 v33, vcc, 0, v125, vcc
	v_lshl_add_u64 v[94:95], s[6:7], 0, v[90:91]
	global_store_dwordx4 v[30:31], v[14:17], off offset:256
	v_lshl_add_u64 v[94:95], v[94:95], 0, v[122:123]
	v_cvt_pk_bf16_f32 v81, v76, v77
	v_lshl_add_u64 v[14:15], v[124:125], 0, s[0:1]
	s_mov_b32 s0, 0x58000
	v_lshlrev_b64 v[74:75], 11, v[74:75]
	v_add_co_u32_e32 v16, vcc, s0, v124
	global_store_dwordx4 v[94:95], v[78:81], off offset:256
	s_nop 0
	v_addc_co_u32_e32 v17, vcc, 0, v125, vcc
	v_lshl_add_u64 v[78:79], s[6:7], 0, v[74:75]
	v_cvt_pk_bf16_f32 v106, v118, v119
	v_cvt_pk_bf16_f32 v107, v120, v121
	v_cvt_pk_bf16_f32 v108, v114, v115
	v_cvt_pk_bf16_f32 v109, v116, v117
	v_cvt_pk_bf16_f32 v90, v102, v103
	v_cvt_pk_bf16_f32 v91, v104, v105
	v_cvt_pk_bf16_f32 v92, v98, v99
	v_cvt_pk_bf16_f32 v93, v100, v101
	v_cvt_pk_bf16_f32 v74, v86, v87
	v_cvt_pk_bf16_f32 v75, v88, v89
	v_cvt_pk_bf16_f32 v76, v82, v83
	v_cvt_pk_bf16_f32 v77, v84, v85
	v_lshl_add_u64 v[78:79], v[78:79], 0, v[122:123]
	v_cvt_pk_bf16_f32 v70, v70, v71
	v_cvt_pk_bf16_f32 v71, v72, v73
	v_cvt_pk_bf16_f32 v72, v66, v67
	v_cvt_pk_bf16_f32 v73, v68, v69
	v_cvt_pk_bf16_f32 v42, v54, v55
	v_cvt_pk_bf16_f32 v43, v56, v57
	v_cvt_pk_bf16_f32 v44, v50, v51
	v_cvt_pk_bf16_f32 v45, v52, v53
	v_cvt_pk_bf16_f32 v26, v38, v39
	v_cvt_pk_bf16_f32 v27, v40, v41
	v_cvt_pk_bf16_f32 v28, v34, v35
	v_cvt_pk_bf16_f32 v29, v36, v37
	v_cvt_pk_bf16_f32 v10, v22, v23
	v_cvt_pk_bf16_f32 v11, v24, v25
	v_cvt_pk_bf16_f32 v12, v18, v19
	v_cvt_pk_bf16_f32 v13, v20, v21
	v_cvt_pk_bf16_f32 v6, v6, v7
	v_cvt_pk_bf16_f32 v7, v8, v9
	v_cvt_pk_bf16_f32 v8, v2, v3
	v_cvt_pk_bf16_f32 v9, v4, v5
	s_and_b64 vcc, exec, s[18:19]
	s_mov_b32 s68, s14
	s_mov_b32 s8, s10
	s_mov_b64 s[24:25], s[20:21]
	s_mov_b64 s[22:23], s[16:17]
	global_store_dwordx4 v[124:125], v[126:129], off
	global_store_dwordx4 v[110:111], v[106:109], off
	global_store_dwordx4 v[94:95], v[90:93], off
	global_store_dwordx4 v[78:79], v[74:77], off
	global_store_dwordx4 v[78:79], v[70:73], off offset:256
	global_store_dwordx4 v[60:61], v[62:65], off
	global_store_dwordx4 v[48:49], v[42:45], off
	global_store_dwordx4 v[32:33], v[26:29], off
	global_store_dwordx4 v[16:17], v[10:13], off
	global_store_dwordx4 v[14:15], v[6:9], off offset:256
	s_cbranch_vccz .LBB0_2555
	s_waitcnt vmcnt(0)
	s_cmpk_gt_u32 s29, 0xff
	s_cbranch_scc1 .LBB0_2567
	s_barrier

.LBB0_2573:
	v_readlane_b32 s6, v254, 2
	v_mov_b32_e32 v1, v0
	v_readlane_b32 s7, v254, 3
	s_load_dword s0, s[6:7], 0x118
	v_readlane_b32 s1, v254, 0
	s_waitcnt lgkmcnt(0)
	s_setprio 0
	s_getreg_b32 s0, hwreg(HW_REG_XCC_ID, 0, 4)
	s_waitcnt vmcnt(0)
	s_barrier
	s_mov_b64 s[4:5], exec
	v_readlane_b32 s2, v254, 6
	v_readlane_b32 s3, v254, 7
	s_and_b64 s[2:3], s[4:5], s[2:3]
	s_mov_b64 exec, s[2:3]
	s_cbranch_execnz .LBB0_2574
	s_getpc_b64 s[98:99]

.LBB0_2919:
	v_readlane_b32 s6, v254, 2
	v_mov_b32_e32 v1, v0
	v_readlane_b32 s7, v254, 3
	s_load_dword s0, s[6:7], 0x118
	v_readlane_b32 s1, v254, 0
	s_waitcnt lgkmcnt(0)
	s_setprio 0
	s_getreg_b32 s0, hwreg(HW_REG_XCC_ID, 0, 4)
	s_waitcnt vmcnt(0)
	v_cmp_eq_u32_e32 vcc, 0, v0
	s_barrier
	s_and_saveexec_b64 s[4:5], vcc
	s_cbranch_execz .LBB0_3001
	s_add_i32 s1, 0, 0x26000
	v_mov_b32_e32 v1, s1
	s_load_dwordx2 s[6:7], s[6:7], 0x108
	s_waitcnt vmcnt(0) expcnt(0) lgkmcnt(0)
	ds_read_b32 v3, v1
	s_add_i32 s1, 0, 0x26004
	v_mov_b32_e32 v1, s1
	ds_read_b32 v1, v1
	s_and_b32 s2, s0, 15
	s_waitcnt lgkmcnt(1)
	v_cmp_ne_u32_e32 vcc, 0, v3
	s_cbranch_vccnz .LBB0_2965
	v_readlane_b32 s8, v254, 4
	v_readlane_b32 s12, v254, 2
	v_readlane_b32 s9, v254, 5
	v_readlane_b32 s13, v254, 3
	s_load_dwordx2 s[0:1], s[8:9], 0x4
	s_load_dword s3, s[12:13], 0x118
	s_add_u32 s8, s6, 0x4200
	s_addc_u32 s9, s7, 0
	s_add_u32 s10, s6, 0x4400
	s_addc_u32 s11, s7, 0
	s_add_u32 s12, s6, 0x4500
	s_addc_u32 s13, s7, 0
	s_add_u32 s14, s6, 0x4600
	s_addc_u32 s15, s7, 0
	s_add_u32 s16, s6, 0x4700
	s_addc_u32 s17, s7, 0
	s_add_u32 s18, s6, 0x4800
	s_addc_u32 s19, s7, 0
	s_add_u32 s20, s6, 0x4900
	s_addc_u32 s21, s7, 0
	s_add_u32 s22, s6, 0x4a00
	s_addc_u32 s23, s7, 0
	s_add_u32 s24, s6, 0x4b00
	s_addc_u32 s25, s7, 0
	s_add_u32 s26, s6, 0x4c00
	s_addc_u32 s27, s7, 0
	s_add_u32 s28, s6, 0x4d00
	s_addc_u32 s29, s7, 0
	s_add_u32 s30, s6, 0x4e00
	s_addc_u32 s31, s7, 0
	s_add_u32 s34, s6, 0x4f00
	s_addc_u32 s35, s7, 0
	s_add_u32 s38, s6, 0x5000
	s_addc_u32 s39, s7, 0
	s_add_u32 s40, s6, 0x5100
	s_addc_u32 s41, s7, 0
	s_add_u32 s42, s6, 0x5200
	s_addc_u32 s43, s7, 0
	s_waitcnt lgkmcnt(0)
	s_mul_i32 s3, s0, s3
	s_add_u32 s44, s6, 0x5300
	s_mul_i32 s3, s3, s1
	s_addc_u32 s45, s7, 0
	s_mov_b32 s0, 1
	v_mov_b32_e32 v17, 0
	s_branch .LBB0_2923
